# last-unit next-tile prefetch LDS-DMA pieces run with one lane when a workgroup has no next GEMM unit
# speedup vs baseline: 1.0071x; 1.0071x over previous
.LBB0_306:
	s_add_i32 s58, s58, 1
	v_readlane_b32 s0, v254, 38
	s_mul_i32 s0, s58, s0
	s_mul_hi_u32 s1, s58, s70
	s_add_i32 s1, s1, s0
	s_mul_i32 s0, s58, s70
	v_readlane_b32 s2, v255, 0
	s_add_u32 s2, s0, s2
	s_addc_u32 s3, s1, s48
	v_mov_b64_e32 v[0:1], 0x6e8
	v_cmp_lt_i64_e64 s[0:1], s[2:3], v[0:1]
	v_mov_b64_e32 v[0:1], 0x6e7
	v_cmp_gt_i64_e32 vcc, s[2:3], v[0:1]
	s_nop 3
	s_cmp_lg_u64 s[0:1], 0
	s_cselect_b64 s[100:101], -1, 1
	s_cbranch_vccnz .LBB0_308
	s_ashr_i32 s3, s2, 31
	s_lshr_b32 s3, s3, 29
	s_add_i32 s3, s2, s3
	s_ashr_i32 s16, s3, 3
	s_and_b32 s3, s3, -8
	s_sub_i32 s2, s2, s3
	s_cmp_lt_i32 s2, 0
	s_movk_i32 s3, 0xde
	s_cselect_b32 s3, s3, 0xdd
	s_mul_i32 s2, s2, s3
	s_add_i32 s2, s2, s16
	s_mul_hi_i32 s3, s2, 0x4ec4ec4f
	s_lshr_b32 s16, s3, 31
	s_ashr_i32 s3, s3, 5
	s_add_i32 s3, s3, s16
	s_lshl_b32 s17, s3, 3
	s_sub_i32 s16, 0x88, s17
	s_min_i32 s18, s16, 8
	s_abs_i32 s16, s18
	v_cvt_f32_u32_e32 v0, s16
	s_sub_i32 s21, 0, s16
	s_mulk_i32 s3, 0x68
	s_sub_i32 s2, s2, s3
	v_rcp_iflag_f32_e32 v0, v0
	s_abs_i32 s3, s2
	s_xor_b32 s19, s2, s18
	s_ashr_i32 s19, s19, 31
	v_mul_f32_e32 v0, 0x4f7ffffe, v0
	v_cvt_u32_f32_e32 v0, v0
	s_nop 0
	v_readfirstlane_b32 s26, v0
	s_mul_i32 s21, s21, s26
	s_mul_hi_u32 s21, s26, s21
	s_add_i32 s26, s26, s21
	s_mul_hi_u32 s21, s3, s26
	s_mul_i32 s26, s21, s16
	s_sub_i32 s3, s3, s26
	s_add_i32 s27, s21, 1
	s_sub_i32 s26, s3, s16
	s_cmp_ge_u32 s3, s16
	s_cselect_b32 s21, s27, s21
	s_cselect_b32 s3, s26, s3
	s_add_i32 s26, s21, 1
	s_cmp_ge_u32 s3, s16
	s_cselect_b32 s3, s26, s21
	s_xor_b32 s3, s3, s19
	s_sub_i32 s16, s3, s19
	s_mul_i32 s3, s16, s18
	s_sub_i32 s2, s2, s3
	s_add_i32 s18, s17, s2

.LBB0_309:
	s_add_u32 s33, s22, s2
	s_addc_u32 s61, s23, s3
	v_add_u32_e32 v132, 0x10000, v136
	v_add_u32_e32 v138, 0x14000, v136
	s_add_u32 s34, s33, 0x100
	ds_read_b128 v[140:143], v132
	ds_read_b128 v[144:147], v132 offset:1024
	ds_read_b128 v[148:151], v132 offset:2048
	ds_read_b128 v[152:155], v132 offset:3072
	ds_read_b128 v[156:159], v138
	ds_read_b128 v[160:163], v138 offset:1024
	ds_read_b128 v[164:167], v138 offset:2048
	ds_read_b128 v[168:171], v138 offset:3072
	s_addc_u32 s35, s61, 0
	s_add_u32 s26, s33, 0x180
	s_addc_u32 s27, s61, 0
	s_add_u32 s19, s24, s2
	s_addc_u32 s21, s25, s3
	s_add_u32 s36, s19, 0x100
	s_addc_u32 s37, s21, 0
	ds_read_b128 v[172:175], v137
	ds_read_b128 v[176:179], v137 offset:1024
	ds_read_b128 v[180:183], v137 offset:2048
	ds_read_b128 v[184:187], v137 offset:3072
	ds_read_b128 v[188:191], v137 offset:4096
	ds_read_b128 v[194:197], v137 offset:5120
	ds_read_b128 v[202:205], v137 offset:6144
	ds_read_b128 v[206:209], v137 offset:7168
	s_add_u32 s62, s33, 0x40080
	s_addc_u32 s63, s61, 0
	s_mov_b32 m0, s57
	s_nop 0
	global_load_lds_dwordx4 v65, s[62:63]
	s_nop 0
	s_mov_b32 m0, s59
	s_nop 0
	global_load_lds_dwordx4 v134, s[62:63]
	s_waitcnt vmcnt(8)
	s_waitcnt lgkmcnt(0)
	s_barrier
	s_setprio 1
	s_waitcnt lgkmcnt(0)
	v_mfma_f32_16x16x32_bf16 v[128:131], v[140:143], v[172:175], v[128:131]
	v_mfma_f32_16x16x32_bf16 v[124:127], v[148:151], v[172:175], v[124:127]
	v_mfma_f32_16x16x32_bf16 v[120:123], v[140:143], v[180:183], v[120:123]
	v_mfma_f32_16x16x32_bf16 v[116:119], v[148:151], v[180:183], v[116:119]
	v_mfma_f32_16x16x32_bf16 v[110:113], v[140:143], v[188:191], v[110:113]
	v_mfma_f32_16x16x32_bf16 v[106:109], v[148:151], v[188:191], v[106:109]
	v_mfma_f32_16x16x32_bf16 v[102:105], v[140:143], v[202:205], v[102:105]
	v_mfma_f32_16x16x32_bf16 v[98:101], v[148:151], v[202:205], v[98:101]
	v_mfma_f32_16x16x32_bf16 v[128:131], v[144:147], v[176:179], v[128:131]
	v_mfma_f32_16x16x32_bf16 v[124:127], v[152:155], v[176:179], v[124:127]
	v_mfma_f32_16x16x32_bf16 v[120:123], v[144:147], v[184:187], v[120:123]
	v_mfma_f32_16x16x32_bf16 v[116:119], v[152:155], v[184:187], v[116:119]
	v_mfma_f32_16x16x32_bf16 v[110:113], v[144:147], v[194:197], v[110:113]
	v_mfma_f32_16x16x32_bf16 v[106:109], v[152:155], v[194:197], v[106:109]
	v_mfma_f32_16x16x32_bf16 v[102:105], v[144:147], v[206:209], v[102:105]
	v_mfma_f32_16x16x32_bf16 v[98:101], v[152:155], v[206:209], v[98:101]
	s_setprio 0
	s_setprio 1
	v_mfma_f32_16x16x32_bf16 v[94:97], v[156:159], v[172:175], v[94:97]
	v_mfma_f32_16x16x32_bf16 v[90:93], v[164:167], v[172:175], v[90:93]
	v_mfma_f32_16x16x32_bf16 v[86:89], v[156:159], v[180:183], v[86:89]
	v_mfma_f32_16x16x32_bf16 v[82:85], v[164:167], v[180:183], v[82:85]
	v_mfma_f32_16x16x32_bf16 v[78:81], v[156:159], v[188:191], v[78:81]
	v_mfma_f32_16x16x32_bf16 v[74:77], v[164:167], v[188:191], v[74:77]
	v_mfma_f32_16x16x32_bf16 v[70:73], v[156:159], v[202:205], v[70:73]
	v_mfma_f32_16x16x32_bf16 v[66:69], v[164:167], v[202:205], v[66:69]
	v_mfma_f32_16x16x32_bf16 v[94:97], v[160:163], v[176:179], v[94:97]
	v_mfma_f32_16x16x32_bf16 v[90:93], v[168:171], v[176:179], v[90:93]
	v_mfma_f32_16x16x32_bf16 v[86:89], v[160:163], v[184:187], v[86:89]
	v_mfma_f32_16x16x32_bf16 v[82:85], v[168:171], v[184:187], v[82:85]
	v_mfma_f32_16x16x32_bf16 v[78:81], v[160:163], v[194:197], v[78:81]
	v_mfma_f32_16x16x32_bf16 v[74:77], v[168:171], v[194:197], v[74:77]
	v_mfma_f32_16x16x32_bf16 v[70:73], v[160:163], v[206:209], v[70:73]
	v_mfma_f32_16x16x32_bf16 v[66:69], v[168:171], v[206:209], v[66:69]
	s_setprio 0
	s_barrier
	ds_read_b128 v[172:175], v137 offset:16384
	ds_read_b128 v[176:179], v137 offset:17408
	ds_read_b128 v[180:183], v137 offset:18432
	ds_read_b128 v[184:187], v137 offset:19456
	ds_read_b128 v[188:191], v137 offset:20480
	ds_read_b128 v[194:197], v137 offset:21504
	ds_read_b128 v[202:205], v137 offset:22528
	ds_read_b128 v[206:209], v137 offset:23552
	s_mov_b32 m0, s41
	s_nop 0
	global_load_lds_dwordx4 v114, s[36:37]
	s_nop 0
	s_mov_b32 m0, s42
	s_nop 0
	global_load_lds_dwordx4 v135, s[36:37]
	s_add_u32 s36, s19, 0x40100
	s_addc_u32 s37, s21, 0
	s_mov_b32 m0, s43
	s_nop 0
	global_load_lds_dwordx4 v114, s[36:37]
	s_nop 0
	s_mov_b32 m0, s44
	s_nop 0
	global_load_lds_dwordx4 v135, s[36:37]
	s_mov_b32 m0, s40
	s_nop 0
	global_load_lds_dwordx4 v65, s[34:35]
	s_nop 0
	s_mov_b32 m0, s45
	s_nop 0
	global_load_lds_dwordx4 v134, s[34:35]
	s_waitcnt vmcnt(8)
	s_waitcnt lgkmcnt(0)
	s_barrier
	s_setprio 1
	s_waitcnt lgkmcnt(0)
	v_mfma_f32_16x16x32_bf16 v[60:63], v[140:143], v[172:175], v[60:63]
	v_mfma_f32_16x16x32_bf16 v[56:59], v[148:151], v[172:175], v[56:59]
	s_waitcnt lgkmcnt(5)
	v_mfma_f32_16x16x32_bf16 v[52:55], v[140:143], v[180:183], v[52:55]
	v_mfma_f32_16x16x32_bf16 v[48:51], v[148:151], v[180:183], v[48:51]
	s_waitcnt lgkmcnt(3)
	v_mfma_f32_16x16x32_bf16 v[44:47], v[140:143], v[188:191], v[44:47]
	v_mfma_f32_16x16x32_bf16 v[40:43], v[148:151], v[188:191], v[40:43]
	s_waitcnt lgkmcnt(1)
	v_mfma_f32_16x16x32_bf16 v[36:39], v[140:143], v[202:205], v[36:39]
	v_mfma_f32_16x16x32_bf16 v[32:35], v[148:151], v[202:205], v[32:35]
	v_mfma_f32_16x16x32_bf16 v[60:63], v[144:147], v[176:179], v[60:63]
	v_mfma_f32_16x16x32_bf16 v[56:59], v[152:155], v[176:179], v[56:59]
	v_mfma_f32_16x16x32_bf16 v[52:55], v[144:147], v[184:187], v[52:55]
	v_mfma_f32_16x16x32_bf16 v[48:51], v[152:155], v[184:187], v[48:51]
	v_mfma_f32_16x16x32_bf16 v[44:47], v[144:147], v[194:197], v[44:47]
	v_mfma_f32_16x16x32_bf16 v[40:43], v[152:155], v[194:197], v[40:43]
	s_waitcnt lgkmcnt(0)
	v_mfma_f32_16x16x32_bf16 v[36:39], v[144:147], v[206:209], v[36:39]
	v_mfma_f32_16x16x32_bf16 v[32:35], v[152:155], v[206:209], v[32:35]
	s_setprio 0
	s_setprio 1
	v_mfma_f32_16x16x32_bf16 v[28:31], v[156:159], v[172:175], v[28:31]
	v_mfma_f32_16x16x32_bf16 v[24:27], v[164:167], v[172:175], v[24:27]
	v_mfma_f32_16x16x32_bf16 v[20:23], v[156:159], v[180:183], v[20:23]
	v_mfma_f32_16x16x32_bf16 v[16:19], v[164:167], v[180:183], v[16:19]
	v_mfma_f32_16x16x32_bf16 v[12:15], v[156:159], v[188:191], v[12:15]
	v_mfma_f32_16x16x32_bf16 v[8:11], v[164:167], v[188:191], v[8:11]
	v_mfma_f32_16x16x32_bf16 v[4:7], v[156:159], v[202:205], v[4:7]
	v_mfma_f32_16x16x32_bf16 v[0:3], v[164:167], v[202:205], v[0:3]
	v_mfma_f32_16x16x32_bf16 v[28:31], v[160:163], v[176:179], v[28:31]
	v_mfma_f32_16x16x32_bf16 v[24:27], v[168:171], v[176:179], v[24:27]
	v_mfma_f32_16x16x32_bf16 v[20:23], v[160:163], v[184:187], v[20:23]
	v_mfma_f32_16x16x32_bf16 v[16:19], v[168:171], v[184:187], v[16:19]
	v_mfma_f32_16x16x32_bf16 v[12:15], v[160:163], v[194:197], v[12:15]
	v_mfma_f32_16x16x32_bf16 v[8:11], v[168:171], v[194:197], v[8:11]
	v_mfma_f32_16x16x32_bf16 v[4:7], v[160:163], v[206:209], v[4:7]
	v_mfma_f32_16x16x32_bf16 v[0:3], v[168:171], v[206:209], v[0:3]
	s_setprio 0
	s_barrier
	v_add_u32_e32 v133, 0x18000, v136
	v_add_u32_e32 v139, 0x1c000, v136
	ds_read_b128 v[140:143], v133
	ds_read_b128 v[144:147], v133 offset:1024
	ds_read_b128 v[148:151], v133 offset:2048
	ds_read_b128 v[152:155], v133 offset:3072
	ds_read_b128 v[156:159], v139
	ds_read_b128 v[160:163], v139 offset:1024
	ds_read_b128 v[164:167], v139 offset:2048
	ds_read_b128 v[168:171], v139 offset:3072
	ds_read_b128 v[172:175], v137 offset:32768
	ds_read_b128 v[176:179], v137 offset:33792
	ds_read_b128 v[180:183], v137 offset:34816
	ds_read_b128 v[184:187], v137 offset:35840
	ds_read_b128 v[188:191], v137 offset:36864
	ds_read_b128 v[194:197], v137 offset:37888
	ds_read_b128 v[202:205], v137 offset:38912
	ds_read_b128 v[206:209], v137 offset:39936
	s_add_u32 s34, s33, 0x40100
	s_addc_u32 s35, s61, 0
	s_mov_b32 m0, s46
	s_nop 0
	global_load_lds_dwordx4 v65, s[34:35]
	s_nop 0
	s_mov_b32 m0, s47
	s_nop 0
	global_load_lds_dwordx4 v134, s[34:35]
	s_waitcnt vmcnt(8)
	s_waitcnt lgkmcnt(0)
	s_barrier
	s_setprio 1
	s_waitcnt lgkmcnt(0)
	v_mfma_f32_16x16x32_bf16 v[128:131], v[140:143], v[172:175], v[128:131]
	v_mfma_f32_16x16x32_bf16 v[124:127], v[148:151], v[172:175], v[124:127]
	s_waitcnt lgkmcnt(5)
	v_mfma_f32_16x16x32_bf16 v[120:123], v[140:143], v[180:183], v[120:123]
	v_mfma_f32_16x16x32_bf16 v[116:119], v[148:151], v[180:183], v[116:119]
	s_waitcnt lgkmcnt(3)
	v_mfma_f32_16x16x32_bf16 v[110:113], v[140:143], v[188:191], v[110:113]
	v_mfma_f32_16x16x32_bf16 v[106:109], v[148:151], v[188:191], v[106:109]
	s_waitcnt lgkmcnt(1)
	v_mfma_f32_16x16x32_bf16 v[102:105], v[140:143], v[202:205], v[102:105]
	v_mfma_f32_16x16x32_bf16 v[98:101], v[148:151], v[202:205], v[98:101]
	v_mfma_f32_16x16x32_bf16 v[128:131], v[144:147], v[176:179], v[128:131]
	v_mfma_f32_16x16x32_bf16 v[124:127], v[152:155], v[176:179], v[124:127]
	v_mfma_f32_16x16x32_bf16 v[120:123], v[144:147], v[184:187], v[120:123]
	v_mfma_f32_16x16x32_bf16 v[116:119], v[152:155], v[184:187], v[116:119]
	v_mfma_f32_16x16x32_bf16 v[110:113], v[144:147], v[194:197], v[110:113]
	v_mfma_f32_16x16x32_bf16 v[106:109], v[152:155], v[194:197], v[106:109]
	s_waitcnt lgkmcnt(0)
	v_mfma_f32_16x16x32_bf16 v[102:105], v[144:147], v[206:209], v[102:105]
	v_mfma_f32_16x16x32_bf16 v[98:101], v[152:155], v[206:209], v[98:101]
	s_setprio 0
	s_setprio 1
	v_mfma_f32_16x16x32_bf16 v[94:97], v[156:159], v[172:175], v[94:97]
	v_mfma_f32_16x16x32_bf16 v[90:93], v[164:167], v[172:175], v[90:93]
	v_mfma_f32_16x16x32_bf16 v[86:89], v[156:159], v[180:183], v[86:89]
	v_mfma_f32_16x16x32_bf16 v[82:85], v[164:167], v[180:183], v[82:85]
	v_mfma_f32_16x16x32_bf16 v[78:81], v[156:159], v[188:191], v[78:81]
	v_mfma_f32_16x16x32_bf16 v[74:77], v[164:167], v[188:191], v[74:77]
	v_mfma_f32_16x16x32_bf16 v[70:73], v[156:159], v[202:205], v[70:73]
	v_mfma_f32_16x16x32_bf16 v[66:69], v[164:167], v[202:205], v[66:69]
	v_mfma_f32_16x16x32_bf16 v[94:97], v[160:163], v[176:179], v[94:97]
	v_mfma_f32_16x16x32_bf16 v[90:93], v[168:171], v[176:179], v[90:93]
	v_mfma_f32_16x16x32_bf16 v[86:89], v[160:163], v[184:187], v[86:89]
	v_mfma_f32_16x16x32_bf16 v[82:85], v[168:171], v[184:187], v[82:85]
	v_mfma_f32_16x16x32_bf16 v[78:81], v[160:163], v[194:197], v[78:81]
	v_mfma_f32_16x16x32_bf16 v[74:77], v[168:171], v[194:197], v[74:77]
	v_mfma_f32_16x16x32_bf16 v[70:73], v[160:163], v[206:209], v[70:73]
	v_mfma_f32_16x16x32_bf16 v[66:69], v[168:171], v[206:209], v[66:69]
	s_setprio 0
	s_barrier
	ds_read_b128 v[172:175], v137 offset:49152
	ds_read_b128 v[176:179], v137 offset:50176
	ds_read_b128 v[180:183], v137 offset:51200
	ds_read_b128 v[184:187], v137 offset:52224
	ds_read_b128 v[188:191], v137 offset:53248
	ds_read_b128 v[194:197], v137 offset:54272
	ds_read_b128 v[202:205], v137 offset:55296
	ds_read_b128 v[206:209], v137 offset:56320
	s_add_u32 s34, s19, 0x180
	s_addc_u32 s35, s21, 0
	s_mov_b32 m0, s51
	s_nop 0
	global_load_lds_dwordx4 v114, s[34:35]
	s_nop 0
	s_mov_b32 m0, s52
	s_nop 0
	global_load_lds_dwordx4 v135, s[34:35]
	s_add_u32 s34, s19, 0x40180
	s_addc_u32 s35, s21, 0
	s_mov_b32 m0, s55
	s_nop 0
	global_load_lds_dwordx4 v114, s[34:35]
	s_nop 0
	s_mov_b32 m0, s56
	s_nop 0
	global_load_lds_dwordx4 v135, s[34:35]
	s_nop 0
	s_mov_b32 m0, s53
	s_nop 0
	global_load_lds_dwordx4 v65, s[26:27]
	s_nop 0
	s_mov_b32 m0, s54
	s_nop 0
	global_load_lds_dwordx4 v134, s[26:27]
	s_waitcnt vmcnt(8)
	s_waitcnt lgkmcnt(0)
	s_barrier
	s_setprio 1
	s_waitcnt lgkmcnt(0)
	v_mfma_f32_16x16x32_bf16 v[60:63], v[140:143], v[172:175], v[60:63]
	v_mfma_f32_16x16x32_bf16 v[56:59], v[148:151], v[172:175], v[56:59]
	s_waitcnt lgkmcnt(5)
	v_mfma_f32_16x16x32_bf16 v[52:55], v[140:143], v[180:183], v[52:55]
	v_mfma_f32_16x16x32_bf16 v[48:51], v[148:151], v[180:183], v[48:51]
	s_waitcnt lgkmcnt(3)
	v_mfma_f32_16x16x32_bf16 v[44:47], v[140:143], v[188:191], v[44:47]
	v_mfma_f32_16x16x32_bf16 v[40:43], v[148:151], v[188:191], v[40:43]
	s_waitcnt lgkmcnt(1)
	v_mfma_f32_16x16x32_bf16 v[36:39], v[140:143], v[202:205], v[36:39]
	v_mfma_f32_16x16x32_bf16 v[32:35], v[148:151], v[202:205], v[32:35]
	v_mfma_f32_16x16x32_bf16 v[60:63], v[144:147], v[176:179], v[60:63]
	v_mfma_f32_16x16x32_bf16 v[56:59], v[152:155], v[176:179], v[56:59]
	v_mfma_f32_16x16x32_bf16 v[52:55], v[144:147], v[184:187], v[52:55]
	v_mfma_f32_16x16x32_bf16 v[48:51], v[152:155], v[184:187], v[48:51]
	v_mfma_f32_16x16x32_bf16 v[44:47], v[144:147], v[194:197], v[44:47]
	v_mfma_f32_16x16x32_bf16 v[40:43], v[152:155], v[194:197], v[40:43]
	s_waitcnt lgkmcnt(0)
	v_mfma_f32_16x16x32_bf16 v[36:39], v[144:147], v[206:209], v[36:39]
	v_mfma_f32_16x16x32_bf16 v[32:35], v[152:155], v[206:209], v[32:35]
	s_setprio 0
	s_setprio 1
	v_mfma_f32_16x16x32_bf16 v[28:31], v[156:159], v[172:175], v[28:31]
	v_mfma_f32_16x16x32_bf16 v[24:27], v[164:167], v[172:175], v[24:27]
	v_mfma_f32_16x16x32_bf16 v[20:23], v[156:159], v[180:183], v[20:23]
	v_mfma_f32_16x16x32_bf16 v[16:19], v[164:167], v[180:183], v[16:19]
	v_mfma_f32_16x16x32_bf16 v[12:15], v[156:159], v[188:191], v[12:15]
	v_mfma_f32_16x16x32_bf16 v[8:11], v[164:167], v[188:191], v[8:11]
	v_mfma_f32_16x16x32_bf16 v[4:7], v[156:159], v[202:205], v[4:7]
	v_mfma_f32_16x16x32_bf16 v[0:3], v[164:167], v[202:205], v[0:3]
	v_mfma_f32_16x16x32_bf16 v[28:31], v[160:163], v[176:179], v[28:31]
	v_mfma_f32_16x16x32_bf16 v[24:27], v[168:171], v[176:179], v[24:27]
	v_mfma_f32_16x16x32_bf16 v[20:23], v[160:163], v[184:187], v[20:23]
	v_mfma_f32_16x16x32_bf16 v[16:19], v[168:171], v[184:187], v[16:19]
	v_mfma_f32_16x16x32_bf16 v[12:15], v[160:163], v[194:197], v[12:15]
	v_mfma_f32_16x16x32_bf16 v[8:11], v[168:171], v[194:197], v[8:11]
	v_mfma_f32_16x16x32_bf16 v[4:7], v[160:163], v[206:209], v[4:7]
	v_mfma_f32_16x16x32_bf16 v[0:3], v[168:171], v[206:209], v[0:3]
	s_setprio 0
	s_barrier
	s_add_i32 s17, s17, 2
	s_add_u32 s2, s2, 0x100
	s_addc_u32 s3, s3, 0
	s_cmp_lt_u32 s17, 12
	s_cbranch_scc1 .LBB0_309
	s_ashr_i32 s19, s18, 31
	s_ashr_i32 s17, s16, 31
	ds_read_b128 v[140:143], v132
	ds_read_b128 v[144:147], v132 offset:1024
	ds_read_b128 v[148:151], v132 offset:2048
	ds_read_b128 v[152:155], v132 offset:3072
	ds_read_b128 v[156:159], v138
	ds_read_b128 v[160:163], v138 offset:1024
	ds_read_b128 v[164:167], v138 offset:2048
	ds_read_b128 v[168:171], v138 offset:3072
	s_lshl_b64 s[2:3], s[18:19], 19
	s_lshl_b64 s[26:27], s[16:17], 19
	s_add_u32 s2, s29, s2
	s_addc_u32 s3, s38, s3
	s_add_u32 s26, s30, s26
	s_addc_u32 s27, s39, s27
	s_and_b64 s[34:35], s[0:1], exec
	s_cselect_b32 s36, s2, s22
	s_cselect_b32 s37, s3, s23
	s_add_u32 s34, s36, 0x80
	s_addc_u32 s35, s37, 0
	s_and_b64 s[62:63], s[0:1], exec
	s_cselect_b32 s25, s27, s25
	s_cselect_b32 s24, s26, s24
	ds_read_b128 v[172:175], v137
	ds_read_b128 v[176:179], v137 offset:1024
	ds_read_b128 v[180:183], v137 offset:2048
	ds_read_b128 v[184:187], v137 offset:3072
	ds_read_b128 v[188:191], v137 offset:4096
	ds_read_b128 v[194:197], v137 offset:5120
	ds_read_b128 v[202:205], v137 offset:6144
	ds_read_b128 v[206:209], v137 offset:7168
	s_add_u32 s22, s22, 0x40780
	s_addc_u32 s23, s23, 0
	s_mov_b32 m0, s57
	s_nop 0
	global_load_lds_dwordx4 v65, s[22:23]
	s_nop 0
	s_mov_b32 m0, s59
	s_nop 0
	global_load_lds_dwordx4 v134, s[22:23]
	s_waitcnt vmcnt(8)
	s_waitcnt lgkmcnt(0)
	s_barrier
	s_setprio 1
	s_waitcnt lgkmcnt(0)
	v_mfma_f32_16x16x32_bf16 v[128:131], v[140:143], v[172:175], v[128:131]
	v_mfma_f32_16x16x32_bf16 v[124:127], v[148:151], v[172:175], v[124:127]
	s_waitcnt lgkmcnt(5)
	v_mfma_f32_16x16x32_bf16 v[120:123], v[140:143], v[180:183], v[120:123]
	v_mfma_f32_16x16x32_bf16 v[116:119], v[148:151], v[180:183], v[116:119]
	s_waitcnt lgkmcnt(1)
	v_mfma_f32_16x16x32_bf16 v[102:105], v[140:143], v[202:205], v[102:105]
	v_mfma_f32_16x16x32_bf16 v[98:101], v[148:151], v[202:205], v[98:101]
	v_mfma_f32_16x16x32_bf16 v[128:131], v[144:147], v[176:179], v[128:131]
	v_mfma_f32_16x16x32_bf16 v[124:127], v[152:155], v[176:179], v[124:127]
	v_mfma_f32_16x16x32_bf16 v[120:123], v[144:147], v[184:187], v[120:123]
	v_mfma_f32_16x16x32_bf16 v[116:119], v[152:155], v[184:187], v[116:119]
	v_mfma_f32_16x16x32_bf16 v[110:113], v[140:143], v[188:191], v[110:113]
	v_mfma_f32_16x16x32_bf16 v[106:109], v[148:151], v[188:191], v[106:109]
	s_waitcnt lgkmcnt(0)
	v_mfma_f32_16x16x32_bf16 v[102:105], v[144:147], v[206:209], v[102:105]
	v_mfma_f32_16x16x32_bf16 v[98:101], v[152:155], v[206:209], v[98:101]
	v_mfma_f32_16x16x32_bf16 v[210:213], v[144:147], v[194:197], v[110:113]
	v_mfma_f32_16x16x32_bf16 v[214:217], v[152:155], v[194:197], v[106:109]
	s_setprio 0
	s_setprio 1
	v_mfma_f32_16x16x32_bf16 v[94:97], v[156:159], v[172:175], v[94:97]
	v_mfma_f32_16x16x32_bf16 v[90:93], v[164:167], v[172:175], v[90:93]
	v_mfma_f32_16x16x32_bf16 v[86:89], v[156:159], v[180:183], v[86:89]
	v_mfma_f32_16x16x32_bf16 v[82:85], v[164:167], v[180:183], v[82:85]
	v_mfma_f32_16x16x32_bf16 v[70:73], v[156:159], v[202:205], v[70:73]
	v_mfma_f32_16x16x32_bf16 v[66:69], v[164:167], v[202:205], v[66:69]
	v_mfma_f32_16x16x32_bf16 v[94:97], v[160:163], v[176:179], v[94:97]
	v_mfma_f32_16x16x32_bf16 v[90:93], v[168:171], v[176:179], v[90:93]
	v_mfma_f32_16x16x32_bf16 v[86:89], v[160:163], v[184:187], v[86:89]
	v_mfma_f32_16x16x32_bf16 v[82:85], v[168:171], v[184:187], v[82:85]
	v_mfma_f32_16x16x32_bf16 v[78:81], v[156:159], v[188:191], v[78:81]
	v_mfma_f32_16x16x32_bf16 v[74:77], v[164:167], v[188:191], v[74:77]
	v_mfma_f32_16x16x32_bf16 v[70:73], v[160:163], v[206:209], v[70:73]
	v_mfma_f32_16x16x32_bf16 v[66:69], v[168:171], v[206:209], v[66:69]
	v_mfma_f32_16x16x32_bf16 v[172:175], v[160:163], v[194:197], v[78:81]
	v_mfma_f32_16x16x32_bf16 v[176:179], v[168:171], v[194:197], v[74:77]
	s_setprio 0
	s_barrier
	s_nop 1
	ds_read_b128 v[74:77], v137 offset:16384
	ds_read_b128 v[78:81], v137 offset:17408
	ds_read_b128 v[106:109], v137 offset:18432
	ds_read_b128 v[110:113], v137 offset:19456
	ds_read_b128 v[180:183], v137 offset:20480
	ds_read_b128 v[184:187], v137 offset:21504
	ds_read_b128 v[188:191], v137 offset:22528
	ds_read_b128 v[194:197], v137 offset:23552
	s_mov_b64 exec, s[100:101]
	s_mov_b32 m0, s41
	s_nop 0
	global_load_lds_dwordx4 v114, s[24:25]
	s_mov_b64 exec, -1
	s_add_u32 s22, s24, 0x40000
	s_mov_b64 exec, s[100:101]
	s_mov_b32 m0, s42
	s_nop 0
	global_load_lds_dwordx4 v135, s[24:25]
	s_mov_b64 exec, -1
	s_addc_u32 s23, s25, 0
	s_mov_b64 exec, s[100:101]
	s_mov_b32 m0, s43
	s_nop 0
	global_load_lds_dwordx4 v114, s[22:23]
	s_mov_b64 exec, -1
	s_nop 0
	s_mov_b64 exec, s[100:101]
	s_mov_b32 m0, s44
	s_nop 0
	global_load_lds_dwordx4 v135, s[22:23]
	s_mov_b64 exec, -1
	s_nop 0
	s_mov_b64 exec, s[100:101]
	s_mov_b32 m0, s40
	s_nop 0
	global_load_lds_dwordx4 v65, s[36:37]
	s_mov_b64 exec, -1
	s_nop 0
	s_mov_b64 exec, s[100:101]
	s_mov_b32 m0, s45
	s_nop 0
	global_load_lds_dwordx4 v134, s[36:37]
	s_mov_b64 exec, -1
	s_waitcnt vmcnt(8)
	s_waitcnt lgkmcnt(0)
	s_barrier
	s_setprio 1
	s_waitcnt lgkmcnt(0)
	v_mfma_f32_16x16x32_bf16 v[52:55], v[140:143], v[106:109], v[52:55]
	v_mfma_f32_16x16x32_bf16 v[48:51], v[148:151], v[106:109], v[48:51]
	v_mfma_f32_16x16x32_bf16 v[60:63], v[140:143], v[74:77], v[60:63]
	v_mfma_f32_16x16x32_bf16 v[56:59], v[148:151], v[74:77], v[56:59]
	s_waitcnt lgkmcnt(4)
	v_mfma_f32_16x16x32_bf16 v[52:55], v[144:147], v[110:113], v[52:55]
	v_mfma_f32_16x16x32_bf16 v[48:51], v[152:155], v[110:113], v[48:51]
	s_waitcnt lgkmcnt(3)
	v_mfma_f32_16x16x32_bf16 v[44:47], v[140:143], v[180:183], v[44:47]
	v_mfma_f32_16x16x32_bf16 v[40:43], v[148:151], v[180:183], v[40:43]
	s_waitcnt lgkmcnt(1)
	v_mfma_f32_16x16x32_bf16 v[36:39], v[140:143], v[188:191], v[36:39]
	v_mfma_f32_16x16x32_bf16 v[32:35], v[148:151], v[188:191], v[32:35]
	v_mfma_f32_16x16x32_bf16 v[202:205], v[144:147], v[78:81], v[60:63]
	v_mfma_f32_16x16x32_bf16 v[206:209], v[152:155], v[78:81], v[56:59]
	v_mfma_f32_16x16x32_bf16 v[218:221], v[144:147], v[184:187], v[44:47]
	v_mfma_f32_16x16x32_bf16 v[222:225], v[152:155], v[184:187], v[40:43]
	s_waitcnt lgkmcnt(0)
	v_mfma_f32_16x16x32_bf16 v[140:143], v[144:147], v[194:197], v[36:39]
	v_mfma_f32_16x16x32_bf16 v[144:147], v[152:155], v[194:197], v[32:35]
	s_setprio 0
	s_setprio 1
	v_mfma_f32_16x16x32_bf16 v[20:23], v[156:159], v[106:109], v[20:23]
	v_mfma_f32_16x16x32_bf16 v[16:19], v[164:167], v[106:109], v[16:19]
	v_mfma_f32_16x16x32_bf16 v[28:31], v[156:159], v[74:77], v[28:31]
	v_mfma_f32_16x16x32_bf16 v[24:27], v[164:167], v[74:77], v[24:27]
	v_mfma_f32_16x16x32_bf16 v[20:23], v[160:163], v[110:113], v[20:23]
	v_mfma_f32_16x16x32_bf16 v[16:19], v[168:171], v[110:113], v[16:19]
	v_mfma_f32_16x16x32_bf16 v[12:15], v[156:159], v[180:183], v[12:15]
	v_mfma_f32_16x16x32_bf16 v[8:11], v[164:167], v[180:183], v[8:11]
	v_mfma_f32_16x16x32_bf16 v[4:7], v[156:159], v[188:191], v[4:7]
	v_mfma_f32_16x16x32_bf16 v[0:3], v[164:167], v[188:191], v[0:3]
	v_mfma_f32_16x16x32_bf16 v[148:151], v[160:163], v[78:81], v[28:31]
	v_mfma_f32_16x16x32_bf16 v[152:155], v[168:171], v[78:81], v[24:27]
	v_mfma_f32_16x16x32_bf16 v[226:229], v[160:163], v[184:187], v[12:15]
	v_mfma_f32_16x16x32_bf16 v[180:183], v[168:171], v[184:187], v[8:11]
	v_mfma_f32_16x16x32_bf16 v[156:159], v[160:163], v[194:197], v[4:7]
	v_mfma_f32_16x16x32_bf16 v[160:163], v[168:171], v[194:197], v[0:3]
	s_setprio 0
	s_barrier
	s_nop 0
	ds_read_b128 v[0:3], v133
	ds_read_b128 v[4:7], v133 offset:1024
	ds_read_b128 v[164:167], v133 offset:2048
	ds_read_b128 v[168:171], v133 offset:3072
	ds_read_b128 v[184:187], v139
	ds_read_b128 v[188:191], v139 offset:1024
	ds_read_b128 v[194:197], v139 offset:2048
	ds_read_b128 v[230:233], v139 offset:3072
	ds_read_b128 v[24:27], v137 offset:32768
	ds_read_b128 v[28:31], v137 offset:33792
	ds_read_b128 v[32:35], v137 offset:34816
	ds_read_b128 v[36:39], v137 offset:35840
	ds_read_b128 v[60:63], v137 offset:36864
	ds_read_b128 v[244:247], v137 offset:37888
	ds_read_b128 v[248:251], v137 offset:38912
	ds_read_b128 v[198:201], v137 offset:39936
	s_add_u32 s22, s36, 0x40000
	s_addc_u32 s23, s37, 0
	s_mov_b64 exec, s[100:101]
	s_mov_b32 m0, s46
	s_nop 0
	global_load_lds_dwordx4 v65, s[22:23]
	s_mov_b64 exec, -1
	s_nop 0
	s_mov_b64 exec, s[100:101]
	s_mov_b32 m0, s47
	s_nop 0
	global_load_lds_dwordx4 v134, s[22:23]
	s_mov_b64 exec, -1
	s_waitcnt vmcnt(8)
	s_waitcnt lgkmcnt(0)
	s_barrier
	s_setprio 1
	s_waitcnt lgkmcnt(0)
	v_mfma_f32_16x16x32_bf16 v[8:11], v[0:3], v[24:27], v[128:131]
	s_waitcnt lgkmcnt(6)
	v_mfma_f32_16x16x32_bf16 v[106:109], v[4:7], v[28:31], v[8:11]
	v_mfma_f32_16x16x32_bf16 v[8:11], v[164:167], v[24:27], v[124:127]
	v_mfma_f32_16x16x32_bf16 v[110:113], v[168:171], v[28:31], v[8:11]
	s_waitcnt lgkmcnt(5)
	v_mfma_f32_16x16x32_bf16 v[8:11], v[0:3], v[32:35], v[120:123]
	s_waitcnt lgkmcnt(4)
	v_mfma_f32_16x16x32_bf16 v[74:77], v[4:7], v[36:39], v[8:11]
	v_mfma_f32_16x16x32_bf16 v[8:11], v[164:167], v[32:35], v[116:119]
	v_mfma_f32_16x16x32_bf16 v[78:81], v[168:171], v[36:39], v[8:11]
	s_waitcnt lgkmcnt(3)
	v_mfma_f32_16x16x32_bf16 v[8:11], v[0:3], v[60:63], v[210:213]
	s_waitcnt lgkmcnt(2)
	v_mfma_f32_16x16x32_bf16 v[40:43], v[4:7], v[244:247], v[8:11]
	v_mfma_f32_16x16x32_bf16 v[8:11], v[164:167], v[60:63], v[214:217]
	v_mfma_f32_16x16x32_bf16 v[44:47], v[168:171], v[244:247], v[8:11]
	s_waitcnt lgkmcnt(1)
	v_mfma_f32_16x16x32_bf16 v[8:11], v[0:3], v[248:251], v[102:105]
	v_mfma_f32_16x16x32_bf16 v[12:15], v[164:167], v[248:251], v[98:101]
	s_waitcnt lgkmcnt(0)
	v_mfma_f32_16x16x32_bf16 v[8:11], v[4:7], v[198:201], v[8:11]
	v_mfma_f32_16x16x32_bf16 v[12:15], v[168:171], v[198:201], v[12:15]
	s_setprio 0
	s_setprio 1
	v_mfma_f32_16x16x32_bf16 v[56:59], v[184:187], v[24:27], v[94:97]
	v_mfma_f32_16x16x32_bf16 v[24:27], v[194:197], v[24:27], v[90:93]
	v_mfma_f32_16x16x32_bf16 v[128:131], v[230:233], v[28:31], v[24:27]
	v_mfma_f32_16x16x32_bf16 v[24:27], v[184:187], v[32:35], v[86:89]
	v_mfma_f32_16x16x32_bf16 v[90:93], v[188:191], v[36:39], v[24:27]
	v_mfma_f32_16x16x32_bf16 v[24:27], v[194:197], v[32:35], v[82:85]
	v_mfma_f32_16x16x32_bf16 v[94:97], v[230:233], v[36:39], v[24:27]
	v_mfma_f32_16x16x32_bf16 v[24:27], v[184:187], v[60:63], v[172:175]
	v_mfma_f32_16x16x32_bf16 v[124:127], v[188:191], v[28:31], v[56:59]
	v_mfma_f32_16x16x32_bf16 v[56:59], v[188:191], v[244:247], v[24:27]
	v_mfma_f32_16x16x32_bf16 v[24:27], v[194:197], v[60:63], v[176:179]
	v_mfma_f32_16x16x32_bf16 v[60:63], v[230:233], v[244:247], v[24:27]
	v_mfma_f32_16x16x32_bf16 v[24:27], v[184:187], v[248:251], v[70:73]
	v_mfma_f32_16x16x32_bf16 v[28:31], v[194:197], v[248:251], v[66:69]
	v_mfma_f32_16x16x32_bf16 v[24:27], v[188:191], v[198:201], v[24:27]
	v_mfma_f32_16x16x32_bf16 v[28:31], v[230:233], v[198:201], v[28:31]
	s_setprio 0
	s_barrier
	ds_read_b128 v[82:85], v137 offset:49152
	ds_read_b128 v[86:89], v137 offset:50176
	ds_read_b128 v[172:175], v137 offset:51200
	ds_read_b128 v[176:179], v137 offset:52224
	ds_read_b128 v[198:201], v137 offset:53248
	ds_read_b128 v[210:213], v137 offset:54272
	ds_read_b128 v[214:217], v137 offset:55296
	ds_read_b128 v[244:247], v137 offset:56320
	s_add_u32 s22, s24, 0x80
	s_addc_u32 s23, s25, 0
	s_mov_b64 exec, s[100:101]
	s_mov_b32 m0, s51
	s_nop 0
	global_load_lds_dwordx4 v114, s[22:23]
	s_mov_b64 exec, -1
	s_nop 0
	s_mov_b64 exec, s[100:101]
	s_mov_b32 m0, s52
	s_nop 0
	global_load_lds_dwordx4 v135, s[22:23]
	s_mov_b64 exec, -1
	s_add_u32 s22, s24, 0x40080
	s_addc_u32 s23, s25, 0
	s_mov_b64 exec, s[100:101]
	s_mov_b32 m0, s55
	s_nop 0
	global_load_lds_dwordx4 v114, s[22:23]
	s_mov_b64 exec, -1
	s_nop 0
	s_mov_b64 exec, s[100:101]
	s_mov_b32 m0, s56
	s_nop 0
	global_load_lds_dwordx4 v135, s[22:23]
	s_mov_b64 exec, -1
	s_nop 0
	s_mov_b64 exec, s[100:101]
	s_mov_b32 m0, s53
	s_nop 0
	global_load_lds_dwordx4 v65, s[34:35]
	s_mov_b64 exec, -1
	s_nop 0
	s_mov_b64 exec, s[100:101]
	s_mov_b32 m0, s54
	s_nop 0
	global_load_lds_dwordx4 v134, s[34:35]
	s_mov_b64 exec, -1
	s_waitcnt vmcnt(8)
	s_waitcnt lgkmcnt(0)
	s_barrier
	s_setprio 1
	s_waitcnt lgkmcnt(0)
	v_mfma_f32_16x16x32_bf16 v[32:35], v[0:3], v[82:85], v[202:205]
	s_waitcnt lgkmcnt(6)
	v_mfma_f32_16x16x32_bf16 v[98:101], v[4:7], v[86:89], v[32:35]
	v_mfma_f32_16x16x32_bf16 v[32:35], v[164:167], v[82:85], v[206:209]
	v_mfma_f32_16x16x32_bf16 v[102:105], v[168:171], v[86:89], v[32:35]
	s_waitcnt lgkmcnt(5)
	v_mfma_f32_16x16x32_bf16 v[32:35], v[0:3], v[172:175], v[52:55]
	s_waitcnt lgkmcnt(4)
	v_mfma_f32_16x16x32_bf16 v[66:69], v[4:7], v[176:179], v[32:35]
	v_mfma_f32_16x16x32_bf16 v[32:35], v[164:167], v[172:175], v[48:51]
	v_mfma_f32_16x16x32_bf16 v[70:73], v[168:171], v[176:179], v[32:35]
	s_waitcnt lgkmcnt(3)
	v_mfma_f32_16x16x32_bf16 v[32:35], v[0:3], v[198:201], v[218:221]
	s_waitcnt lgkmcnt(1)
	v_mfma_f32_16x16x32_bf16 v[0:3], v[0:3], v[214:217], v[140:143]
	v_mfma_f32_16x16x32_bf16 v[32:35], v[4:7], v[210:213], v[32:35]
	v_mfma_f32_16x16x32_bf16 v[36:39], v[164:167], v[198:201], v[222:225]
	s_waitcnt lgkmcnt(0)
	v_mfma_f32_16x16x32_bf16 v[0:3], v[4:7], v[244:247], v[0:3]
	v_mfma_f32_16x16x32_bf16 v[4:7], v[164:167], v[214:217], v[144:147]
	v_mfma_f32_16x16x32_bf16 v[36:39], v[168:171], v[210:213], v[36:39]
	v_mfma_f32_16x16x32_bf16 v[4:7], v[168:171], v[244:247], v[4:7]
	s_setprio 0
	s_setprio 1
	v_mfma_f32_16x16x32_bf16 v[48:51], v[184:187], v[82:85], v[148:151]
	v_mfma_f32_16x16x32_bf16 v[116:119], v[188:191], v[86:89], v[48:51]
	v_mfma_f32_16x16x32_bf16 v[48:51], v[194:197], v[82:85], v[152:155]
	v_mfma_f32_16x16x32_bf16 v[16:19], v[194:197], v[172:175], v[16:19]
	v_mfma_f32_16x16x32_bf16 v[120:123], v[230:233], v[86:89], v[48:51]
	v_mfma_f32_16x16x32_bf16 v[86:89], v[230:233], v[176:179], v[16:19]
	v_mfma_f32_16x16x32_bf16 v[16:19], v[184:187], v[198:201], v[226:229]
	v_mfma_f32_16x16x32_bf16 v[20:23], v[184:187], v[172:175], v[20:23]
	v_mfma_f32_16x16x32_bf16 v[48:51], v[188:191], v[210:213], v[16:19]
	v_mfma_f32_16x16x32_bf16 v[16:19], v[194:197], v[198:201], v[180:183]
	v_mfma_f32_16x16x32_bf16 v[82:85], v[188:191], v[176:179], v[20:23]
	v_mfma_f32_16x16x32_bf16 v[52:55], v[230:233], v[210:213], v[16:19]
	v_mfma_f32_16x16x32_bf16 v[16:19], v[184:187], v[214:217], v[156:159]
	v_mfma_f32_16x16x32_bf16 v[20:23], v[194:197], v[214:217], v[160:163]
	v_mfma_f32_16x16x32_bf16 v[16:19], v[188:191], v[244:247], v[16:19]
	v_mfma_f32_16x16x32_bf16 v[20:23], v[230:233], v[244:247], v[20:23]
	s_setprio 0
	s_barrier
	s_andn2_b64 vcc, exec, s[12:13]
	s_cbranch_vccnz .LBB0_312
	s_barrier

.LBB0_624:
	s_add_i32 s63, s63, 1
	v_readlane_b32 s2, v254, 38
	s_mul_i32 s2, s63, s2
	s_mul_hi_u32 s3, s63, s70
	s_add_i32 s3, s3, s2
	s_mul_i32 s2, s63, s70
	v_readlane_b32 s13, v255, 0
	s_add_u32 s2, s2, s13
	s_addc_u32 s3, s3, s62
	v_mov_b64_e32 v[0:1], 0x4c8
	v_cmp_lt_i64_e64 s[34:35], s[2:3], v[0:1]
	v_mov_b64_e32 v[0:1], 0x4c7
	v_cmp_gt_i64_e32 vcc, s[2:3], v[0:1]
	s_nop 3
	s_cmp_lg_u64 s[34:35], 0
	s_cselect_b64 s[100:101], -1, 1
	s_cbranch_vccnz .LBB0_626
	s_ashr_i32 s3, s2, 31
	s_lshr_b32 s3, s3, 29
	s_add_i32 s3, s2, s3
	s_ashr_i32 s12, s3, 3
	s_and_b32 s3, s3, -8
	s_sub_i32 s2, s2, s3
	s_cmp_lt_i32 s2, 0
	s_movk_i32 s3, 0x9a
	s_cselect_b32 s3, s3, 0x99
	s_mul_i32 s2, s2, s3
	s_add_i32 s2, s2, s12
	s_mul_hi_i32 s3, s2, 0x38e38e39
	s_lshr_b32 s12, s3, 31
	s_ashr_i32 s3, s3, 4
	s_add_i32 s3, s3, s12
	s_lshl_b32 s13, s3, 3
	s_sub_i32 s12, 0x88, s13
	s_min_i32 s14, s12, 8
	s_abs_i32 s12, s14
	v_cvt_f32_u32_e32 v0, s12
	s_sub_i32 s16, 0, s12
	s_mulk_i32 s3, 0x48
	s_sub_i32 s2, s2, s3
	v_rcp_iflag_f32_e32 v0, v0
	s_abs_i32 s3, s2
	s_xor_b32 s15, s2, s14
	s_ashr_i32 s15, s15, 31
	v_mul_f32_e32 v0, 0x4f7ffffe, v0
	v_cvt_u32_f32_e32 v0, v0
	s_nop 0
	v_readfirstlane_b32 s17, v0
	s_mul_i32 s16, s16, s17
	s_mul_hi_u32 s16, s17, s16
	s_add_i32 s17, s17, s16
	s_mul_hi_u32 s16, s3, s17
	s_mul_i32 s17, s16, s12
	s_sub_i32 s3, s3, s17
	s_add_i32 s18, s16, 1
	s_sub_i32 s17, s3, s12
	s_cmp_ge_u32 s3, s12
	s_cselect_b32 s16, s18, s16
	s_cselect_b32 s3, s17, s3
	s_add_i32 s17, s16, 1
	s_cmp_ge_u32 s3, s12
	s_cselect_b32 s3, s17, s16
	s_xor_b32 s3, s3, s15
	s_sub_i32 s12, s3, s15
	s_mul_i32 s3, s12, s14
	s_sub_i32 s2, s2, s3
	s_add_i32 s14, s13, s2

.LBB0_627:
	s_add_u32 s33, s24, s2
	s_addc_u32 s40, s25, s3
	v_add_u32_e32 v114, 0x10000, v143
	v_add_u32_e32 v133, 0x14000, v143
	s_add_u32 s18, s33, 0x100
	ds_read_b128 v[134:137], v114
	ds_read_b128 v[146:149], v114 offset:1024
	ds_read_b128 v[150:153], v114 offset:2048
	ds_read_b128 v[154:157], v114 offset:3072
	ds_read_b128 v[158:161], v133
	ds_read_b128 v[162:165], v133 offset:1024
	ds_read_b128 v[166:169], v133 offset:2048
	ds_read_b128 v[170:173], v133 offset:3072
	s_addc_u32 s19, s40, 0
	s_add_u32 s16, s33, 0x180
	s_addc_u32 s17, s40, 0
	s_add_u32 s15, s26, s2
	s_addc_u32 s23, s27, s3
	s_add_u32 s36, s15, 0x100
	s_addc_u32 s37, s23, 0
	ds_read_b128 v[174:177], v144
	ds_read_b128 v[178:181], v144 offset:1024
	ds_read_b128 v[182:185], v144 offset:2048
	ds_read_b128 v[186:189], v144 offset:3072
	ds_read_b128 v[202:205], v144 offset:4096
	ds_read_b128 v[206:209], v144 offset:5120
	ds_read_b128 v[210:213], v144 offset:6144
	ds_read_b128 v[214:217], v144 offset:7168
	s_add_u32 s38, s33, 0x40080
	s_addc_u32 s39, s40, 0
	s_mov_b32 m0, s60
	s_nop 0
	global_load_lds_dwordx4 v65, s[38:39]
	s_nop 0
	s_mov_b32 m0, s61
	s_nop 0
	global_load_lds_dwordx4 v141, s[38:39]
	s_waitcnt vmcnt(8)
	s_waitcnt lgkmcnt(0)
	s_barrier
	s_setprio 1
	s_waitcnt lgkmcnt(0)
	v_mfma_f32_16x16x32_bf16 v[128:131], v[134:137], v[174:177], v[128:131]
	v_mfma_f32_16x16x32_bf16 v[124:127], v[150:153], v[174:177], v[124:127]
	v_mfma_f32_16x16x32_bf16 v[120:123], v[134:137], v[182:185], v[120:123]
	v_mfma_f32_16x16x32_bf16 v[116:119], v[150:153], v[182:185], v[116:119]
	v_mfma_f32_16x16x32_bf16 v[110:113], v[134:137], v[202:205], v[110:113]
	v_mfma_f32_16x16x32_bf16 v[106:109], v[150:153], v[202:205], v[106:109]
	v_mfma_f32_16x16x32_bf16 v[102:105], v[134:137], v[210:213], v[102:105]
	v_mfma_f32_16x16x32_bf16 v[98:101], v[150:153], v[210:213], v[98:101]
	v_mfma_f32_16x16x32_bf16 v[128:131], v[146:149], v[178:181], v[128:131]
	v_mfma_f32_16x16x32_bf16 v[124:127], v[154:157], v[178:181], v[124:127]
	v_mfma_f32_16x16x32_bf16 v[120:123], v[146:149], v[186:189], v[120:123]
	v_mfma_f32_16x16x32_bf16 v[116:119], v[154:157], v[186:189], v[116:119]
	v_mfma_f32_16x16x32_bf16 v[110:113], v[146:149], v[206:209], v[110:113]
	v_mfma_f32_16x16x32_bf16 v[106:109], v[154:157], v[206:209], v[106:109]
	v_mfma_f32_16x16x32_bf16 v[102:105], v[146:149], v[214:217], v[102:105]
	v_mfma_f32_16x16x32_bf16 v[98:101], v[154:157], v[214:217], v[98:101]
	s_setprio 0
	s_setprio 1
	v_mfma_f32_16x16x32_bf16 v[94:97], v[158:161], v[174:177], v[94:97]
	v_mfma_f32_16x16x32_bf16 v[90:93], v[166:169], v[174:177], v[90:93]
	v_mfma_f32_16x16x32_bf16 v[86:89], v[158:161], v[182:185], v[86:89]
	v_mfma_f32_16x16x32_bf16 v[82:85], v[166:169], v[182:185], v[82:85]
	v_mfma_f32_16x16x32_bf16 v[78:81], v[158:161], v[202:205], v[78:81]
	v_mfma_f32_16x16x32_bf16 v[74:77], v[166:169], v[202:205], v[74:77]
	v_mfma_f32_16x16x32_bf16 v[70:73], v[158:161], v[210:213], v[70:73]
	v_mfma_f32_16x16x32_bf16 v[66:69], v[166:169], v[210:213], v[66:69]
	v_mfma_f32_16x16x32_bf16 v[94:97], v[162:165], v[178:181], v[94:97]
	v_mfma_f32_16x16x32_bf16 v[90:93], v[170:173], v[178:181], v[90:93]
	v_mfma_f32_16x16x32_bf16 v[86:89], v[162:165], v[186:189], v[86:89]
	v_mfma_f32_16x16x32_bf16 v[82:85], v[170:173], v[186:189], v[82:85]
	v_mfma_f32_16x16x32_bf16 v[78:81], v[162:165], v[206:209], v[78:81]
	v_mfma_f32_16x16x32_bf16 v[74:77], v[170:173], v[206:209], v[74:77]
	v_mfma_f32_16x16x32_bf16 v[70:73], v[162:165], v[214:217], v[70:73]
	v_mfma_f32_16x16x32_bf16 v[66:69], v[170:173], v[214:217], v[66:69]
	s_setprio 0
	s_barrier
	ds_read_b128 v[174:177], v144 offset:16384
	ds_read_b128 v[178:181], v144 offset:17408
	ds_read_b128 v[182:185], v144 offset:18432
	ds_read_b128 v[186:189], v144 offset:19456
	ds_read_b128 v[202:205], v144 offset:20480
	ds_read_b128 v[206:209], v144 offset:21504
	ds_read_b128 v[210:213], v144 offset:22528
	ds_read_b128 v[214:217], v144 offset:23552
	s_mov_b32 m0, s48
	s_nop 0
	global_load_lds_dwordx4 v140, s[36:37]
	s_nop 0
	s_mov_b32 m0, s49
	s_nop 0
	global_load_lds_dwordx4 v142, s[36:37]
	s_add_u32 s36, s15, 0x40100
	s_addc_u32 s37, s23, 0
	s_mov_b32 m0, s50
	s_nop 0
	global_load_lds_dwordx4 v140, s[36:37]
	s_nop 0
	s_mov_b32 m0, s51
	s_nop 0
	global_load_lds_dwordx4 v142, s[36:37]
	s_mov_b32 m0, s47
	s_nop 0
	global_load_lds_dwordx4 v65, s[18:19]
	s_nop 0
	s_mov_b32 m0, s52
	s_nop 0
	global_load_lds_dwordx4 v141, s[18:19]
	s_waitcnt vmcnt(8)
	s_waitcnt lgkmcnt(0)
	s_barrier
	s_setprio 1
	s_waitcnt lgkmcnt(0)
	v_mfma_f32_16x16x32_bf16 v[60:63], v[134:137], v[174:177], v[60:63]
	v_mfma_f32_16x16x32_bf16 v[56:59], v[150:153], v[174:177], v[56:59]
	s_waitcnt lgkmcnt(5)
	v_mfma_f32_16x16x32_bf16 v[52:55], v[134:137], v[182:185], v[52:55]
	v_mfma_f32_16x16x32_bf16 v[48:51], v[150:153], v[182:185], v[48:51]
	s_waitcnt lgkmcnt(3)
	v_mfma_f32_16x16x32_bf16 v[44:47], v[134:137], v[202:205], v[44:47]
	v_mfma_f32_16x16x32_bf16 v[40:43], v[150:153], v[202:205], v[40:43]
	s_waitcnt lgkmcnt(1)
	v_mfma_f32_16x16x32_bf16 v[36:39], v[134:137], v[210:213], v[36:39]
	v_mfma_f32_16x16x32_bf16 v[32:35], v[150:153], v[210:213], v[32:35]
	v_mfma_f32_16x16x32_bf16 v[60:63], v[146:149], v[178:181], v[60:63]
	v_mfma_f32_16x16x32_bf16 v[56:59], v[154:157], v[178:181], v[56:59]
	v_mfma_f32_16x16x32_bf16 v[52:55], v[146:149], v[186:189], v[52:55]
	v_mfma_f32_16x16x32_bf16 v[48:51], v[154:157], v[186:189], v[48:51]
	v_mfma_f32_16x16x32_bf16 v[44:47], v[146:149], v[206:209], v[44:47]
	v_mfma_f32_16x16x32_bf16 v[40:43], v[154:157], v[206:209], v[40:43]
	s_waitcnt lgkmcnt(0)
	v_mfma_f32_16x16x32_bf16 v[36:39], v[146:149], v[214:217], v[36:39]
	v_mfma_f32_16x16x32_bf16 v[32:35], v[154:157], v[214:217], v[32:35]
	s_setprio 0
	s_setprio 1
	v_mfma_f32_16x16x32_bf16 v[28:31], v[158:161], v[174:177], v[28:31]
	v_mfma_f32_16x16x32_bf16 v[24:27], v[166:169], v[174:177], v[24:27]
	v_mfma_f32_16x16x32_bf16 v[20:23], v[158:161], v[182:185], v[20:23]
	v_mfma_f32_16x16x32_bf16 v[16:19], v[166:169], v[182:185], v[16:19]
	v_mfma_f32_16x16x32_bf16 v[12:15], v[158:161], v[202:205], v[12:15]
	v_mfma_f32_16x16x32_bf16 v[8:11], v[166:169], v[202:205], v[8:11]
	v_mfma_f32_16x16x32_bf16 v[4:7], v[158:161], v[210:213], v[4:7]
	v_mfma_f32_16x16x32_bf16 v[0:3], v[166:169], v[210:213], v[0:3]
	v_mfma_f32_16x16x32_bf16 v[28:31], v[162:165], v[178:181], v[28:31]
	v_mfma_f32_16x16x32_bf16 v[24:27], v[170:173], v[178:181], v[24:27]
	v_mfma_f32_16x16x32_bf16 v[20:23], v[162:165], v[186:189], v[20:23]
	v_mfma_f32_16x16x32_bf16 v[16:19], v[170:173], v[186:189], v[16:19]
	v_mfma_f32_16x16x32_bf16 v[12:15], v[162:165], v[206:209], v[12:15]
	v_mfma_f32_16x16x32_bf16 v[8:11], v[170:173], v[206:209], v[8:11]
	v_mfma_f32_16x16x32_bf16 v[4:7], v[162:165], v[214:217], v[4:7]
	v_mfma_f32_16x16x32_bf16 v[0:3], v[170:173], v[214:217], v[0:3]
	s_setprio 0
	s_barrier
	v_add_u32_e32 v132, 0x18000, v143
	v_add_u32_e32 v134, 0x1c000, v143
	ds_read_b128 v[136:139], v132
	ds_read_b128 v[146:149], v132 offset:1024
	ds_read_b128 v[150:153], v132 offset:2048
	ds_read_b128 v[154:157], v132 offset:3072
	ds_read_b128 v[158:161], v134
	ds_read_b128 v[162:165], v134 offset:1024
	ds_read_b128 v[166:169], v134 offset:2048
	ds_read_b128 v[170:173], v134 offset:3072
	ds_read_b128 v[174:177], v144 offset:32768
	ds_read_b128 v[178:181], v144 offset:33792
	ds_read_b128 v[182:185], v144 offset:34816
	ds_read_b128 v[186:189], v144 offset:35840
	ds_read_b128 v[202:205], v144 offset:36864
	ds_read_b128 v[206:209], v144 offset:37888
	ds_read_b128 v[210:213], v144 offset:38912
	ds_read_b128 v[214:217], v144 offset:39936
	s_add_u32 s18, s33, 0x40100
	s_addc_u32 s19, s40, 0
	s_mov_b32 m0, s53
	s_nop 0
	global_load_lds_dwordx4 v65, s[18:19]
	s_nop 0
	s_mov_b32 m0, s54
	s_nop 0
	global_load_lds_dwordx4 v141, s[18:19]
	s_waitcnt vmcnt(8)
	s_waitcnt lgkmcnt(0)
	s_barrier
	s_setprio 1
	s_waitcnt lgkmcnt(0)
	v_mfma_f32_16x16x32_bf16 v[128:131], v[136:139], v[174:177], v[128:131]
	v_mfma_f32_16x16x32_bf16 v[124:127], v[150:153], v[174:177], v[124:127]
	s_waitcnt lgkmcnt(5)
	v_mfma_f32_16x16x32_bf16 v[120:123], v[136:139], v[182:185], v[120:123]
	v_mfma_f32_16x16x32_bf16 v[116:119], v[150:153], v[182:185], v[116:119]
	s_waitcnt lgkmcnt(3)
	v_mfma_f32_16x16x32_bf16 v[110:113], v[136:139], v[202:205], v[110:113]
	v_mfma_f32_16x16x32_bf16 v[106:109], v[150:153], v[202:205], v[106:109]
	s_waitcnt lgkmcnt(1)
	v_mfma_f32_16x16x32_bf16 v[102:105], v[136:139], v[210:213], v[102:105]
	v_mfma_f32_16x16x32_bf16 v[98:101], v[150:153], v[210:213], v[98:101]
	v_mfma_f32_16x16x32_bf16 v[128:131], v[146:149], v[178:181], v[128:131]
	v_mfma_f32_16x16x32_bf16 v[124:127], v[154:157], v[178:181], v[124:127]
	v_mfma_f32_16x16x32_bf16 v[120:123], v[146:149], v[186:189], v[120:123]
	v_mfma_f32_16x16x32_bf16 v[116:119], v[154:157], v[186:189], v[116:119]
	v_mfma_f32_16x16x32_bf16 v[110:113], v[146:149], v[206:209], v[110:113]
	v_mfma_f32_16x16x32_bf16 v[106:109], v[154:157], v[206:209], v[106:109]
	s_waitcnt lgkmcnt(0)
	v_mfma_f32_16x16x32_bf16 v[102:105], v[146:149], v[214:217], v[102:105]
	v_mfma_f32_16x16x32_bf16 v[98:101], v[154:157], v[214:217], v[98:101]
	s_setprio 0
	s_setprio 1
	v_mfma_f32_16x16x32_bf16 v[94:97], v[158:161], v[174:177], v[94:97]
	v_mfma_f32_16x16x32_bf16 v[90:93], v[166:169], v[174:177], v[90:93]
	v_mfma_f32_16x16x32_bf16 v[86:89], v[158:161], v[182:185], v[86:89]
	v_mfma_f32_16x16x32_bf16 v[82:85], v[166:169], v[182:185], v[82:85]
	v_mfma_f32_16x16x32_bf16 v[78:81], v[158:161], v[202:205], v[78:81]
	v_mfma_f32_16x16x32_bf16 v[74:77], v[166:169], v[202:205], v[74:77]
	v_mfma_f32_16x16x32_bf16 v[70:73], v[158:161], v[210:213], v[70:73]
	v_mfma_f32_16x16x32_bf16 v[66:69], v[166:169], v[210:213], v[66:69]
	v_mfma_f32_16x16x32_bf16 v[94:97], v[162:165], v[178:181], v[94:97]
	v_mfma_f32_16x16x32_bf16 v[90:93], v[170:173], v[178:181], v[90:93]
	v_mfma_f32_16x16x32_bf16 v[86:89], v[162:165], v[186:189], v[86:89]
	v_mfma_f32_16x16x32_bf16 v[82:85], v[170:173], v[186:189], v[82:85]
	v_mfma_f32_16x16x32_bf16 v[78:81], v[162:165], v[206:209], v[78:81]
	v_mfma_f32_16x16x32_bf16 v[74:77], v[170:173], v[206:209], v[74:77]
	v_mfma_f32_16x16x32_bf16 v[70:73], v[162:165], v[214:217], v[70:73]
	v_mfma_f32_16x16x32_bf16 v[66:69], v[170:173], v[214:217], v[66:69]
	s_setprio 0
	s_barrier
	ds_read_b128 v[174:177], v144 offset:49152
	ds_read_b128 v[178:181], v144 offset:50176
	ds_read_b128 v[182:185], v144 offset:51200
	ds_read_b128 v[186:189], v144 offset:52224
	ds_read_b128 v[202:205], v144 offset:53248
	ds_read_b128 v[206:209], v144 offset:54272
	ds_read_b128 v[210:213], v144 offset:55296
	ds_read_b128 v[214:217], v144 offset:56320
	s_add_u32 s18, s15, 0x180
	s_addc_u32 s19, s23, 0
	s_mov_b32 m0, s30
	s_nop 0
	global_load_lds_dwordx4 v140, s[18:19]
	s_nop 0
	s_mov_b32 m0, s55
	s_nop 0
	global_load_lds_dwordx4 v142, s[18:19]
	s_add_u32 s18, s15, 0x40180
	s_addc_u32 s19, s23, 0
	s_mov_b32 m0, s58
	s_nop 0
	global_load_lds_dwordx4 v140, s[18:19]
	s_nop 0
	s_mov_b32 m0, s59
	s_nop 0
	global_load_lds_dwordx4 v142, s[18:19]
	s_nop 0
	s_mov_b32 m0, s56
	s_nop 0
	global_load_lds_dwordx4 v65, s[16:17]
	s_nop 0
	s_mov_b32 m0, s57
	s_nop 0
	global_load_lds_dwordx4 v141, s[16:17]
	s_waitcnt vmcnt(8)
	s_waitcnt lgkmcnt(0)
	s_barrier
	s_setprio 1
	s_waitcnt lgkmcnt(0)
	v_mfma_f32_16x16x32_bf16 v[60:63], v[136:139], v[174:177], v[60:63]
	v_mfma_f32_16x16x32_bf16 v[56:59], v[150:153], v[174:177], v[56:59]
	s_waitcnt lgkmcnt(5)
	v_mfma_f32_16x16x32_bf16 v[52:55], v[136:139], v[182:185], v[52:55]
	v_mfma_f32_16x16x32_bf16 v[48:51], v[150:153], v[182:185], v[48:51]
	s_waitcnt lgkmcnt(3)
	v_mfma_f32_16x16x32_bf16 v[44:47], v[136:139], v[202:205], v[44:47]
	v_mfma_f32_16x16x32_bf16 v[40:43], v[150:153], v[202:205], v[40:43]
	s_waitcnt lgkmcnt(1)
	v_mfma_f32_16x16x32_bf16 v[36:39], v[136:139], v[210:213], v[36:39]
	v_mfma_f32_16x16x32_bf16 v[32:35], v[150:153], v[210:213], v[32:35]
	v_mfma_f32_16x16x32_bf16 v[60:63], v[146:149], v[178:181], v[60:63]
	v_mfma_f32_16x16x32_bf16 v[56:59], v[154:157], v[178:181], v[56:59]
	v_mfma_f32_16x16x32_bf16 v[52:55], v[146:149], v[186:189], v[52:55]
	v_mfma_f32_16x16x32_bf16 v[48:51], v[154:157], v[186:189], v[48:51]
	v_mfma_f32_16x16x32_bf16 v[44:47], v[146:149], v[206:209], v[44:47]
	v_mfma_f32_16x16x32_bf16 v[40:43], v[154:157], v[206:209], v[40:43]
	s_waitcnt lgkmcnt(0)
	v_mfma_f32_16x16x32_bf16 v[36:39], v[146:149], v[214:217], v[36:39]
	v_mfma_f32_16x16x32_bf16 v[32:35], v[154:157], v[214:217], v[32:35]
	s_setprio 0
	s_setprio 1
	v_mfma_f32_16x16x32_bf16 v[28:31], v[158:161], v[174:177], v[28:31]
	v_mfma_f32_16x16x32_bf16 v[24:27], v[166:169], v[174:177], v[24:27]
	v_mfma_f32_16x16x32_bf16 v[20:23], v[158:161], v[182:185], v[20:23]
	v_mfma_f32_16x16x32_bf16 v[16:19], v[166:169], v[182:185], v[16:19]
	v_mfma_f32_16x16x32_bf16 v[12:15], v[158:161], v[202:205], v[12:15]
	v_mfma_f32_16x16x32_bf16 v[8:11], v[166:169], v[202:205], v[8:11]
	v_mfma_f32_16x16x32_bf16 v[4:7], v[158:161], v[210:213], v[4:7]
	v_mfma_f32_16x16x32_bf16 v[0:3], v[166:169], v[210:213], v[0:3]
	v_mfma_f32_16x16x32_bf16 v[28:31], v[162:165], v[178:181], v[28:31]
	v_mfma_f32_16x16x32_bf16 v[24:27], v[170:173], v[178:181], v[24:27]
	v_mfma_f32_16x16x32_bf16 v[20:23], v[162:165], v[186:189], v[20:23]
	v_mfma_f32_16x16x32_bf16 v[16:19], v[170:173], v[186:189], v[16:19]
	v_mfma_f32_16x16x32_bf16 v[12:15], v[162:165], v[206:209], v[12:15]
	v_mfma_f32_16x16x32_bf16 v[8:11], v[170:173], v[206:209], v[8:11]
	v_mfma_f32_16x16x32_bf16 v[4:7], v[162:165], v[214:217], v[4:7]
	v_mfma_f32_16x16x32_bf16 v[0:3], v[170:173], v[214:217], v[0:3]
	s_setprio 0
	s_barrier
	s_add_i32 s13, s13, 2
	s_add_u32 s2, s2, 0x100
	s_addc_u32 s3, s3, 0
	s_cmp_lt_u32 s13, 12
	s_cbranch_scc1 .LBB0_627
	s_ashr_i32 s15, s14, 31
	s_ashr_i32 s13, s12, 31
	ds_read_b128 v[136:139], v114
	ds_read_b128 v[146:149], v114 offset:1024
	ds_read_b128 v[150:153], v114 offset:2048
	ds_read_b128 v[154:157], v114 offset:3072
	ds_read_b128 v[158:161], v133
	ds_read_b128 v[162:165], v133 offset:1024
	ds_read_b128 v[166:169], v133 offset:2048
	ds_read_b128 v[170:173], v133 offset:3072
	s_lshl_b64 s[2:3], s[14:15], 19
	s_lshl_b64 s[18:19], s[12:13], 19
	s_add_u32 s16, s42, s2
	s_addc_u32 s17, s43, s3
	s_add_u32 s18, s44, s18
	s_addc_u32 s19, s45, s19
	s_and_b64 s[2:3], s[34:35], exec
	s_cselect_b32 s36, s16, s24
	s_cselect_b32 s37, s17, s25
	s_add_u32 s2, s36, 0x80
	s_addc_u32 s3, s37, 0
	s_and_b64 s[38:39], s[34:35], exec
	s_cselect_b32 s27, s19, s27
	s_cselect_b32 s26, s18, s26
	ds_read_b128 v[174:177], v144
	ds_read_b128 v[178:181], v144 offset:1024
	ds_read_b128 v[182:185], v144 offset:2048
	ds_read_b128 v[186:189], v144 offset:3072
	ds_read_b128 v[202:205], v144 offset:4096
	ds_read_b128 v[206:209], v144 offset:5120
	ds_read_b128 v[210:213], v144 offset:6144
	ds_read_b128 v[214:217], v144 offset:7168
	s_add_u32 s24, s24, 0x40780
	s_addc_u32 s25, s25, 0
	s_mov_b32 m0, s60
	s_nop 0
	global_load_lds_dwordx4 v65, s[24:25]
	s_nop 0
	s_mov_b32 m0, s61
	s_nop 0
	global_load_lds_dwordx4 v141, s[24:25]
	s_waitcnt vmcnt(8)
	s_waitcnt lgkmcnt(0)
	s_barrier
	s_setprio 1
	s_waitcnt lgkmcnt(0)
	v_mfma_f32_16x16x32_bf16 v[128:131], v[136:139], v[174:177], v[128:131]
	v_mfma_f32_16x16x32_bf16 v[124:127], v[150:153], v[174:177], v[124:127]
	s_waitcnt lgkmcnt(3)
	v_mfma_f32_16x16x32_bf16 v[110:113], v[136:139], v[202:205], v[110:113]
	v_mfma_f32_16x16x32_bf16 v[106:109], v[150:153], v[202:205], v[106:109]
	v_mfma_f32_16x16x32_bf16 v[128:131], v[146:149], v[178:181], v[128:131]
	v_mfma_f32_16x16x32_bf16 v[124:127], v[154:157], v[178:181], v[124:127]
	v_mfma_f32_16x16x32_bf16 v[120:123], v[136:139], v[182:185], v[120:123]
	v_mfma_f32_16x16x32_bf16 v[116:119], v[150:153], v[182:185], v[116:119]
	s_waitcnt lgkmcnt(2)
	v_mfma_f32_16x16x32_bf16 v[110:113], v[146:149], v[206:209], v[110:113]
	v_mfma_f32_16x16x32_bf16 v[106:109], v[154:157], v[206:209], v[106:109]
	s_waitcnt lgkmcnt(1)
	v_mfma_f32_16x16x32_bf16 v[102:105], v[136:139], v[210:213], v[102:105]
	v_mfma_f32_16x16x32_bf16 v[98:101], v[150:153], v[210:213], v[98:101]
	v_mfma_f32_16x16x32_bf16 v[218:221], v[146:149], v[186:189], v[120:123]
	v_mfma_f32_16x16x32_bf16 v[222:225], v[154:157], v[186:189], v[116:119]
	s_waitcnt lgkmcnt(0)
	v_mfma_f32_16x16x32_bf16 v[226:229], v[146:149], v[214:217], v[102:105]
	v_mfma_f32_16x16x32_bf16 v[230:233], v[154:157], v[214:217], v[98:101]
	s_setprio 0
	s_setprio 1
	v_mfma_f32_16x16x32_bf16 v[94:97], v[158:161], v[174:177], v[94:97]
	v_mfma_f32_16x16x32_bf16 v[90:93], v[166:169], v[174:177], v[90:93]
	v_mfma_f32_16x16x32_bf16 v[78:81], v[158:161], v[202:205], v[78:81]
	v_mfma_f32_16x16x32_bf16 v[74:77], v[166:169], v[202:205], v[74:77]
	v_mfma_f32_16x16x32_bf16 v[94:97], v[162:165], v[178:181], v[94:97]
	v_mfma_f32_16x16x32_bf16 v[90:93], v[170:173], v[178:181], v[90:93]
	v_mfma_f32_16x16x32_bf16 v[86:89], v[158:161], v[182:185], v[86:89]
	v_mfma_f32_16x16x32_bf16 v[82:85], v[166:169], v[182:185], v[82:85]
	v_mfma_f32_16x16x32_bf16 v[78:81], v[162:165], v[206:209], v[78:81]
	v_mfma_f32_16x16x32_bf16 v[74:77], v[170:173], v[206:209], v[74:77]
	v_mfma_f32_16x16x32_bf16 v[70:73], v[158:161], v[210:213], v[70:73]
	v_mfma_f32_16x16x32_bf16 v[66:69], v[166:169], v[210:213], v[66:69]
	v_mfma_f32_16x16x32_bf16 v[174:177], v[162:165], v[186:189], v[86:89]
	v_mfma_f32_16x16x32_bf16 v[178:181], v[170:173], v[186:189], v[82:85]
	v_mfma_f32_16x16x32_bf16 v[182:185], v[162:165], v[214:217], v[70:73]
	v_mfma_f32_16x16x32_bf16 v[186:189], v[170:173], v[214:217], v[66:69]
	s_setprio 0
	s_barrier
	s_nop 1
	ds_read_b128 v[66:69], v144 offset:16384
	ds_read_b128 v[70:73], v144 offset:17408
	ds_read_b128 v[82:85], v144 offset:18432
	ds_read_b128 v[86:89], v144 offset:19456
	ds_read_b128 v[98:101], v144 offset:20480
	ds_read_b128 v[102:105], v144 offset:21504
	ds_read_b128 v[116:119], v144 offset:22528
	ds_read_b128 v[120:123], v144 offset:23552
	s_mov_b64 exec, s[100:101]
	s_mov_b32 m0, s48
	s_nop 0
	global_load_lds_dwordx4 v140, s[26:27]
	s_mov_b64 exec, -1
	s_add_u32 s24, s26, 0x40000
	s_mov_b64 exec, s[100:101]
	s_mov_b32 m0, s49
	s_nop 0
	global_load_lds_dwordx4 v142, s[26:27]
	s_mov_b64 exec, -1
	s_addc_u32 s25, s27, 0
	s_mov_b64 exec, s[100:101]
	s_mov_b32 m0, s50
	s_nop 0
	global_load_lds_dwordx4 v140, s[24:25]
	s_mov_b64 exec, -1
	s_nop 0
	s_mov_b64 exec, s[100:101]
	s_mov_b32 m0, s51
	s_nop 0
	global_load_lds_dwordx4 v142, s[24:25]
	s_mov_b64 exec, -1
	s_nop 0
	s_mov_b64 exec, s[100:101]
	s_mov_b32 m0, s47
	s_nop 0
	global_load_lds_dwordx4 v65, s[36:37]
	s_mov_b64 exec, -1
	s_nop 0
	s_mov_b64 exec, s[100:101]
	s_mov_b32 m0, s52
	s_nop 0
	global_load_lds_dwordx4 v141, s[36:37]
	s_mov_b64 exec, -1
	s_waitcnt vmcnt(8)
	s_waitcnt lgkmcnt(0)
	s_barrier
	s_setprio 1
	s_waitcnt lgkmcnt(0)
	v_mfma_f32_16x16x32_bf16 v[60:63], v[136:139], v[66:69], v[60:63]
	v_mfma_f32_16x16x32_bf16 v[56:59], v[150:153], v[66:69], v[56:59]
	s_waitcnt lgkmcnt(3)
	v_mfma_f32_16x16x32_bf16 v[44:47], v[136:139], v[98:101], v[44:47]
	v_mfma_f32_16x16x32_bf16 v[40:43], v[150:153], v[98:101], v[40:43]
	v_mfma_f32_16x16x32_bf16 v[60:63], v[146:149], v[70:73], v[60:63]
	v_mfma_f32_16x16x32_bf16 v[56:59], v[154:157], v[70:73], v[56:59]
	v_mfma_f32_16x16x32_bf16 v[52:55], v[136:139], v[82:85], v[52:55]
	v_mfma_f32_16x16x32_bf16 v[48:51], v[150:153], v[82:85], v[48:51]
	s_waitcnt lgkmcnt(2)
	v_mfma_f32_16x16x32_bf16 v[44:47], v[146:149], v[102:105], v[44:47]
	v_mfma_f32_16x16x32_bf16 v[40:43], v[154:157], v[102:105], v[40:43]
	s_waitcnt lgkmcnt(1)
	v_mfma_f32_16x16x32_bf16 v[36:39], v[136:139], v[116:119], v[36:39]
	v_mfma_f32_16x16x32_bf16 v[32:35], v[150:153], v[116:119], v[32:35]
	v_mfma_f32_16x16x32_bf16 v[202:205], v[146:149], v[86:89], v[52:55]
	v_mfma_f32_16x16x32_bf16 v[206:209], v[154:157], v[86:89], v[48:51]
	s_waitcnt lgkmcnt(0)
	v_mfma_f32_16x16x32_bf16 v[136:139], v[146:149], v[120:123], v[36:39]
	v_mfma_f32_16x16x32_bf16 v[146:149], v[154:157], v[120:123], v[32:35]
	s_setprio 0
	s_setprio 1
	v_mfma_f32_16x16x32_bf16 v[28:31], v[158:161], v[66:69], v[28:31]
	v_mfma_f32_16x16x32_bf16 v[24:27], v[166:169], v[66:69], v[24:27]
	v_mfma_f32_16x16x32_bf16 v[12:15], v[158:161], v[98:101], v[12:15]
	v_mfma_f32_16x16x32_bf16 v[8:11], v[166:169], v[98:101], v[8:11]
	v_mfma_f32_16x16x32_bf16 v[28:31], v[162:165], v[70:73], v[28:31]
	v_mfma_f32_16x16x32_bf16 v[24:27], v[170:173], v[70:73], v[24:27]
	v_mfma_f32_16x16x32_bf16 v[20:23], v[158:161], v[82:85], v[20:23]
	v_mfma_f32_16x16x32_bf16 v[16:19], v[166:169], v[82:85], v[16:19]
	v_mfma_f32_16x16x32_bf16 v[12:15], v[162:165], v[102:105], v[12:15]
	v_mfma_f32_16x16x32_bf16 v[8:11], v[170:173], v[102:105], v[8:11]
	v_mfma_f32_16x16x32_bf16 v[4:7], v[158:161], v[116:119], v[4:7]
	v_mfma_f32_16x16x32_bf16 v[0:3], v[166:169], v[116:119], v[0:3]
	v_mfma_f32_16x16x32_bf16 v[150:153], v[162:165], v[86:89], v[20:23]
	v_mfma_f32_16x16x32_bf16 v[154:157], v[170:173], v[86:89], v[16:19]
	v_mfma_f32_16x16x32_bf16 v[158:161], v[162:165], v[120:123], v[4:7]
	v_mfma_f32_16x16x32_bf16 v[162:165], v[170:173], v[120:123], v[0:3]
	s_setprio 0
	s_barrier
	s_nop 1
	ds_read_b128 v[0:3], v132
	ds_read_b128 v[4:7], v132 offset:1024
	ds_read_b128 v[166:169], v132 offset:2048
	ds_read_b128 v[170:173], v132 offset:3072
	ds_read_b128 v[210:213], v134
	ds_read_b128 v[214:217], v134 offset:1024
	ds_read_b128 v[244:247], v134 offset:2048
	ds_read_b128 v[132:135], v134 offset:3072
	ds_read_b128 v[16:19], v144 offset:32768
	ds_read_b128 v[20:23], v144 offset:33792
	ds_read_b128 v[32:35], v144 offset:34816
	ds_read_b128 v[36:39], v144 offset:35840
	ds_read_b128 v[48:51], v144 offset:36864
	ds_read_b128 v[52:55], v144 offset:37888
	ds_read_b128 v[248:251], v144 offset:38912
	ds_read_b128 v[194:197], v144 offset:39936
	s_add_u32 s24, s36, 0x40000
	s_addc_u32 s25, s37, 0
	s_mov_b64 exec, s[100:101]
	s_mov_b32 m0, s53
	s_nop 0
	global_load_lds_dwordx4 v65, s[24:25]
	s_mov_b64 exec, -1
	s_nop 0
	s_mov_b64 exec, s[100:101]
	s_mov_b32 m0, s54
	s_nop 0
	global_load_lds_dwordx4 v141, s[24:25]
	s_mov_b64 exec, -1
	s_waitcnt vmcnt(8)
	s_waitcnt lgkmcnt(0)
	s_barrier
	s_setprio 1
	s_waitcnt lgkmcnt(0)
	v_mfma_f32_16x16x32_bf16 v[66:69], v[0:3], v[16:19], v[128:131]
	s_waitcnt lgkmcnt(6)
	v_mfma_f32_16x16x32_bf16 v[116:119], v[4:7], v[20:23], v[66:69]
	v_mfma_f32_16x16x32_bf16 v[66:69], v[166:169], v[16:19], v[124:127]
	v_mfma_f32_16x16x32_bf16 v[120:123], v[170:173], v[20:23], v[66:69]
	s_waitcnt lgkmcnt(5)
	v_mfma_f32_16x16x32_bf16 v[66:69], v[0:3], v[32:35], v[218:221]
	s_waitcnt lgkmcnt(4)
	v_mfma_f32_16x16x32_bf16 v[98:101], v[4:7], v[36:39], v[66:69]
	v_mfma_f32_16x16x32_bf16 v[66:69], v[166:169], v[32:35], v[222:225]
	v_mfma_f32_16x16x32_bf16 v[102:105], v[170:173], v[36:39], v[66:69]
	s_waitcnt lgkmcnt(3)
	v_mfma_f32_16x16x32_bf16 v[66:69], v[0:3], v[48:51], v[110:113]
	s_waitcnt lgkmcnt(2)
	v_mfma_f32_16x16x32_bf16 v[82:85], v[4:7], v[52:55], v[66:69]
	v_mfma_f32_16x16x32_bf16 v[66:69], v[166:169], v[48:51], v[106:109]
	v_mfma_f32_16x16x32_bf16 v[86:89], v[170:173], v[52:55], v[66:69]
	s_waitcnt lgkmcnt(1)
	v_mfma_f32_16x16x32_bf16 v[66:69], v[0:3], v[248:251], v[226:229]
	v_mfma_f32_16x16x32_bf16 v[70:73], v[166:169], v[248:251], v[230:233]
	s_waitcnt lgkmcnt(0)
	v_mfma_f32_16x16x32_bf16 v[66:69], v[4:7], v[194:197], v[66:69]
	v_mfma_f32_16x16x32_bf16 v[70:73], v[170:173], v[194:197], v[70:73]
	s_setprio 0
	s_setprio 1
	v_mfma_f32_16x16x32_bf16 v[94:97], v[210:213], v[16:19], v[94:97]
	v_mfma_f32_16x16x32_bf16 v[16:19], v[244:247], v[16:19], v[90:93]
	v_mfma_f32_16x16x32_bf16 v[128:131], v[132:135], v[20:23], v[16:19]
	v_mfma_f32_16x16x32_bf16 v[16:19], v[210:213], v[32:35], v[174:177]
	v_mfma_f32_16x16x32_bf16 v[106:109], v[214:217], v[36:39], v[16:19]
	v_mfma_f32_16x16x32_bf16 v[16:19], v[244:247], v[32:35], v[178:181]
	v_mfma_f32_16x16x32_bf16 v[110:113], v[132:135], v[36:39], v[16:19]
	v_mfma_f32_16x16x32_bf16 v[16:19], v[210:213], v[48:51], v[78:81]
	v_mfma_f32_16x16x32_bf16 v[90:93], v[214:217], v[52:55], v[16:19]
	v_mfma_f32_16x16x32_bf16 v[16:19], v[244:247], v[48:51], v[74:77]
	v_mfma_f32_16x16x32_bf16 v[124:127], v[214:217], v[20:23], v[94:97]
	v_mfma_f32_16x16x32_bf16 v[94:97], v[132:135], v[52:55], v[16:19]
	v_mfma_f32_16x16x32_bf16 v[16:19], v[210:213], v[248:251], v[182:185]
	v_mfma_f32_16x16x32_bf16 v[74:77], v[214:217], v[194:197], v[16:19]
	v_mfma_f32_16x16x32_bf16 v[16:19], v[244:247], v[248:251], v[186:189]
	v_mfma_f32_16x16x32_bf16 v[78:81], v[132:135], v[194:197], v[16:19]
	s_setprio 0
	s_barrier
	ds_read_b128 v[174:177], v144 offset:49152
	ds_read_b128 v[178:181], v144 offset:50176
	ds_read_b128 v[182:185], v144 offset:51200
	ds_read_b128 v[186:189], v144 offset:52224
	ds_read_b128 v[194:197], v144 offset:53248
	ds_read_b128 v[218:221], v144 offset:54272
	ds_read_b128 v[222:225], v144 offset:55296
	ds_read_b128 v[226:229], v144 offset:56320
	s_add_u32 s24, s26, 0x80
	s_addc_u32 s25, s27, 0
	s_mov_b64 exec, s[100:101]
	s_mov_b32 m0, s30
	s_nop 0
	global_load_lds_dwordx4 v140, s[24:25]
	s_mov_b64 exec, -1
	s_nop 0
	s_mov_b64 exec, s[100:101]
	s_mov_b32 m0, s55
	s_nop 0
	global_load_lds_dwordx4 v142, s[24:25]
	s_mov_b64 exec, -1
	s_add_u32 s24, s26, 0x40080
	s_addc_u32 s25, s27, 0
	s_mov_b64 exec, s[100:101]
	s_mov_b32 m0, s58
	s_nop 0
	global_load_lds_dwordx4 v140, s[24:25]
	s_mov_b64 exec, -1
	s_nop 0
	s_mov_b64 exec, s[100:101]
	s_mov_b32 m0, s59
	s_nop 0
	global_load_lds_dwordx4 v142, s[24:25]
	s_mov_b64 exec, -1
	s_nop 0
	s_mov_b64 exec, s[100:101]
	s_mov_b32 m0, s56
	s_nop 0
	global_load_lds_dwordx4 v65, s[2:3]
	s_mov_b64 exec, -1
	s_nop 0
	s_mov_b64 exec, s[100:101]
	s_mov_b32 m0, s57
	s_nop 0
	global_load_lds_dwordx4 v141, s[2:3]
	s_mov_b64 exec, -1
	s_waitcnt vmcnt(8)
	s_waitcnt lgkmcnt(0)
	s_barrier
	s_setprio 1
	s_waitcnt lgkmcnt(0)
	v_mfma_f32_16x16x32_bf16 v[16:19], v[0:3], v[174:177], v[60:63]
	s_waitcnt lgkmcnt(6)
	v_mfma_f32_16x16x32_bf16 v[48:51], v[4:7], v[178:181], v[16:19]
	v_mfma_f32_16x16x32_bf16 v[16:19], v[166:169], v[174:177], v[56:59]
	v_mfma_f32_16x16x32_bf16 v[52:55], v[170:173], v[178:181], v[16:19]
	s_waitcnt lgkmcnt(5)
	v_mfma_f32_16x16x32_bf16 v[16:19], v[0:3], v[182:185], v[202:205]
	s_waitcnt lgkmcnt(4)
	v_mfma_f32_16x16x32_bf16 v[32:35], v[4:7], v[186:189], v[16:19]
	v_mfma_f32_16x16x32_bf16 v[16:19], v[166:169], v[182:185], v[206:209]
	v_mfma_f32_16x16x32_bf16 v[36:39], v[170:173], v[186:189], v[16:19]
	s_waitcnt lgkmcnt(3)
	v_mfma_f32_16x16x32_bf16 v[16:19], v[0:3], v[194:197], v[44:47]
	s_waitcnt lgkmcnt(1)
	v_mfma_f32_16x16x32_bf16 v[0:3], v[0:3], v[222:225], v[136:139]
	v_mfma_f32_16x16x32_bf16 v[16:19], v[4:7], v[218:221], v[16:19]
	v_mfma_f32_16x16x32_bf16 v[20:23], v[166:169], v[194:197], v[40:43]
	s_waitcnt lgkmcnt(0)
	v_mfma_f32_16x16x32_bf16 v[0:3], v[4:7], v[226:229], v[0:3]
	v_mfma_f32_16x16x32_bf16 v[4:7], v[166:169], v[222:225], v[146:149]
	v_mfma_f32_16x16x32_bf16 v[20:23], v[170:173], v[218:221], v[20:23]
	v_mfma_f32_16x16x32_bf16 v[4:7], v[170:173], v[226:229], v[4:7]
	s_setprio 0
	s_setprio 1
	v_mfma_f32_16x16x32_bf16 v[24:27], v[244:247], v[174:177], v[24:27]
	v_mfma_f32_16x16x32_bf16 v[60:63], v[132:135], v[178:181], v[24:27]
	v_mfma_f32_16x16x32_bf16 v[24:27], v[210:213], v[182:185], v[150:153]
	v_mfma_f32_16x16x32_bf16 v[28:31], v[210:213], v[174:177], v[28:31]
	v_mfma_f32_16x16x32_bf16 v[40:43], v[214:217], v[186:189], v[24:27]
	v_mfma_f32_16x16x32_bf16 v[24:27], v[244:247], v[182:185], v[154:157]
	v_mfma_f32_16x16x32_bf16 v[12:15], v[210:213], v[194:197], v[12:15]
	v_mfma_f32_16x16x32_bf16 v[8:11], v[244:247], v[194:197], v[8:11]
	v_mfma_f32_16x16x32_bf16 v[56:59], v[214:217], v[178:181], v[28:31]
	v_mfma_f32_16x16x32_bf16 v[44:47], v[132:135], v[186:189], v[24:27]
	v_mfma_f32_16x16x32_bf16 v[24:27], v[214:217], v[218:221], v[12:15]
	v_mfma_f32_16x16x32_bf16 v[28:31], v[132:135], v[218:221], v[8:11]
	v_mfma_f32_16x16x32_bf16 v[8:11], v[210:213], v[222:225], v[158:161]
	v_mfma_f32_16x16x32_bf16 v[12:15], v[244:247], v[222:225], v[162:165]
	v_mfma_f32_16x16x32_bf16 v[8:11], v[214:217], v[226:229], v[8:11]
	v_mfma_f32_16x16x32_bf16 v[12:15], v[132:135], v[226:229], v[12:15]
	s_setprio 0
	s_barrier
	s_andn2_b64 vcc, exec, s[10:11]
	s_cbranch_vccnz .LBB0_630
	s_barrier

.LBB0_1108:
	s_add_i32 s53, s53, 1
	v_readlane_b32 s0, v254, 38
	s_mul_i32 s0, s53, s0
	s_mul_hi_u32 s1, s53, s70
	s_add_i32 s1, s1, s0
	s_mul_i32 s0, s53, s70
	v_readlane_b32 s2, v255, 0
	s_add_u32 s2, s0, s2
	s_addc_u32 s3, s1, s41
	v_mov_b64_e32 v[0:1], s[30:31]
	v_cmp_ge_i64_e32 vcc, s[2:3], v[0:1]
	v_cmp_lt_i64_e64 s[0:1], s[2:3], v[0:1]
	s_nop 3
	s_cmp_lg_u64 s[0:1], 0
	s_cselect_b64 s[100:101], -1, 1
	s_cbranch_vccnz .LBB0_1110
	s_ashr_i32 s3, s2, 31
	s_lshr_b32 s3, s3, 29
	s_add_i32 s3, s2, s3
	s_ashr_i32 s14, s3, 3
	s_and_b32 s3, s3, -8
	s_sub_i32 s2, s2, s3
	s_cmp_lt_i32 s2, 0
	s_cselect_b32 s3, s42, s40
	s_mul_i32 s2, s3, s2
	s_add_i32 s2, s2, s14
	s_ashr_i32 s3, s2, 31
	s_lshr_b32 s3, s3, 27
	s_add_i32 s3, s2, s3
	s_ashr_i32 s14, s3, 5
	s_lshl_b32 s15, s14, 3
	s_sub_i32 s14, s39, s15
	s_min_i32 s16, s14, 8
	s_abs_i32 s14, s16
	v_cvt_f32_u32_e32 v0, s14
	s_sub_i32 s18, 0, s14
	s_andn2_b32 s3, s3, 31
	s_sub_i32 s2, s2, s3
	v_rcp_iflag_f32_e32 v0, v0
	s_abs_i32 s3, s2
	s_xor_b32 s17, s2, s16
	s_ashr_i32 s17, s17, 31
	v_mul_f32_e32 v0, 0x4f7ffffe, v0
	v_cvt_u32_f32_e32 v0, v0
	s_nop 0
	v_readfirstlane_b32 s19, v0
	s_mul_i32 s18, s18, s19
	s_mul_hi_u32 s18, s19, s18
	s_add_i32 s19, s19, s18
	s_mul_hi_u32 s18, s3, s19
	s_mul_i32 s19, s18, s14
	s_sub_i32 s3, s3, s19
	s_add_i32 s20, s18, 1
	s_sub_i32 s19, s3, s14
	s_cmp_ge_u32 s3, s14
	s_cselect_b32 s18, s20, s18
	s_cselect_b32 s3, s19, s3
	s_add_i32 s19, s18, 1
	s_cmp_ge_u32 s3, s14
	s_cselect_b32 s3, s19, s18
	s_xor_b32 s3, s3, s17
	s_sub_i32 s14, s3, s17
	s_mul_i32 s3, s14, s16
	s_sub_i32 s2, s2, s3
	s_add_i32 s15, s2, s15
	s_ashr_i32 s16, s15, 4
	s_and_b64 s[2:3], s[4:5], exec
	s_cselect_b32 s2, s16, 0
	s_add_i32 s16, s2, s15

.LBB0_1111:
	s_add_u32 s66, s26, s2
	s_addc_u32 s67, s27, s3
	s_nop 0
	v_add_u32_e32 v132, 0x10000, v204
	v_add_u32_e32 v134, 0x14000, v204
	s_add_u32 s20, s66, 0x100
	ds_read_b128 v[136:139], v132
	ds_read_b128 v[140:143], v132 offset:1024
	ds_read_b128 v[144:147], v132 offset:2048
	ds_read_b128 v[148:151], v132 offset:3072
	ds_read_b128 v[152:155], v134
	ds_read_b128 v[156:159], v134 offset:1024
	ds_read_b128 v[160:163], v134 offset:2048
	ds_read_b128 v[164:167], v134 offset:3072
	s_addc_u32 s21, s67, 0
	s_add_u32 s18, s66, 0x180
	s_addc_u32 s19, s67, 0
	s_add_u32 s17, s24, s2
	s_addc_u32 s33, s25, s3
	s_add_u32 s34, s17, 0x100
	s_addc_u32 s35, s33, 0
	ds_read_b128 v[168:171], v205
	ds_read_b128 v[172:175], v205 offset:1024
	ds_read_b128 v[176:179], v205 offset:2048
	ds_read_b128 v[180:183], v205 offset:3072
	ds_read_b128 v[184:187], v205 offset:4096
	ds_read_b128 v[188:191], v205 offset:5120
	ds_read_b128 v[194:197], v205 offset:6144
	ds_read_b128 v[198:201], v205 offset:7168
	s_add_u32 s64, s66, 0x40080
	s_addc_u32 s65, s67, 0
	s_mov_b32 m0, s62
	s_nop 0
	global_load_lds_dwordx4 v65, s[64:65]
	s_nop 0
	s_mov_b32 m0, s63
	s_nop 0
	global_load_lds_dwordx4 v202, s[64:65]
	s_waitcnt vmcnt(8)
	s_waitcnt lgkmcnt(0)
	s_barrier
	s_setprio 1
	s_waitcnt lgkmcnt(0)
	v_mfma_f32_16x16x32_bf16 v[128:131], v[136:139], v[168:171], v[128:131]
	v_mfma_f32_16x16x32_bf16 v[124:127], v[144:147], v[168:171], v[124:127]
	v_mfma_f32_16x16x32_bf16 v[120:123], v[136:139], v[176:179], v[120:123]
	v_mfma_f32_16x16x32_bf16 v[116:119], v[144:147], v[176:179], v[116:119]
	v_mfma_f32_16x16x32_bf16 v[110:113], v[136:139], v[184:187], v[110:113]
	v_mfma_f32_16x16x32_bf16 v[106:109], v[144:147], v[184:187], v[106:109]
	v_mfma_f32_16x16x32_bf16 v[102:105], v[136:139], v[194:197], v[102:105]
	v_mfma_f32_16x16x32_bf16 v[98:101], v[144:147], v[194:197], v[98:101]
	v_mfma_f32_16x16x32_bf16 v[128:131], v[140:143], v[172:175], v[128:131]
	v_mfma_f32_16x16x32_bf16 v[124:127], v[148:151], v[172:175], v[124:127]
	v_mfma_f32_16x16x32_bf16 v[120:123], v[140:143], v[180:183], v[120:123]
	v_mfma_f32_16x16x32_bf16 v[116:119], v[148:151], v[180:183], v[116:119]
	v_mfma_f32_16x16x32_bf16 v[110:113], v[140:143], v[188:191], v[110:113]
	v_mfma_f32_16x16x32_bf16 v[106:109], v[148:151], v[188:191], v[106:109]
	v_mfma_f32_16x16x32_bf16 v[102:105], v[140:143], v[198:201], v[102:105]
	v_mfma_f32_16x16x32_bf16 v[98:101], v[148:151], v[198:201], v[98:101]
	s_setprio 0
	s_setprio 1
	v_mfma_f32_16x16x32_bf16 v[94:97], v[152:155], v[168:171], v[94:97]
	v_mfma_f32_16x16x32_bf16 v[90:93], v[160:163], v[168:171], v[90:93]
	v_mfma_f32_16x16x32_bf16 v[86:89], v[152:155], v[176:179], v[86:89]
	v_mfma_f32_16x16x32_bf16 v[82:85], v[160:163], v[176:179], v[82:85]
	v_mfma_f32_16x16x32_bf16 v[78:81], v[152:155], v[184:187], v[78:81]
	v_mfma_f32_16x16x32_bf16 v[74:77], v[160:163], v[184:187], v[74:77]
	v_mfma_f32_16x16x32_bf16 v[70:73], v[152:155], v[194:197], v[70:73]
	v_mfma_f32_16x16x32_bf16 v[66:69], v[160:163], v[194:197], v[66:69]
	v_mfma_f32_16x16x32_bf16 v[94:97], v[156:159], v[172:175], v[94:97]
	v_mfma_f32_16x16x32_bf16 v[90:93], v[164:167], v[172:175], v[90:93]
	v_mfma_f32_16x16x32_bf16 v[86:89], v[156:159], v[180:183], v[86:89]
	v_mfma_f32_16x16x32_bf16 v[82:85], v[164:167], v[180:183], v[82:85]
	v_mfma_f32_16x16x32_bf16 v[78:81], v[156:159], v[188:191], v[78:81]
	v_mfma_f32_16x16x32_bf16 v[74:77], v[164:167], v[188:191], v[74:77]
	v_mfma_f32_16x16x32_bf16 v[70:73], v[156:159], v[198:201], v[70:73]
	v_mfma_f32_16x16x32_bf16 v[66:69], v[164:167], v[198:201], v[66:69]
	s_setprio 0
	s_barrier
	ds_read_b128 v[168:171], v205 offset:16384
	ds_read_b128 v[172:175], v205 offset:17408
	ds_read_b128 v[176:179], v205 offset:18432
	ds_read_b128 v[180:183], v205 offset:19456
	ds_read_b128 v[184:187], v205 offset:20480
	ds_read_b128 v[188:191], v205 offset:21504
	ds_read_b128 v[194:197], v205 offset:22528
	ds_read_b128 v[198:201], v205 offset:23552
	s_mov_b32 m0, s44
	s_nop 0
	global_load_lds_dwordx4 v114, s[34:35]
	s_nop 0
	s_mov_b32 m0, s45
	s_nop 0
	global_load_lds_dwordx4 v203, s[34:35]
	s_add_u32 s34, s17, 0x40100
	s_addc_u32 s35, s33, 0
	s_mov_b32 m0, s46
	s_nop 0
	global_load_lds_dwordx4 v114, s[34:35]
	s_nop 0
	s_mov_b32 m0, s47
	s_nop 0
	global_load_lds_dwordx4 v203, s[34:35]
	s_mov_b32 m0, s43
	s_nop 0
	global_load_lds_dwordx4 v65, s[20:21]
	s_nop 0
	s_mov_b32 m0, s48
	s_nop 0
	global_load_lds_dwordx4 v202, s[20:21]
	s_waitcnt vmcnt(8)
	s_waitcnt lgkmcnt(0)
	s_barrier
	s_setprio 1
	s_waitcnt lgkmcnt(7)
	v_mfma_f32_16x16x32_bf16 v[60:63], v[136:139], v[168:171], v[60:63]
	v_mfma_f32_16x16x32_bf16 v[56:59], v[144:147], v[168:171], v[56:59]
	s_waitcnt lgkmcnt(5)
	v_mfma_f32_16x16x32_bf16 v[52:55], v[136:139], v[176:179], v[52:55]
	v_mfma_f32_16x16x32_bf16 v[48:51], v[144:147], v[176:179], v[48:51]
	s_waitcnt lgkmcnt(3)
	v_mfma_f32_16x16x32_bf16 v[44:47], v[136:139], v[184:187], v[44:47]
	v_mfma_f32_16x16x32_bf16 v[40:43], v[144:147], v[184:187], v[40:43]
	s_waitcnt lgkmcnt(1)
	v_mfma_f32_16x16x32_bf16 v[36:39], v[136:139], v[194:197], v[36:39]
	v_mfma_f32_16x16x32_bf16 v[32:35], v[144:147], v[194:197], v[32:35]
	v_mfma_f32_16x16x32_bf16 v[60:63], v[140:143], v[172:175], v[60:63]
	v_mfma_f32_16x16x32_bf16 v[56:59], v[148:151], v[172:175], v[56:59]
	v_mfma_f32_16x16x32_bf16 v[52:55], v[140:143], v[180:183], v[52:55]
	v_mfma_f32_16x16x32_bf16 v[48:51], v[148:151], v[180:183], v[48:51]
	v_mfma_f32_16x16x32_bf16 v[44:47], v[140:143], v[188:191], v[44:47]
	v_mfma_f32_16x16x32_bf16 v[40:43], v[148:151], v[188:191], v[40:43]
	s_waitcnt lgkmcnt(0)
	v_mfma_f32_16x16x32_bf16 v[36:39], v[140:143], v[198:201], v[36:39]
	v_mfma_f32_16x16x32_bf16 v[32:35], v[148:151], v[198:201], v[32:35]
	s_setprio 0
	s_setprio 1
	v_mfma_f32_16x16x32_bf16 v[28:31], v[152:155], v[168:171], v[28:31]
	v_mfma_f32_16x16x32_bf16 v[24:27], v[160:163], v[168:171], v[24:27]
	v_mfma_f32_16x16x32_bf16 v[20:23], v[152:155], v[176:179], v[20:23]
	v_mfma_f32_16x16x32_bf16 v[16:19], v[160:163], v[176:179], v[16:19]
	v_mfma_f32_16x16x32_bf16 v[12:15], v[152:155], v[184:187], v[12:15]
	v_mfma_f32_16x16x32_bf16 v[8:11], v[160:163], v[184:187], v[8:11]
	v_mfma_f32_16x16x32_bf16 v[4:7], v[152:155], v[194:197], v[4:7]
	v_mfma_f32_16x16x32_bf16 v[0:3], v[160:163], v[194:197], v[0:3]
	v_mfma_f32_16x16x32_bf16 v[28:31], v[156:159], v[172:175], v[28:31]
	v_mfma_f32_16x16x32_bf16 v[24:27], v[164:167], v[172:175], v[24:27]
	v_mfma_f32_16x16x32_bf16 v[20:23], v[156:159], v[180:183], v[20:23]
	v_mfma_f32_16x16x32_bf16 v[16:19], v[164:167], v[180:183], v[16:19]
	v_mfma_f32_16x16x32_bf16 v[12:15], v[156:159], v[188:191], v[12:15]
	v_mfma_f32_16x16x32_bf16 v[8:11], v[164:167], v[188:191], v[8:11]
	v_mfma_f32_16x16x32_bf16 v[4:7], v[156:159], v[198:201], v[4:7]
	v_mfma_f32_16x16x32_bf16 v[0:3], v[164:167], v[198:201], v[0:3]
	s_setprio 0
	s_barrier
	v_add_u32_e32 v133, 0x18000, v204
	v_add_u32_e32 v135, 0x1c000, v204
	ds_read_b128 v[136:139], v133
	ds_read_b128 v[140:143], v133 offset:1024
	ds_read_b128 v[144:147], v133 offset:2048
	ds_read_b128 v[148:151], v133 offset:3072
	ds_read_b128 v[152:155], v135
	ds_read_b128 v[156:159], v135 offset:1024
	ds_read_b128 v[160:163], v135 offset:2048
	ds_read_b128 v[164:167], v135 offset:3072
	ds_read_b128 v[168:171], v205 offset:32768
	ds_read_b128 v[172:175], v205 offset:33792
	ds_read_b128 v[176:179], v205 offset:34816
	ds_read_b128 v[180:183], v205 offset:35840
	ds_read_b128 v[184:187], v205 offset:36864
	ds_read_b128 v[188:191], v205 offset:37888
	ds_read_b128 v[194:197], v205 offset:38912
	ds_read_b128 v[198:201], v205 offset:39936
	s_add_u32 s20, s66, 0x40100
	s_addc_u32 s21, s67, 0
	s_mov_b32 m0, s49
	s_nop 0
	global_load_lds_dwordx4 v65, s[20:21]
	s_nop 0
	s_mov_b32 m0, s50
	s_nop 0
	global_load_lds_dwordx4 v202, s[20:21]
	s_waitcnt vmcnt(8)
	s_waitcnt lgkmcnt(0)
	s_barrier
	s_setprio 1
	s_waitcnt lgkmcnt(7)
	v_mfma_f32_16x16x32_bf16 v[128:131], v[136:139], v[168:171], v[128:131]
	v_mfma_f32_16x16x32_bf16 v[124:127], v[144:147], v[168:171], v[124:127]
	s_waitcnt lgkmcnt(5)
	v_mfma_f32_16x16x32_bf16 v[120:123], v[136:139], v[176:179], v[120:123]
	v_mfma_f32_16x16x32_bf16 v[116:119], v[144:147], v[176:179], v[116:119]
	s_waitcnt lgkmcnt(3)
	v_mfma_f32_16x16x32_bf16 v[110:113], v[136:139], v[184:187], v[110:113]
	v_mfma_f32_16x16x32_bf16 v[106:109], v[144:147], v[184:187], v[106:109]
	s_waitcnt lgkmcnt(1)
	v_mfma_f32_16x16x32_bf16 v[102:105], v[136:139], v[194:197], v[102:105]
	v_mfma_f32_16x16x32_bf16 v[98:101], v[144:147], v[194:197], v[98:101]
	v_mfma_f32_16x16x32_bf16 v[128:131], v[140:143], v[172:175], v[128:131]
	v_mfma_f32_16x16x32_bf16 v[124:127], v[148:151], v[172:175], v[124:127]
	v_mfma_f32_16x16x32_bf16 v[120:123], v[140:143], v[180:183], v[120:123]
	v_mfma_f32_16x16x32_bf16 v[116:119], v[148:151], v[180:183], v[116:119]
	v_mfma_f32_16x16x32_bf16 v[110:113], v[140:143], v[188:191], v[110:113]
	v_mfma_f32_16x16x32_bf16 v[106:109], v[148:151], v[188:191], v[106:109]
	s_waitcnt lgkmcnt(0)
	v_mfma_f32_16x16x32_bf16 v[102:105], v[140:143], v[198:201], v[102:105]
	v_mfma_f32_16x16x32_bf16 v[98:101], v[148:151], v[198:201], v[98:101]
	s_setprio 0
	s_setprio 1
	v_mfma_f32_16x16x32_bf16 v[94:97], v[152:155], v[168:171], v[94:97]
	v_mfma_f32_16x16x32_bf16 v[90:93], v[160:163], v[168:171], v[90:93]
	v_mfma_f32_16x16x32_bf16 v[86:89], v[152:155], v[176:179], v[86:89]
	v_mfma_f32_16x16x32_bf16 v[82:85], v[160:163], v[176:179], v[82:85]
	v_mfma_f32_16x16x32_bf16 v[78:81], v[152:155], v[184:187], v[78:81]
	v_mfma_f32_16x16x32_bf16 v[74:77], v[160:163], v[184:187], v[74:77]
	v_mfma_f32_16x16x32_bf16 v[70:73], v[152:155], v[194:197], v[70:73]
	v_mfma_f32_16x16x32_bf16 v[66:69], v[160:163], v[194:197], v[66:69]
	v_mfma_f32_16x16x32_bf16 v[94:97], v[156:159], v[172:175], v[94:97]
	v_mfma_f32_16x16x32_bf16 v[90:93], v[164:167], v[172:175], v[90:93]
	v_mfma_f32_16x16x32_bf16 v[86:89], v[156:159], v[180:183], v[86:89]
	v_mfma_f32_16x16x32_bf16 v[82:85], v[164:167], v[180:183], v[82:85]
	v_mfma_f32_16x16x32_bf16 v[78:81], v[156:159], v[188:191], v[78:81]
	v_mfma_f32_16x16x32_bf16 v[74:77], v[164:167], v[188:191], v[74:77]
	v_mfma_f32_16x16x32_bf16 v[70:73], v[156:159], v[198:201], v[70:73]
	v_mfma_f32_16x16x32_bf16 v[66:69], v[164:167], v[198:201], v[66:69]
	s_setprio 0
	s_barrier
	ds_read_b128 v[168:171], v205 offset:49152
	ds_read_b128 v[172:175], v205 offset:50176
	ds_read_b128 v[176:179], v205 offset:51200
	ds_read_b128 v[180:183], v205 offset:52224
	ds_read_b128 v[184:187], v205 offset:53248
	ds_read_b128 v[188:191], v205 offset:54272
	ds_read_b128 v[194:197], v205 offset:55296
	ds_read_b128 v[198:201], v205 offset:56320
	s_add_u32 s20, s17, 0x180
	s_addc_u32 s21, s33, 0
	s_mov_b32 m0, s56
	s_nop 0
	global_load_lds_dwordx4 v114, s[20:21]
	s_nop 0
	s_mov_b32 m0, s57
	s_nop 0
	global_load_lds_dwordx4 v203, s[20:21]
	s_add_u32 s20, s17, 0x40180
	s_addc_u32 s21, s33, 0
	s_mov_b32 m0, s60
	s_nop 0
	global_load_lds_dwordx4 v114, s[20:21]
	s_nop 0
	s_mov_b32 m0, s61
	s_nop 0
	global_load_lds_dwordx4 v203, s[20:21]
	s_nop 0
	s_mov_b32 m0, s58
	s_nop 0
	global_load_lds_dwordx4 v65, s[18:19]
	s_nop 0
	s_mov_b32 m0, s59
	s_nop 0
	global_load_lds_dwordx4 v202, s[18:19]
	s_waitcnt vmcnt(8)
	s_waitcnt lgkmcnt(0)
	s_barrier
	s_setprio 1
	s_waitcnt lgkmcnt(7)
	v_mfma_f32_16x16x32_bf16 v[60:63], v[136:139], v[168:171], v[60:63]
	v_mfma_f32_16x16x32_bf16 v[56:59], v[144:147], v[168:171], v[56:59]
	s_waitcnt lgkmcnt(5)
	v_mfma_f32_16x16x32_bf16 v[52:55], v[136:139], v[176:179], v[52:55]
	v_mfma_f32_16x16x32_bf16 v[48:51], v[144:147], v[176:179], v[48:51]
	s_waitcnt lgkmcnt(3)
	v_mfma_f32_16x16x32_bf16 v[44:47], v[136:139], v[184:187], v[44:47]
	v_mfma_f32_16x16x32_bf16 v[40:43], v[144:147], v[184:187], v[40:43]
	s_waitcnt lgkmcnt(1)
	v_mfma_f32_16x16x32_bf16 v[36:39], v[136:139], v[194:197], v[36:39]
	v_mfma_f32_16x16x32_bf16 v[32:35], v[144:147], v[194:197], v[32:35]
	v_mfma_f32_16x16x32_bf16 v[60:63], v[140:143], v[172:175], v[60:63]
	v_mfma_f32_16x16x32_bf16 v[56:59], v[148:151], v[172:175], v[56:59]
	v_mfma_f32_16x16x32_bf16 v[52:55], v[140:143], v[180:183], v[52:55]
	v_mfma_f32_16x16x32_bf16 v[48:51], v[148:151], v[180:183], v[48:51]
	v_mfma_f32_16x16x32_bf16 v[44:47], v[140:143], v[188:191], v[44:47]
	v_mfma_f32_16x16x32_bf16 v[40:43], v[148:151], v[188:191], v[40:43]
	s_waitcnt lgkmcnt(0)
	v_mfma_f32_16x16x32_bf16 v[36:39], v[140:143], v[198:201], v[36:39]
	v_mfma_f32_16x16x32_bf16 v[32:35], v[148:151], v[198:201], v[32:35]
	s_setprio 0
	s_setprio 1
	v_mfma_f32_16x16x32_bf16 v[28:31], v[152:155], v[168:171], v[28:31]
	v_mfma_f32_16x16x32_bf16 v[24:27], v[160:163], v[168:171], v[24:27]
	v_mfma_f32_16x16x32_bf16 v[20:23], v[152:155], v[176:179], v[20:23]
	v_mfma_f32_16x16x32_bf16 v[16:19], v[160:163], v[176:179], v[16:19]
	v_mfma_f32_16x16x32_bf16 v[12:15], v[152:155], v[184:187], v[12:15]
	v_mfma_f32_16x16x32_bf16 v[8:11], v[160:163], v[184:187], v[8:11]
	v_mfma_f32_16x16x32_bf16 v[4:7], v[152:155], v[194:197], v[4:7]
	v_mfma_f32_16x16x32_bf16 v[0:3], v[160:163], v[194:197], v[0:3]
	v_mfma_f32_16x16x32_bf16 v[28:31], v[156:159], v[172:175], v[28:31]
	v_mfma_f32_16x16x32_bf16 v[24:27], v[164:167], v[172:175], v[24:27]
	v_mfma_f32_16x16x32_bf16 v[20:23], v[156:159], v[180:183], v[20:23]
	v_mfma_f32_16x16x32_bf16 v[16:19], v[164:167], v[180:183], v[16:19]
	v_mfma_f32_16x16x32_bf16 v[12:15], v[156:159], v[188:191], v[12:15]
	v_mfma_f32_16x16x32_bf16 v[8:11], v[164:167], v[188:191], v[8:11]
	v_mfma_f32_16x16x32_bf16 v[4:7], v[156:159], v[198:201], v[4:7]
	v_mfma_f32_16x16x32_bf16 v[0:3], v[164:167], v[198:201], v[0:3]
	s_setprio 0
	s_barrier
	s_add_i32 s15, s15, 2
	s_add_u32 s2, s2, 0x100
	s_addc_u32 s3, s3, 0
	s_cmp_lt_u32 s15, 12
	s_cbranch_scc1 .LBB0_1111
	s_ashr_i32 s17, s16, 31
	s_ashr_i32 s15, s14, 31
	ds_read_b128 v[136:139], v132
	ds_read_b128 v[140:143], v132 offset:1024
	ds_read_b128 v[144:147], v132 offset:2048
	ds_read_b128 v[148:151], v132 offset:3072
	ds_read_b128 v[152:155], v134
	ds_read_b128 v[156:159], v134 offset:1024
	ds_read_b128 v[160:163], v134 offset:2048
	ds_read_b128 v[164:167], v134 offset:3072
	s_lshl_b64 s[2:3], s[16:17], 19
	s_lshl_b64 s[20:21], s[14:15], 19
	s_add_u32 s18, s29, s2
	s_addc_u32 s19, s36, s3
	s_add_u32 s20, s37, s20
	s_addc_u32 s21, s38, s21
	s_and_b64 s[2:3], s[0:1], exec
	s_cselect_b32 s34, s18, s26
	s_cselect_b32 s35, s19, s27
	s_add_u32 s2, s34, 0x80
	s_addc_u32 s3, s35, 0
	s_and_b64 s[64:65], s[0:1], exec
	s_cselect_b32 s25, s21, s25
	s_cselect_b32 s24, s20, s24
	ds_read_b128 v[168:171], v205
	ds_read_b128 v[172:175], v205 offset:1024
	ds_read_b128 v[176:179], v205 offset:2048
	ds_read_b128 v[180:183], v205 offset:3072
	ds_read_b128 v[184:187], v205 offset:4096
	ds_read_b128 v[188:191], v205 offset:5120
	ds_read_b128 v[194:197], v205 offset:6144
	ds_read_b128 v[198:201], v205 offset:7168
	s_add_u32 s26, s26, 0x40780
	s_addc_u32 s27, s27, 0
	s_mov_b32 m0, s62
	s_nop 0
	global_load_lds_dwordx4 v65, s[26:27]
	s_nop 0
	s_mov_b32 m0, s63
	s_nop 0
	global_load_lds_dwordx4 v202, s[26:27]
	s_waitcnt vmcnt(8)
	s_waitcnt lgkmcnt(0)
	s_barrier
	s_setprio 1
	s_waitcnt lgkmcnt(7)
	v_mfma_f32_16x16x32_bf16 v[128:131], v[136:139], v[168:171], v[128:131]
	v_mfma_f32_16x16x32_bf16 v[124:127], v[144:147], v[168:171], v[124:127]
	s_waitcnt lgkmcnt(5)
	v_mfma_f32_16x16x32_bf16 v[120:123], v[136:139], v[176:179], v[120:123]
	v_mfma_f32_16x16x32_bf16 v[116:119], v[144:147], v[176:179], v[116:119]
	s_waitcnt lgkmcnt(3)
	v_mfma_f32_16x16x32_bf16 v[110:113], v[136:139], v[184:187], v[110:113]
	v_mfma_f32_16x16x32_bf16 v[106:109], v[144:147], v[184:187], v[106:109]
	v_mfma_f32_16x16x32_bf16 v[128:131], v[140:143], v[172:175], v[128:131]
	v_mfma_f32_16x16x32_bf16 v[124:127], v[148:151], v[172:175], v[124:127]
	v_mfma_f32_16x16x32_bf16 v[120:123], v[140:143], v[180:183], v[120:123]
	v_mfma_f32_16x16x32_bf16 v[116:119], v[148:151], v[180:183], v[116:119]
	s_waitcnt lgkmcnt(2)
	v_mfma_f32_16x16x32_bf16 v[110:113], v[140:143], v[188:191], v[110:113]
	v_mfma_f32_16x16x32_bf16 v[106:109], v[148:151], v[188:191], v[106:109]
	s_waitcnt lgkmcnt(1)
	v_mfma_f32_16x16x32_bf16 v[102:105], v[136:139], v[194:197], v[102:105]
	v_mfma_f32_16x16x32_bf16 v[98:101], v[144:147], v[194:197], v[98:101]
	s_waitcnt lgkmcnt(0)
	v_mfma_f32_16x16x32_bf16 v[206:209], v[140:143], v[198:201], v[102:105]
	v_mfma_f32_16x16x32_bf16 v[210:213], v[148:151], v[198:201], v[98:101]
	s_setprio 0
	s_setprio 1
	v_mfma_f32_16x16x32_bf16 v[94:97], v[152:155], v[168:171], v[94:97]
	v_mfma_f32_16x16x32_bf16 v[90:93], v[160:163], v[168:171], v[90:93]
	v_mfma_f32_16x16x32_bf16 v[78:81], v[152:155], v[184:187], v[78:81]
	v_mfma_f32_16x16x32_bf16 v[74:77], v[160:163], v[184:187], v[74:77]
	v_mfma_f32_16x16x32_bf16 v[70:73], v[152:155], v[194:197], v[70:73]
	v_mfma_f32_16x16x32_bf16 v[66:69], v[160:163], v[194:197], v[66:69]
	v_mfma_f32_16x16x32_bf16 v[94:97], v[156:159], v[172:175], v[94:97]
	v_mfma_f32_16x16x32_bf16 v[90:93], v[164:167], v[172:175], v[90:93]
	v_mfma_f32_16x16x32_bf16 v[86:89], v[152:155], v[176:179], v[86:89]
	v_mfma_f32_16x16x32_bf16 v[82:85], v[160:163], v[176:179], v[82:85]
	v_mfma_f32_16x16x32_bf16 v[78:81], v[156:159], v[188:191], v[78:81]
	v_mfma_f32_16x16x32_bf16 v[74:77], v[164:167], v[188:191], v[74:77]
	v_mfma_f32_16x16x32_bf16 v[70:73], v[156:159], v[198:201], v[70:73]
	v_mfma_f32_16x16x32_bf16 v[66:69], v[164:167], v[198:201], v[66:69]
	v_mfma_f32_16x16x32_bf16 v[168:171], v[156:159], v[180:183], v[86:89]
	v_mfma_f32_16x16x32_bf16 v[172:175], v[164:167], v[180:183], v[82:85]
	s_setprio 0
	s_barrier
	s_nop 0
	ds_read_b128 v[82:85], v205 offset:16384
	ds_read_b128 v[86:89], v205 offset:17408
	ds_read_b128 v[98:101], v205 offset:18432
	ds_read_b128 v[102:105], v205 offset:19456
	ds_read_b128 v[176:179], v205 offset:20480
	ds_read_b128 v[180:183], v205 offset:21504
	ds_read_b128 v[184:187], v205 offset:22528
	ds_read_b128 v[188:191], v205 offset:23552
	s_mov_b64 exec, s[100:101]
	s_mov_b32 m0, s44
	s_nop 0
	global_load_lds_dwordx4 v114, s[24:25]
	s_mov_b64 exec, -1
	s_add_u32 s26, s24, 0x40000
	s_mov_b64 exec, s[100:101]
	s_mov_b32 m0, s45
	s_nop 0
	global_load_lds_dwordx4 v203, s[24:25]
	s_mov_b64 exec, -1
	s_addc_u32 s27, s25, 0
	s_mov_b64 exec, s[100:101]
	s_mov_b32 m0, s46
	s_nop 0
	global_load_lds_dwordx4 v114, s[26:27]
	s_mov_b64 exec, -1
	s_nop 0
	s_mov_b64 exec, s[100:101]
	s_mov_b32 m0, s47
	s_nop 0
	global_load_lds_dwordx4 v203, s[26:27]
	s_mov_b64 exec, -1
	s_nop 0
	s_mov_b64 exec, s[100:101]
	s_mov_b32 m0, s43
	s_nop 0
	global_load_lds_dwordx4 v65, s[34:35]
	s_mov_b64 exec, -1
	s_nop 0
	s_mov_b64 exec, s[100:101]
	s_mov_b32 m0, s48
	s_nop 0
	global_load_lds_dwordx4 v202, s[34:35]
	s_mov_b64 exec, -1
	s_waitcnt vmcnt(8)
	s_waitcnt lgkmcnt(0)
	s_barrier
	s_setprio 1
	s_waitcnt lgkmcnt(7)
	v_mfma_f32_16x16x32_bf16 v[60:63], v[136:139], v[82:85], v[60:63]
	v_mfma_f32_16x16x32_bf16 v[56:59], v[144:147], v[82:85], v[56:59]
	s_waitcnt lgkmcnt(5)
	v_mfma_f32_16x16x32_bf16 v[52:55], v[136:139], v[98:101], v[52:55]
	v_mfma_f32_16x16x32_bf16 v[48:51], v[144:147], v[98:101], v[48:51]
	v_mfma_f32_16x16x32_bf16 v[60:63], v[140:143], v[86:89], v[60:63]
	v_mfma_f32_16x16x32_bf16 v[56:59], v[148:151], v[86:89], v[56:59]
	s_waitcnt lgkmcnt(4)
	v_mfma_f32_16x16x32_bf16 v[52:55], v[140:143], v[102:105], v[52:55]
	v_mfma_f32_16x16x32_bf16 v[48:51], v[148:151], v[102:105], v[48:51]
	s_waitcnt lgkmcnt(3)
	v_mfma_f32_16x16x32_bf16 v[44:47], v[136:139], v[176:179], v[44:47]
	v_mfma_f32_16x16x32_bf16 v[40:43], v[144:147], v[176:179], v[40:43]
	s_waitcnt lgkmcnt(1)
	v_mfma_f32_16x16x32_bf16 v[36:39], v[136:139], v[184:187], v[36:39]
	v_mfma_f32_16x16x32_bf16 v[32:35], v[144:147], v[184:187], v[32:35]
	v_mfma_f32_16x16x32_bf16 v[44:47], v[140:143], v[180:183], v[44:47]
	v_mfma_f32_16x16x32_bf16 v[40:43], v[148:151], v[180:183], v[40:43]
	s_waitcnt lgkmcnt(0)
	v_mfma_f32_16x16x32_bf16 v[36:39], v[140:143], v[188:191], v[36:39]
	v_mfma_f32_16x16x32_bf16 v[148:151], v[148:151], v[188:191], v[32:35]
	s_setprio 0
	s_setprio 1
	v_mfma_f32_16x16x32_bf16 v[20:23], v[152:155], v[98:101], v[20:23]
	v_mfma_f32_16x16x32_bf16 v[16:19], v[160:163], v[98:101], v[16:19]
	v_mfma_f32_16x16x32_bf16 v[4:7], v[152:155], v[184:187], v[4:7]
	v_mfma_f32_16x16x32_bf16 v[0:3], v[160:163], v[184:187], v[0:3]
	v_mfma_f32_16x16x32_bf16 v[28:31], v[152:155], v[82:85], v[28:31]
	v_mfma_f32_16x16x32_bf16 v[24:27], v[160:163], v[82:85], v[24:27]
	v_mfma_f32_16x16x32_bf16 v[20:23], v[156:159], v[102:105], v[20:23]
	v_mfma_f32_16x16x32_bf16 v[16:19], v[164:167], v[102:105], v[16:19]
	v_mfma_f32_16x16x32_bf16 v[12:15], v[152:155], v[176:179], v[12:15]
	v_mfma_f32_16x16x32_bf16 v[8:11], v[160:163], v[176:179], v[8:11]
	v_mfma_f32_16x16x32_bf16 v[4:7], v[156:159], v[188:191], v[4:7]
	v_mfma_f32_16x16x32_bf16 v[0:3], v[164:167], v[188:191], v[0:3]
	v_mfma_f32_16x16x32_bf16 v[28:31], v[156:159], v[86:89], v[28:31]
	v_mfma_f32_16x16x32_bf16 v[194:197], v[164:167], v[86:89], v[24:27]
	v_mfma_f32_16x16x32_bf16 v[198:201], v[156:159], v[180:183], v[12:15]
	v_mfma_f32_16x16x32_bf16 v[176:179], v[164:167], v[180:183], v[8:11]
	s_setprio 0
	s_barrier
	s_nop 0
	ds_read_b128 v[8:11], v133
	ds_read_b128 v[12:15], v133 offset:1024
	ds_read_b128 v[152:155], v133 offset:2048
	ds_read_b128 v[156:159], v133 offset:3072
	ds_read_b128 v[160:163], v135
	ds_read_b128 v[164:167], v135 offset:1024
	ds_read_b128 v[180:183], v135 offset:2048
	ds_read_b128 v[184:187], v135 offset:3072
	ds_read_b128 v[24:27], v205 offset:32768
	ds_read_b128 v[32:35], v205 offset:33792
	ds_read_b128 v[188:191], v205 offset:34816
	ds_read_b128 v[214:217], v205 offset:35840
	ds_read_b128 v[218:221], v205 offset:36864
	ds_read_b128 v[222:225], v205 offset:37888
	ds_read_b128 v[226:229], v205 offset:38912
	ds_read_b128 v[230:233], v205 offset:39936
	s_add_u32 s26, s34, 0x40000
	s_addc_u32 s27, s35, 0
	s_mov_b64 exec, s[100:101]
	s_mov_b32 m0, s49
	s_nop 0
	global_load_lds_dwordx4 v65, s[26:27]
	s_mov_b64 exec, -1
	s_nop 0
	s_mov_b64 exec, s[100:101]
	s_mov_b32 m0, s50
	s_nop 0
	global_load_lds_dwordx4 v202, s[26:27]
	s_mov_b64 exec, -1
	s_waitcnt vmcnt(8)
	s_waitcnt lgkmcnt(0)
	s_barrier
	s_setprio 1
	s_waitcnt lgkmcnt(7)
	v_mfma_f32_16x16x32_bf16 v[82:85], v[8:11], v[24:27], v[128:131]
	s_waitcnt lgkmcnt(6)
	v_mfma_f32_16x16x32_bf16 v[140:143], v[12:15], v[32:35], v[82:85]
	v_mfma_f32_16x16x32_bf16 v[82:85], v[152:155], v[24:27], v[124:127]
	v_mfma_f32_16x16x32_bf16 v[144:147], v[156:159], v[32:35], v[82:85]
	s_waitcnt lgkmcnt(5)
	v_mfma_f32_16x16x32_bf16 v[82:85], v[8:11], v[188:191], v[120:123]
	s_waitcnt lgkmcnt(4)
	v_mfma_f32_16x16x32_bf16 v[124:127], v[12:15], v[214:217], v[82:85]
	v_mfma_f32_16x16x32_bf16 v[82:85], v[152:155], v[188:191], v[116:119]
	v_mfma_f32_16x16x32_bf16 v[128:131], v[156:159], v[214:217], v[82:85]
	s_waitcnt lgkmcnt(3)
	v_mfma_f32_16x16x32_bf16 v[82:85], v[8:11], v[218:221], v[110:113]
	s_waitcnt lgkmcnt(2)
	v_mfma_f32_16x16x32_bf16 v[98:101], v[12:15], v[222:225], v[82:85]
	v_mfma_f32_16x16x32_bf16 v[82:85], v[152:155], v[218:221], v[106:109]
	v_mfma_f32_16x16x32_bf16 v[102:105], v[156:159], v[222:225], v[82:85]
	s_waitcnt lgkmcnt(1)
	v_mfma_f32_16x16x32_bf16 v[82:85], v[8:11], v[226:229], v[206:209]
	v_mfma_f32_16x16x32_bf16 v[86:89], v[152:155], v[226:229], v[210:213]
	s_waitcnt lgkmcnt(0)
	v_mfma_f32_16x16x32_bf16 v[82:85], v[12:15], v[230:233], v[82:85]
	v_mfma_f32_16x16x32_bf16 v[86:89], v[156:159], v[230:233], v[86:89]
	s_setprio 0
	s_setprio 1
	v_mfma_f32_16x16x32_bf16 v[94:97], v[160:163], v[24:27], v[94:97]
	v_mfma_f32_16x16x32_bf16 v[24:27], v[180:183], v[24:27], v[90:93]
	v_mfma_f32_16x16x32_bf16 v[132:135], v[184:187], v[32:35], v[24:27]
	v_mfma_f32_16x16x32_bf16 v[24:27], v[160:163], v[188:191], v[168:171]
	v_mfma_f32_16x16x32_bf16 v[120:123], v[164:167], v[214:217], v[24:27]
	v_mfma_f32_16x16x32_bf16 v[24:27], v[180:183], v[188:191], v[172:175]
	v_mfma_f32_16x16x32_bf16 v[116:119], v[184:187], v[214:217], v[24:27]
	v_mfma_f32_16x16x32_bf16 v[24:27], v[160:163], v[218:221], v[78:81]
	v_mfma_f32_16x16x32_bf16 v[106:109], v[164:167], v[222:225], v[24:27]
	v_mfma_f32_16x16x32_bf16 v[24:27], v[180:183], v[218:221], v[74:77]
	v_mfma_f32_16x16x32_bf16 v[110:113], v[184:187], v[222:225], v[24:27]
	v_mfma_f32_16x16x32_bf16 v[24:27], v[160:163], v[226:229], v[70:73]
	v_mfma_f32_16x16x32_bf16 v[90:93], v[164:167], v[230:233], v[24:27]
	v_mfma_f32_16x16x32_bf16 v[24:27], v[180:183], v[226:229], v[66:69]
	v_mfma_f32_16x16x32_bf16 v[136:139], v[164:167], v[32:35], v[94:97]
	v_mfma_f32_16x16x32_bf16 v[94:97], v[184:187], v[230:233], v[24:27]
	s_setprio 0
	s_barrier
	ds_read_b128 v[66:69], v205 offset:49152
	ds_read_b128 v[168:171], v205 offset:50176
	ds_read_b128 v[172:175], v205 offset:51200
	ds_read_b128 v[188:191], v205 offset:52224
	ds_read_b128 v[206:209], v205 offset:53248
	ds_read_b128 v[210:213], v205 offset:54272
	ds_read_b128 v[214:217], v205 offset:55296
	ds_read_b128 v[218:221], v205 offset:56320
	s_add_u32 s26, s24, 0x80
	s_addc_u32 s27, s25, 0
	s_mov_b64 exec, s[100:101]
	s_mov_b32 m0, s56
	s_nop 0
	global_load_lds_dwordx4 v114, s[26:27]
	s_mov_b64 exec, -1
	s_add_u32 s24, s24, 0x40080
	s_mov_b64 exec, s[100:101]
	s_mov_b32 m0, s57
	s_nop 0
	global_load_lds_dwordx4 v203, s[26:27]
	s_mov_b64 exec, -1
	s_addc_u32 s25, s25, 0
	s_mov_b64 exec, s[100:101]
	s_mov_b32 m0, s60
	s_nop 0
	global_load_lds_dwordx4 v114, s[24:25]
	s_mov_b64 exec, -1
	s_nop 0
	s_mov_b64 exec, s[100:101]
	s_mov_b32 m0, s61
	s_nop 0
	global_load_lds_dwordx4 v203, s[24:25]
	s_mov_b64 exec, -1
	s_nop 0
	s_mov_b64 exec, s[100:101]
	s_mov_b32 m0, s58
	s_nop 0
	global_load_lds_dwordx4 v65, s[2:3]
	s_mov_b64 exec, -1
	s_nop 0
	s_mov_b64 exec, s[100:101]
	s_mov_b32 m0, s59
	s_nop 0
	global_load_lds_dwordx4 v202, s[2:3]
	s_mov_b64 exec, -1
	s_waitcnt vmcnt(8)
	s_waitcnt lgkmcnt(0)
	s_barrier
	s_setprio 1
	s_waitcnt lgkmcnt(7)
	v_mfma_f32_16x16x32_bf16 v[24:27], v[8:11], v[66:69], v[60:63]
	s_waitcnt lgkmcnt(6)
	v_mfma_f32_16x16x32_bf16 v[78:81], v[12:15], v[168:171], v[24:27]
	v_mfma_f32_16x16x32_bf16 v[24:27], v[152:155], v[66:69], v[56:59]
	v_mfma_f32_16x16x32_bf16 v[74:77], v[156:159], v[168:171], v[24:27]
	s_waitcnt lgkmcnt(5)
	v_mfma_f32_16x16x32_bf16 v[24:27], v[8:11], v[172:175], v[52:55]
	s_waitcnt lgkmcnt(4)
	v_mfma_f32_16x16x32_bf16 v[60:63], v[12:15], v[188:191], v[24:27]
	v_mfma_f32_16x16x32_bf16 v[24:27], v[152:155], v[172:175], v[48:51]
	v_mfma_f32_16x16x32_bf16 v[56:59], v[156:159], v[188:191], v[24:27]
	s_waitcnt lgkmcnt(3)
	v_mfma_f32_16x16x32_bf16 v[24:27], v[8:11], v[206:209], v[44:47]
	s_waitcnt lgkmcnt(1)
	v_mfma_f32_16x16x32_bf16 v[8:11], v[8:11], v[214:217], v[36:39]
	v_mfma_f32_16x16x32_bf16 v[32:35], v[12:15], v[210:213], v[24:27]
	v_mfma_f32_16x16x32_bf16 v[24:27], v[152:155], v[206:209], v[40:43]
	s_waitcnt lgkmcnt(0)
	v_mfma_f32_16x16x32_bf16 v[12:15], v[12:15], v[218:221], v[8:11]
	v_mfma_f32_16x16x32_bf16 v[8:11], v[152:155], v[214:217], v[148:151]
	v_mfma_f32_16x16x32_bf16 v[24:27], v[156:159], v[210:213], v[24:27]
	v_mfma_f32_16x16x32_bf16 v[8:11], v[156:159], v[218:221], v[8:11]
	s_setprio 0
	s_setprio 1
	v_mfma_f32_16x16x32_bf16 v[16:19], v[180:183], v[172:175], v[16:19]
	v_mfma_f32_16x16x32_bf16 v[28:31], v[160:163], v[66:69], v[28:31]
	v_mfma_f32_16x16x32_bf16 v[20:23], v[160:163], v[172:175], v[20:23]
	v_mfma_f32_16x16x32_bf16 v[48:51], v[184:187], v[188:191], v[16:19]
	v_mfma_f32_16x16x32_bf16 v[16:19], v[160:163], v[206:209], v[198:201]
	v_mfma_f32_16x16x32_bf16 v[70:73], v[164:167], v[168:171], v[28:31]
	v_mfma_f32_16x16x32_bf16 v[28:31], v[180:183], v[66:69], v[194:197]
	v_mfma_f32_16x16x32_bf16 v[52:55], v[164:167], v[188:191], v[20:23]
	v_mfma_f32_16x16x32_bf16 v[20:23], v[164:167], v[210:213], v[16:19]
	v_mfma_f32_16x16x32_bf16 v[16:19], v[180:183], v[206:209], v[176:179]
	v_mfma_f32_16x16x32_bf16 v[4:7], v[160:163], v[214:217], v[4:7]
	v_mfma_f32_16x16x32_bf16 v[0:3], v[180:183], v[214:217], v[0:3]
	v_mfma_f32_16x16x32_bf16 v[66:69], v[184:187], v[168:171], v[28:31]
	v_mfma_f32_16x16x32_bf16 v[16:19], v[184:187], v[210:213], v[16:19]
	v_mfma_f32_16x16x32_bf16 v[4:7], v[164:167], v[218:221], v[4:7]
	v_mfma_f32_16x16x32_bf16 v[0:3], v[184:187], v[218:221], v[0:3]
	s_setprio 0
	s_barrier
	s_andn2_b64 vcc, exec, s[10:11]
	s_cbranch_vccnz .LBB0_1114
	s_barrier

.LBB0_1418:
	s_add_i32 s59, s59, 1
	v_readlane_b32 s0, v254, 38
	s_mul_i32 s0, s59, s0
	s_mul_hi_u32 s1, s59, s70
	s_add_i32 s1, s1, s0
	s_mul_i32 s0, s59, s70
	v_readlane_b32 s2, v255, 0
	s_add_u32 s0, s0, s2
	s_addc_u32 s1, s1, s48
	v_mov_b64_e32 v[0:1], s[30:31]
	v_cmp_ge_i64_e32 vcc, s[0:1], v[0:1]
	v_cmp_lt_i64_e64 s[4:5], s[0:1], v[0:1]
	s_nop 3
	s_cmp_lg_u64 s[4:5], 0
	s_cselect_b64 s[100:101], -1, 1
	s_cbranch_vccnz .LBB0_1420
	s_ashr_i32 s1, s0, 31
	s_lshr_b32 s1, s1, 29
	s_add_i32 s1, s0, s1
	s_ashr_i32 s2, s1, 3
	s_and_b32 s1, s1, -8
	s_sub_i32 s0, s0, s1
	s_cmp_lt_i32 s0, 0
	s_cselect_b32 s1, s39, s29
	s_mul_i32 s0, s1, s0
	s_add_i32 s0, s0, s2
	s_ashr_i32 s1, s0, 31
	s_lshr_b32 s1, s1, 26
	s_add_i32 s1, s0, s1
	s_ashr_i32 s2, s1, 6
	s_lshl_b32 s2, s2, 3
	s_sub_i32 s3, s29, s2
	s_min_i32 s3, s3, 8
	s_abs_i32 s20, s3
	v_cvt_f32_u32_e32 v0, s20
	s_sub_i32 s22, 0, s20
	s_andn2_b32 s1, s1, 63
	s_sub_i32 s0, s0, s1
	v_rcp_iflag_f32_e32 v0, v0
	s_abs_i32 s1, s0
	s_xor_b32 s21, s0, s3
	s_ashr_i32 s21, s21, 31
	v_mul_f32_e32 v0, 0x4f7ffffe, v0
	v_cvt_u32_f32_e32 v0, v0
	s_nop 0
	v_readfirstlane_b32 s23, v0
	s_mul_i32 s22, s22, s23
	s_mul_hi_u32 s22, s23, s22
	s_add_i32 s23, s23, s22
	s_mul_hi_u32 s22, s1, s23
	s_mul_i32 s23, s22, s20
	s_sub_i32 s1, s1, s23
	s_add_i32 s26, s22, 1
	s_sub_i32 s23, s1, s20
	s_cmp_ge_u32 s1, s20
	s_cselect_b32 s22, s26, s22
	s_cselect_b32 s1, s23, s1
	s_add_i32 s23, s22, 1
	s_cmp_ge_u32 s1, s20
	s_cselect_b32 s1, s23, s22
	s_xor_b32 s1, s1, s21
	s_sub_i32 s20, s1, s21
	s_mul_i32 s1, s20, s3
	s_sub_i32 s0, s0, s1
	s_add_i32 s60, s0, s2

.LBB0_1425:
	s_add_u32 s66, s72, s2
	s_addc_u32 s67, s73, s3
	s_add_u32 s34, s66, 0x2000100
	s_addc_u32 s35, s67, 0
	v_add_u32_e32 v141, 0x10000, v134
	v_add_u32_e32 v142, 0x14000, v134
	s_add_u32 s26, s66, 0x2000180
	ds_read_b128 v[144:147], v141
	ds_read_b128 v[148:151], v141 offset:1024
	ds_read_b128 v[152:155], v141 offset:2048
	ds_read_b128 v[156:159], v141 offset:3072
	ds_read_b128 v[160:163], v142
	ds_read_b128 v[164:167], v142 offset:1024
	ds_read_b128 v[168:171], v142 offset:2048
	ds_read_b128 v[172:175], v142 offset:3072
	s_addc_u32 s27, s67, 0
	s_add_u32 s33, s24, s2
	s_addc_u32 s63, s25, s3
	s_add_u32 s64, s33, 0x100
	s_addc_u32 s65, s63, 0
	s_add_u32 s66, s66, 0x2000080
	s_addc_u32 s67, s67, 0
	ds_read_b128 v[176:179], v135
	ds_read_b128 v[180:183], v135 offset:1024
	ds_read_b128 v[184:187], v135 offset:2048
	ds_read_b128 v[188:191], v135 offset:3072
	ds_read_b128 v[194:197], v135 offset:4096
	ds_read_b128 v[198:201], v135 offset:5120
	ds_read_b128 v[202:205], v135 offset:6144
	ds_read_b128 v[206:209], v135 offset:7168
	s_mov_b32 m0, s57
	s_nop 0
	global_load_lds_dwordx4 v133, s[66:67]
	s_nop 0
	s_mov_b32 m0, s58
	s_nop 0
	global_load_lds_dwordx4 v132, s[66:67]
	s_waitcnt vmcnt(8)
	s_waitcnt lgkmcnt(0)
	s_barrier
	s_setprio 1
	s_waitcnt lgkmcnt(0)
	v_mfma_f32_16x16x32_bf16 v[128:131], v[144:147], v[176:179], v[128:131]
	v_mfma_f32_16x16x32_bf16 v[124:127], v[152:155], v[176:179], v[124:127]
	s_waitcnt lgkmcnt(5)
	v_mfma_f32_16x16x32_bf16 v[120:123], v[144:147], v[184:187], v[120:123]
	v_mfma_f32_16x16x32_bf16 v[116:119], v[152:155], v[184:187], v[116:119]
	s_waitcnt lgkmcnt(3)
	v_mfma_f32_16x16x32_bf16 v[110:113], v[144:147], v[194:197], v[110:113]
	v_mfma_f32_16x16x32_bf16 v[106:109], v[152:155], v[194:197], v[106:109]
	s_waitcnt lgkmcnt(1)
	v_mfma_f32_16x16x32_bf16 v[102:105], v[144:147], v[202:205], v[102:105]
	v_mfma_f32_16x16x32_bf16 v[98:101], v[152:155], v[202:205], v[98:101]
	v_mfma_f32_16x16x32_bf16 v[128:131], v[148:151], v[180:183], v[128:131]
	v_mfma_f32_16x16x32_bf16 v[124:127], v[156:159], v[180:183], v[124:127]
	v_mfma_f32_16x16x32_bf16 v[120:123], v[148:151], v[188:191], v[120:123]
	v_mfma_f32_16x16x32_bf16 v[116:119], v[156:159], v[188:191], v[116:119]
	v_mfma_f32_16x16x32_bf16 v[110:113], v[148:151], v[198:201], v[110:113]
	v_mfma_f32_16x16x32_bf16 v[106:109], v[156:159], v[198:201], v[106:109]
	s_waitcnt lgkmcnt(0)
	v_mfma_f32_16x16x32_bf16 v[102:105], v[148:151], v[206:209], v[102:105]
	v_mfma_f32_16x16x32_bf16 v[98:101], v[156:159], v[206:209], v[98:101]
	s_setprio 0
	s_setprio 1
	v_mfma_f32_16x16x32_bf16 v[94:97], v[160:163], v[176:179], v[94:97]
	v_mfma_f32_16x16x32_bf16 v[90:93], v[168:171], v[176:179], v[90:93]
	v_mfma_f32_16x16x32_bf16 v[86:89], v[160:163], v[184:187], v[86:89]
	v_mfma_f32_16x16x32_bf16 v[82:85], v[168:171], v[184:187], v[82:85]
	v_mfma_f32_16x16x32_bf16 v[78:81], v[160:163], v[194:197], v[78:81]
	v_mfma_f32_16x16x32_bf16 v[74:77], v[168:171], v[194:197], v[74:77]
	v_mfma_f32_16x16x32_bf16 v[70:73], v[160:163], v[202:205], v[70:73]
	v_mfma_f32_16x16x32_bf16 v[66:69], v[168:171], v[202:205], v[66:69]
	v_mfma_f32_16x16x32_bf16 v[94:97], v[164:167], v[180:183], v[94:97]
	v_mfma_f32_16x16x32_bf16 v[90:93], v[172:175], v[180:183], v[90:93]
	v_mfma_f32_16x16x32_bf16 v[86:89], v[164:167], v[188:191], v[86:89]
	v_mfma_f32_16x16x32_bf16 v[82:85], v[172:175], v[188:191], v[82:85]
	v_mfma_f32_16x16x32_bf16 v[78:81], v[164:167], v[198:201], v[78:81]
	v_mfma_f32_16x16x32_bf16 v[74:77], v[172:175], v[198:201], v[74:77]
	v_mfma_f32_16x16x32_bf16 v[70:73], v[164:167], v[206:209], v[70:73]
	v_mfma_f32_16x16x32_bf16 v[66:69], v[172:175], v[206:209], v[66:69]
	s_setprio 0
	s_barrier
	ds_read_b128 v[176:179], v135 offset:16384
	ds_read_b128 v[180:183], v135 offset:17408
	ds_read_b128 v[184:187], v135 offset:18432
	ds_read_b128 v[188:191], v135 offset:19456
	ds_read_b128 v[194:197], v135 offset:20480
	ds_read_b128 v[198:201], v135 offset:21504
	ds_read_b128 v[202:205], v135 offset:22528
	ds_read_b128 v[206:209], v135 offset:23552
	s_mov_b32 m0, s41
	s_nop 0
	global_load_lds_dwordx4 v65, s[64:65]
	s_nop 0
	s_mov_b32 m0, s42
	s_nop 0
	global_load_lds_dwordx4 v114, s[64:65]
	s_add_u32 s64, s33, 0x40100
	s_addc_u32 s65, s63, 0
	s_mov_b32 m0, s43
	s_nop 0
	global_load_lds_dwordx4 v65, s[64:65]
	s_nop 0
	s_mov_b32 m0, s44
	s_nop 0
	global_load_lds_dwordx4 v114, s[64:65]
	s_mov_b32 m0, s40
	s_nop 0
	global_load_lds_dwordx4 v139, s[34:35]
	s_nop 0
	s_mov_b32 m0, s45
	s_nop 0
	global_load_lds_dwordx4 v138, s[34:35]
	s_waitcnt vmcnt(8)
	s_waitcnt lgkmcnt(0)
	s_barrier
	s_setprio 1
	s_waitcnt lgkmcnt(0)
	v_mfma_f32_16x16x32_bf16 v[60:63], v[144:147], v[176:179], v[60:63]
	v_mfma_f32_16x16x32_bf16 v[56:59], v[152:155], v[176:179], v[56:59]
	s_waitcnt lgkmcnt(5)
	v_mfma_f32_16x16x32_bf16 v[52:55], v[144:147], v[184:187], v[52:55]
	v_mfma_f32_16x16x32_bf16 v[48:51], v[152:155], v[184:187], v[48:51]
	s_waitcnt lgkmcnt(3)
	v_mfma_f32_16x16x32_bf16 v[44:47], v[144:147], v[194:197], v[44:47]
	v_mfma_f32_16x16x32_bf16 v[40:43], v[152:155], v[194:197], v[40:43]
	s_waitcnt lgkmcnt(1)
	v_mfma_f32_16x16x32_bf16 v[36:39], v[144:147], v[202:205], v[36:39]
	v_mfma_f32_16x16x32_bf16 v[32:35], v[152:155], v[202:205], v[32:35]
	v_mfma_f32_16x16x32_bf16 v[60:63], v[148:151], v[180:183], v[60:63]
	v_mfma_f32_16x16x32_bf16 v[56:59], v[156:159], v[180:183], v[56:59]
	v_mfma_f32_16x16x32_bf16 v[52:55], v[148:151], v[188:191], v[52:55]
	v_mfma_f32_16x16x32_bf16 v[48:51], v[156:159], v[188:191], v[48:51]
	v_mfma_f32_16x16x32_bf16 v[44:47], v[148:151], v[198:201], v[44:47]
	v_mfma_f32_16x16x32_bf16 v[40:43], v[156:159], v[198:201], v[40:43]
	s_waitcnt lgkmcnt(0)
	v_mfma_f32_16x16x32_bf16 v[36:39], v[148:151], v[206:209], v[36:39]
	v_mfma_f32_16x16x32_bf16 v[32:35], v[156:159], v[206:209], v[32:35]
	s_setprio 0
	s_setprio 1
	v_mfma_f32_16x16x32_bf16 v[28:31], v[160:163], v[176:179], v[28:31]
	v_mfma_f32_16x16x32_bf16 v[24:27], v[168:171], v[176:179], v[24:27]
	v_mfma_f32_16x16x32_bf16 v[20:23], v[160:163], v[184:187], v[20:23]
	v_mfma_f32_16x16x32_bf16 v[16:19], v[168:171], v[184:187], v[16:19]
	v_mfma_f32_16x16x32_bf16 v[12:15], v[160:163], v[194:197], v[12:15]
	v_mfma_f32_16x16x32_bf16 v[8:11], v[168:171], v[194:197], v[8:11]
	v_mfma_f32_16x16x32_bf16 v[4:7], v[160:163], v[202:205], v[4:7]
	v_mfma_f32_16x16x32_bf16 v[0:3], v[168:171], v[202:205], v[0:3]
	v_mfma_f32_16x16x32_bf16 v[28:31], v[164:167], v[180:183], v[28:31]
	v_mfma_f32_16x16x32_bf16 v[24:27], v[172:175], v[180:183], v[24:27]
	v_mfma_f32_16x16x32_bf16 v[20:23], v[164:167], v[188:191], v[20:23]
	v_mfma_f32_16x16x32_bf16 v[16:19], v[172:175], v[188:191], v[16:19]
	v_mfma_f32_16x16x32_bf16 v[12:15], v[164:167], v[198:201], v[12:15]
	v_mfma_f32_16x16x32_bf16 v[8:11], v[172:175], v[198:201], v[8:11]
	v_mfma_f32_16x16x32_bf16 v[4:7], v[164:167], v[206:209], v[4:7]
	v_mfma_f32_16x16x32_bf16 v[0:3], v[172:175], v[206:209], v[0:3]
	s_setprio 0
	s_barrier
	v_add_u32_e32 v143, 0x18000, v134
	v_add_u32_e32 v144, 0x1c000, v134
	ds_read_b128 v[146:149], v143
	ds_read_b128 v[150:153], v143 offset:1024
	ds_read_b128 v[154:157], v143 offset:2048
	ds_read_b128 v[158:161], v143 offset:3072
	ds_read_b128 v[162:165], v144
	ds_read_b128 v[166:169], v144 offset:1024
	ds_read_b128 v[170:173], v144 offset:2048
	ds_read_b128 v[174:177], v144 offset:3072
	ds_read_b128 v[178:181], v135 offset:32768
	ds_read_b128 v[182:185], v135 offset:33792
	ds_read_b128 v[186:189], v135 offset:34816
	ds_read_b128 v[194:197], v135 offset:35840
	ds_read_b128 v[198:201], v135 offset:36864
	ds_read_b128 v[202:205], v135 offset:37888
	ds_read_b128 v[206:209], v135 offset:38912
	ds_read_b128 v[210:213], v135 offset:39936
	s_mov_b32 m0, s46
	s_nop 0
	global_load_lds_dwordx4 v133, s[34:35]
	s_nop 0
	s_mov_b32 m0, s47
	s_nop 0
	global_load_lds_dwordx4 v132, s[34:35]
	s_waitcnt vmcnt(8)
	s_waitcnt lgkmcnt(0)
	s_barrier
	s_setprio 1
	s_waitcnt lgkmcnt(0)
	v_mfma_f32_16x16x32_bf16 v[128:131], v[146:149], v[178:181], v[128:131]
	v_mfma_f32_16x16x32_bf16 v[124:127], v[154:157], v[178:181], v[124:127]
	s_waitcnt lgkmcnt(5)
	v_mfma_f32_16x16x32_bf16 v[120:123], v[146:149], v[186:189], v[120:123]
	v_mfma_f32_16x16x32_bf16 v[116:119], v[154:157], v[186:189], v[116:119]
	s_waitcnt lgkmcnt(3)
	v_mfma_f32_16x16x32_bf16 v[110:113], v[146:149], v[198:201], v[110:113]
	v_mfma_f32_16x16x32_bf16 v[106:109], v[154:157], v[198:201], v[106:109]
	s_waitcnt lgkmcnt(1)
	v_mfma_f32_16x16x32_bf16 v[102:105], v[146:149], v[206:209], v[102:105]
	v_mfma_f32_16x16x32_bf16 v[98:101], v[154:157], v[206:209], v[98:101]
	v_mfma_f32_16x16x32_bf16 v[128:131], v[150:153], v[182:185], v[128:131]
	v_mfma_f32_16x16x32_bf16 v[124:127], v[158:161], v[182:185], v[124:127]
	v_mfma_f32_16x16x32_bf16 v[120:123], v[150:153], v[194:197], v[120:123]
	v_mfma_f32_16x16x32_bf16 v[116:119], v[158:161], v[194:197], v[116:119]
	v_mfma_f32_16x16x32_bf16 v[110:113], v[150:153], v[202:205], v[110:113]
	v_mfma_f32_16x16x32_bf16 v[106:109], v[158:161], v[202:205], v[106:109]
	s_waitcnt lgkmcnt(0)
	v_mfma_f32_16x16x32_bf16 v[102:105], v[150:153], v[210:213], v[102:105]
	v_mfma_f32_16x16x32_bf16 v[98:101], v[158:161], v[210:213], v[98:101]
	s_setprio 0
	s_setprio 1
	v_mfma_f32_16x16x32_bf16 v[94:97], v[162:165], v[178:181], v[94:97]
	v_mfma_f32_16x16x32_bf16 v[90:93], v[170:173], v[178:181], v[90:93]
	v_mfma_f32_16x16x32_bf16 v[86:89], v[162:165], v[186:189], v[86:89]
	v_mfma_f32_16x16x32_bf16 v[82:85], v[170:173], v[186:189], v[82:85]
	v_mfma_f32_16x16x32_bf16 v[78:81], v[162:165], v[198:201], v[78:81]
	v_mfma_f32_16x16x32_bf16 v[74:77], v[170:173], v[198:201], v[74:77]
	v_mfma_f32_16x16x32_bf16 v[70:73], v[162:165], v[206:209], v[70:73]
	v_mfma_f32_16x16x32_bf16 v[66:69], v[170:173], v[206:209], v[66:69]
	v_mfma_f32_16x16x32_bf16 v[94:97], v[166:169], v[182:185], v[94:97]
	v_mfma_f32_16x16x32_bf16 v[90:93], v[174:177], v[182:185], v[90:93]
	v_mfma_f32_16x16x32_bf16 v[86:89], v[166:169], v[194:197], v[86:89]
	v_mfma_f32_16x16x32_bf16 v[82:85], v[174:177], v[194:197], v[82:85]
	v_mfma_f32_16x16x32_bf16 v[78:81], v[166:169], v[202:205], v[78:81]
	v_mfma_f32_16x16x32_bf16 v[74:77], v[174:177], v[202:205], v[74:77]
	v_mfma_f32_16x16x32_bf16 v[70:73], v[166:169], v[210:213], v[70:73]
	v_mfma_f32_16x16x32_bf16 v[66:69], v[174:177], v[210:213], v[66:69]
	s_setprio 0
	s_barrier
	ds_read_b128 v[178:181], v135 offset:49152
	ds_read_b128 v[182:185], v135 offset:50176
	ds_read_b128 v[186:189], v135 offset:51200
	ds_read_b128 v[194:197], v135 offset:52224
	ds_read_b128 v[198:201], v135 offset:53248
	ds_read_b128 v[202:205], v135 offset:54272
	ds_read_b128 v[206:209], v135 offset:55296
	ds_read_b128 v[210:213], v135 offset:56320
	s_add_u32 s34, s33, 0x180
	s_addc_u32 s35, s63, 0
	s_mov_b32 m0, s51
	s_nop 0
	global_load_lds_dwordx4 v65, s[34:35]
	s_nop 0
	s_mov_b32 m0, s52
	s_nop 0
	global_load_lds_dwordx4 v114, s[34:35]
	s_add_u32 s34, s33, 0x40180
	s_addc_u32 s35, s63, 0
	s_mov_b32 m0, s55
	s_nop 0
	global_load_lds_dwordx4 v65, s[34:35]
	s_nop 0
	s_mov_b32 m0, s56
	s_nop 0
	global_load_lds_dwordx4 v114, s[34:35]
	s_nop 0
	s_mov_b32 m0, s53
	s_nop 0
	global_load_lds_dwordx4 v139, s[26:27]
	s_nop 0
	s_mov_b32 m0, s54
	s_nop 0
	global_load_lds_dwordx4 v138, s[26:27]
	s_waitcnt vmcnt(8)
	s_waitcnt lgkmcnt(0)
	s_barrier
	s_setprio 1
	s_waitcnt lgkmcnt(0)
	v_mfma_f32_16x16x32_bf16 v[60:63], v[146:149], v[178:181], v[60:63]
	v_mfma_f32_16x16x32_bf16 v[56:59], v[154:157], v[178:181], v[56:59]
	s_waitcnt lgkmcnt(5)
	v_mfma_f32_16x16x32_bf16 v[52:55], v[146:149], v[186:189], v[52:55]
	v_mfma_f32_16x16x32_bf16 v[48:51], v[154:157], v[186:189], v[48:51]
	s_waitcnt lgkmcnt(3)
	v_mfma_f32_16x16x32_bf16 v[44:47], v[146:149], v[198:201], v[44:47]
	v_mfma_f32_16x16x32_bf16 v[40:43], v[154:157], v[198:201], v[40:43]
	s_waitcnt lgkmcnt(1)
	v_mfma_f32_16x16x32_bf16 v[36:39], v[146:149], v[206:209], v[36:39]
	v_mfma_f32_16x16x32_bf16 v[32:35], v[154:157], v[206:209], v[32:35]
	v_mfma_f32_16x16x32_bf16 v[60:63], v[150:153], v[182:185], v[60:63]
	v_mfma_f32_16x16x32_bf16 v[56:59], v[158:161], v[182:185], v[56:59]
	v_mfma_f32_16x16x32_bf16 v[52:55], v[150:153], v[194:197], v[52:55]
	v_mfma_f32_16x16x32_bf16 v[48:51], v[158:161], v[194:197], v[48:51]
	v_mfma_f32_16x16x32_bf16 v[44:47], v[150:153], v[202:205], v[44:47]
	v_mfma_f32_16x16x32_bf16 v[40:43], v[158:161], v[202:205], v[40:43]
	s_waitcnt lgkmcnt(0)
	v_mfma_f32_16x16x32_bf16 v[36:39], v[150:153], v[210:213], v[36:39]
	v_mfma_f32_16x16x32_bf16 v[32:35], v[158:161], v[210:213], v[32:35]
	s_setprio 0
	s_setprio 1
	v_mfma_f32_16x16x32_bf16 v[28:31], v[162:165], v[178:181], v[28:31]
	v_mfma_f32_16x16x32_bf16 v[24:27], v[170:173], v[178:181], v[24:27]
	v_mfma_f32_16x16x32_bf16 v[20:23], v[162:165], v[186:189], v[20:23]
	v_mfma_f32_16x16x32_bf16 v[16:19], v[170:173], v[186:189], v[16:19]
	v_mfma_f32_16x16x32_bf16 v[12:15], v[162:165], v[198:201], v[12:15]
	v_mfma_f32_16x16x32_bf16 v[8:11], v[170:173], v[198:201], v[8:11]
	v_mfma_f32_16x16x32_bf16 v[4:7], v[162:165], v[206:209], v[4:7]
	v_mfma_f32_16x16x32_bf16 v[0:3], v[170:173], v[206:209], v[0:3]
	v_mfma_f32_16x16x32_bf16 v[28:31], v[166:169], v[182:185], v[28:31]
	v_mfma_f32_16x16x32_bf16 v[24:27], v[174:177], v[182:185], v[24:27]
	v_mfma_f32_16x16x32_bf16 v[20:23], v[166:169], v[194:197], v[20:23]
	v_mfma_f32_16x16x32_bf16 v[16:19], v[174:177], v[194:197], v[16:19]
	v_mfma_f32_16x16x32_bf16 v[12:15], v[166:169], v[202:205], v[12:15]
	v_mfma_f32_16x16x32_bf16 v[8:11], v[174:177], v[202:205], v[8:11]
	v_mfma_f32_16x16x32_bf16 v[4:7], v[166:169], v[210:213], v[4:7]
	v_mfma_f32_16x16x32_bf16 v[0:3], v[174:177], v[210:213], v[0:3]
	s_setprio 0
	s_barrier
	s_add_i32 s21, s21, 2
	s_add_u32 s2, s2, 0x100
	s_addc_u32 s3, s3, 0
	s_cmp_lt_u32 s21, 12
	s_cbranch_scc1 .LBB0_1425
	ds_read_b128 v[146:149], v141
	ds_read_b128 v[150:153], v141 offset:1024
	ds_read_b128 v[154:157], v141 offset:2048
	ds_read_b128 v[158:161], v141 offset:3072
	ds_read_b128 v[162:165], v142
	ds_read_b128 v[166:169], v142 offset:1024
	ds_read_b128 v[170:173], v142 offset:2048
	ds_read_b128 v[174:177], v142 offset:3072
	s_mov_b32 s2, 0x87ff
	v_min_u32_sdwa v140, v248, s2 dst_sel:DWORD dst_unused:UNUSED_PAD src0_sel:WORD_0 src1_sel:DWORD
	v_and_b32_e32 v145, 0x7ff, v139
	v_lshl_or_b32 v140, v140, 11, v145
	v_cndmask_b32_e64 v190, v139, v140, s[4:5]
	v_min_u32_sdwa v139, v249, s2 dst_sel:DWORD dst_unused:UNUSED_PAD src0_sel:WORD_0 src1_sel:DWORD
	v_and_b32_e32 v145, 0x7ff, v138
	v_lshl_or_b32 v139, v139, 11, v145
	v_cndmask_b32_e64 v191, v138, v139, s[4:5]
	v_min_u32_sdwa v138, v250, s2 dst_sel:DWORD dst_unused:UNUSED_PAD src0_sel:WORD_0 src1_sel:DWORD
	v_and_b32_e32 v145, 0x7ff, v133
	v_min_u32_sdwa v141, v251, s2 dst_sel:DWORD dst_unused:UNUSED_PAD src0_sel:WORD_0 src1_sel:DWORD
	v_and_b32_e32 v142, 0x7ff, v132
	v_lshl_or_b32 v138, v138, 11, v145
	v_lshl_or_b32 v141, v141, 11, v142
	v_cndmask_b32_e64 v234, v133, v138, s[4:5]
	v_cndmask_b32_e64 v235, v132, v141, s[4:5]
	ds_read_b128 v[178:181], v135
	ds_read_b128 v[182:185], v135 offset:1024
	ds_read_b128 v[186:189], v135 offset:2048
	ds_read_b128 v[194:197], v135 offset:3072
	ds_read_b128 v[198:201], v135 offset:4096
	ds_read_b128 v[202:205], v135 offset:5120
	ds_read_b128 v[206:209], v135 offset:6144
	ds_read_b128 v[210:213], v135 offset:7168
	s_mov_b32 m0, s57
	s_nop 0
	global_load_lds_dwordx4 v133, s[18:19]
	s_nop 0
	s_mov_b32 m0, s58
	s_nop 0
	global_load_lds_dwordx4 v132, s[18:19]
	s_waitcnt vmcnt(8)
	s_waitcnt lgkmcnt(0)
	s_barrier
	s_setprio 1
	s_waitcnt lgkmcnt(0)
	v_mfma_f32_16x16x32_bf16 v[128:131], v[146:149], v[178:181], v[128:131]
	v_mfma_f32_16x16x32_bf16 v[124:127], v[154:157], v[178:181], v[124:127]
	s_waitcnt lgkmcnt(5)
	v_mfma_f32_16x16x32_bf16 v[120:123], v[146:149], v[186:189], v[120:123]
	s_waitcnt lgkmcnt(3)
	v_mfma_f32_16x16x32_bf16 v[106:109], v[154:157], v[198:201], v[106:109]
	s_waitcnt lgkmcnt(1)
	v_mfma_f32_16x16x32_bf16 v[102:105], v[146:149], v[206:209], v[102:105]
	v_mfma_f32_16x16x32_bf16 v[128:131], v[150:153], v[182:185], v[128:131]
	v_mfma_f32_16x16x32_bf16 v[124:127], v[158:161], v[182:185], v[124:127]
	v_mfma_f32_16x16x32_bf16 v[120:123], v[150:153], v[194:197], v[120:123]
	v_mfma_f32_16x16x32_bf16 v[116:119], v[154:157], v[186:189], v[116:119]
	v_mfma_f32_16x16x32_bf16 v[110:113], v[146:149], v[198:201], v[110:113]
	v_mfma_f32_16x16x32_bf16 v[106:109], v[158:161], v[202:205], v[106:109]
	s_waitcnt lgkmcnt(0)
	v_mfma_f32_16x16x32_bf16 v[102:105], v[150:153], v[210:213], v[102:105]
	v_mfma_f32_16x16x32_bf16 v[98:101], v[154:157], v[206:209], v[98:101]
	v_mfma_f32_16x16x32_bf16 v[214:217], v[158:161], v[194:197], v[116:119]
	v_mfma_f32_16x16x32_bf16 v[218:221], v[150:153], v[202:205], v[110:113]
	v_mfma_f32_16x16x32_bf16 v[222:225], v[158:161], v[210:213], v[98:101]
	s_setprio 0
	s_setprio 1
	v_mfma_f32_16x16x32_bf16 v[90:93], v[170:173], v[178:181], v[90:93]
	v_mfma_f32_16x16x32_bf16 v[86:89], v[162:165], v[186:189], v[86:89]
	v_mfma_f32_16x16x32_bf16 v[74:77], v[170:173], v[198:201], v[74:77]
	v_mfma_f32_16x16x32_bf16 v[70:73], v[162:165], v[206:209], v[70:73]
	v_mfma_f32_16x16x32_bf16 v[66:69], v[170:173], v[206:209], v[66:69]
	v_mfma_f32_16x16x32_bf16 v[94:97], v[162:165], v[178:181], v[94:97]
	v_mfma_f32_16x16x32_bf16 v[90:93], v[174:177], v[182:185], v[90:93]
	v_mfma_f32_16x16x32_bf16 v[86:89], v[166:169], v[194:197], v[86:89]
	v_mfma_f32_16x16x32_bf16 v[82:85], v[170:173], v[186:189], v[82:85]
	v_mfma_f32_16x16x32_bf16 v[78:81], v[162:165], v[198:201], v[78:81]
	v_mfma_f32_16x16x32_bf16 v[74:77], v[174:177], v[202:205], v[74:77]
	v_mfma_f32_16x16x32_bf16 v[70:73], v[166:169], v[210:213], v[70:73]
	v_mfma_f32_16x16x32_bf16 v[66:69], v[174:177], v[210:213], v[66:69]
	v_mfma_f32_16x16x32_bf16 v[226:229], v[166:169], v[182:185], v[94:97]
	v_mfma_f32_16x16x32_bf16 v[178:181], v[174:177], v[194:197], v[82:85]
	v_mfma_f32_16x16x32_bf16 v[182:185], v[166:169], v[202:205], v[78:81]
	s_setprio 0
	s_barrier
	s_nop 0
	ds_read_b128 v[78:81], v135 offset:16384
	ds_read_b128 v[82:85], v135 offset:17408
	ds_read_b128 v[94:97], v135 offset:18432
	ds_read_b128 v[98:101], v135 offset:19456
	ds_read_b128 v[110:113], v135 offset:20480
	ds_read_b128 v[116:119], v135 offset:21504
	ds_read_b128 v[186:189], v135 offset:22528
	ds_read_b128 v[194:197], v135 offset:23552
	s_mov_b64 exec, s[100:101]
	s_mov_b32 m0, s41
	s_nop 0
	global_load_lds_dwordx4 v65, s[22:23]
	s_mov_b64 exec, -1
	s_nop 0
	s_mov_b64 exec, s[100:101]
	s_mov_b32 m0, s42
	s_nop 0
	global_load_lds_dwordx4 v114, s[22:23]
	s_mov_b64 exec, -1
	s_add_u32 s2, s22, 0x40000
	s_addc_u32 s3, s23, 0
	s_mov_b64 exec, s[100:101]
	s_mov_b32 m0, s43
	s_nop 0
	global_load_lds_dwordx4 v65, s[2:3]
	s_mov_b64 exec, -1
	s_nop 0
	s_mov_b64 exec, s[100:101]
	s_mov_b32 m0, s44
	s_nop 0
	global_load_lds_dwordx4 v114, s[2:3]
	s_mov_b64 exec, s[100:101]
	s_mov_b64 exec, -1
	s_mov_b32 m0, s40
	s_nop 0
	global_load_lds_dwordx4 v190, s[6:7]
	s_mov_b64 exec, -1
	s_nop 0
	s_mov_b64 exec, s[100:101]
	s_mov_b32 m0, s45
	s_nop 0
	global_load_lds_dwordx4 v191, s[6:7]
	s_mov_b64 exec, -1
	s_waitcnt vmcnt(8)
	s_waitcnt lgkmcnt(0)
	s_barrier
	s_setprio 1
	s_waitcnt lgkmcnt(0)
	v_mfma_f32_16x16x32_bf16 v[60:63], v[146:149], v[78:81], v[60:63]
	s_waitcnt lgkmcnt(5)
	v_mfma_f32_16x16x32_bf16 v[52:55], v[146:149], v[94:97], v[52:55]
	s_waitcnt lgkmcnt(3)
	v_mfma_f32_16x16x32_bf16 v[40:43], v[154:157], v[110:113], v[40:43]
	s_waitcnt lgkmcnt(1)
	v_mfma_f32_16x16x32_bf16 v[36:39], v[146:149], v[186:189], v[36:39]
	v_mfma_f32_16x16x32_bf16 v[60:63], v[150:153], v[82:85], v[60:63]
	v_mfma_f32_16x16x32_bf16 v[56:59], v[154:157], v[78:81], v[56:59]
	v_mfma_f32_16x16x32_bf16 v[52:55], v[150:153], v[98:101], v[52:55]
	v_mfma_f32_16x16x32_bf16 v[48:51], v[154:157], v[94:97], v[48:51]
	v_mfma_f32_16x16x32_bf16 v[44:47], v[146:149], v[110:113], v[44:47]
	v_mfma_f32_16x16x32_bf16 v[40:43], v[158:161], v[116:119], v[40:43]
	s_waitcnt lgkmcnt(0)
	v_mfma_f32_16x16x32_bf16 v[36:39], v[150:153], v[194:197], v[36:39]
	v_mfma_f32_16x16x32_bf16 v[32:35], v[154:157], v[186:189], v[32:35]
	v_mfma_f32_16x16x32_bf16 v[198:201], v[158:161], v[82:85], v[56:59]
	v_mfma_f32_16x16x32_bf16 v[202:205], v[158:161], v[98:101], v[48:51]
	v_mfma_f32_16x16x32_bf16 v[206:209], v[150:153], v[116:119], v[44:47]
	v_mfma_f32_16x16x32_bf16 v[146:149], v[158:161], v[194:197], v[32:35]
	s_setprio 0
	s_setprio 1
	v_mfma_f32_16x16x32_bf16 v[24:27], v[170:173], v[78:81], v[24:27]
	v_mfma_f32_16x16x32_bf16 v[20:23], v[162:165], v[94:97], v[20:23]
	v_mfma_f32_16x16x32_bf16 v[8:11], v[170:173], v[110:113], v[8:11]
	v_mfma_f32_16x16x32_bf16 v[4:7], v[162:165], v[186:189], v[4:7]
	v_mfma_f32_16x16x32_bf16 v[28:31], v[162:165], v[78:81], v[28:31]
	v_mfma_f32_16x16x32_bf16 v[24:27], v[174:177], v[82:85], v[24:27]
	v_mfma_f32_16x16x32_bf16 v[20:23], v[166:169], v[98:101], v[20:23]
	v_mfma_f32_16x16x32_bf16 v[16:19], v[170:173], v[94:97], v[16:19]
	v_mfma_f32_16x16x32_bf16 v[12:15], v[162:165], v[110:113], v[12:15]
	v_mfma_f32_16x16x32_bf16 v[8:11], v[174:177], v[116:119], v[8:11]
	v_mfma_f32_16x16x32_bf16 v[4:7], v[166:169], v[194:197], v[4:7]
	v_mfma_f32_16x16x32_bf16 v[0:3], v[170:173], v[186:189], v[0:3]
	v_mfma_f32_16x16x32_bf16 v[150:153], v[166:169], v[82:85], v[28:31]
	v_mfma_f32_16x16x32_bf16 v[154:157], v[174:177], v[98:101], v[16:19]
	v_mfma_f32_16x16x32_bf16 v[158:161], v[166:169], v[116:119], v[12:15]
	v_mfma_f32_16x16x32_bf16 v[162:165], v[174:177], v[194:197], v[0:3]
	s_setprio 0
	s_barrier
	s_nop 1
	ds_read_b128 v[0:3], v143
	ds_read_b128 v[12:15], v143 offset:1024
	ds_read_b128 v[166:169], v143 offset:2048
	ds_read_b128 v[170:173], v143 offset:3072
	ds_read_b128 v[174:177], v144
	ds_read_b128 v[186:189], v144 offset:1024
	ds_read_b128 v[194:197], v144 offset:2048
	ds_read_b128 v[142:145], v144 offset:3072
	ds_read_b128 v[16:19], v135 offset:32768
	ds_read_b128 v[28:31], v135 offset:33792
	ds_read_b128 v[32:35], v135 offset:34816
	ds_read_b128 v[44:47], v135 offset:35840
	ds_read_b128 v[48:51], v135 offset:36864
	ds_read_b128 v[210:213], v135 offset:37888
	ds_read_b128 v[230:233], v135 offset:38912
	ds_read_b128 v[244:247], v135 offset:39936
	s_mov_b64 exec, s[100:101]
	s_mov_b32 m0, s46
	s_nop 0
	global_load_lds_dwordx4 v234, s[6:7]
	s_mov_b64 exec, -1
	s_nop 0
	s_mov_b64 exec, s[100:101]
	s_mov_b32 m0, s47
	s_nop 0
	global_load_lds_dwordx4 v235, s[6:7]
	s_mov_b64 exec, -1
	s_waitcnt vmcnt(8)
	s_waitcnt lgkmcnt(0)
	s_barrier
	s_setprio 1
	s_waitcnt lgkmcnt(0)
	v_mfma_f32_16x16x32_bf16 v[56:59], v[0:3], v[16:19], v[128:131]
	s_waitcnt lgkmcnt(6)
	v_mfma_f32_16x16x32_bf16 v[128:131], v[12:15], v[28:31], v[56:59]
	v_mfma_f32_16x16x32_bf16 v[56:59], v[166:169], v[16:19], v[124:127]
	v_mfma_f32_16x16x32_bf16 v[116:119], v[170:173], v[28:31], v[56:59]
	s_waitcnt lgkmcnt(5)
	v_mfma_f32_16x16x32_bf16 v[56:59], v[0:3], v[32:35], v[120:123]
	s_waitcnt lgkmcnt(4)
	v_mfma_f32_16x16x32_bf16 v[110:113], v[12:15], v[44:47], v[56:59]
	v_mfma_f32_16x16x32_bf16 v[56:59], v[166:169], v[32:35], v[214:217]
	v_mfma_f32_16x16x32_bf16 v[98:101], v[170:173], v[44:47], v[56:59]
	s_waitcnt lgkmcnt(3)
	v_mfma_f32_16x16x32_bf16 v[56:59], v[0:3], v[48:51], v[218:221]
	s_waitcnt lgkmcnt(2)
	v_mfma_f32_16x16x32_bf16 v[94:97], v[12:15], v[210:213], v[56:59]
	v_mfma_f32_16x16x32_bf16 v[56:59], v[166:169], v[48:51], v[106:109]
	v_mfma_f32_16x16x32_bf16 v[82:85], v[170:173], v[210:213], v[56:59]
	s_waitcnt lgkmcnt(1)
	v_mfma_f32_16x16x32_bf16 v[56:59], v[0:3], v[230:233], v[102:105]
	s_waitcnt lgkmcnt(0)
	v_mfma_f32_16x16x32_bf16 v[78:81], v[12:15], v[244:247], v[56:59]
	v_mfma_f32_16x16x32_bf16 v[56:59], v[166:169], v[230:233], v[222:225]
	v_mfma_f32_16x16x32_bf16 v[56:59], v[170:173], v[244:247], v[56:59]
	s_setprio 0
	s_setprio 1
	v_mfma_f32_16x16x32_bf16 v[102:105], v[174:177], v[16:19], v[226:229]
	v_mfma_f32_16x16x32_bf16 v[16:19], v[194:197], v[16:19], v[90:93]
	v_mfma_f32_16x16x32_bf16 v[120:123], v[142:145], v[28:31], v[16:19]
	v_mfma_f32_16x16x32_bf16 v[16:19], v[174:177], v[32:35], v[86:89]
	v_mfma_f32_16x16x32_bf16 v[106:109], v[186:189], v[44:47], v[16:19]
	v_mfma_f32_16x16x32_bf16 v[16:19], v[194:197], v[32:35], v[178:181]
	v_mfma_f32_16x16x32_bf16 v[124:127], v[186:189], v[28:31], v[102:105]
	v_mfma_f32_16x16x32_bf16 v[102:105], v[142:145], v[44:47], v[16:19]
	v_mfma_f32_16x16x32_bf16 v[16:19], v[174:177], v[48:51], v[182:185]
	v_mfma_f32_16x16x32_bf16 v[90:93], v[186:189], v[210:213], v[16:19]
	v_mfma_f32_16x16x32_bf16 v[16:19], v[194:197], v[48:51], v[74:77]
	v_mfma_f32_16x16x32_bf16 v[86:89], v[142:145], v[210:213], v[16:19]
	v_mfma_f32_16x16x32_bf16 v[16:19], v[174:177], v[230:233], v[70:73]
	v_mfma_f32_16x16x32_bf16 v[74:77], v[186:189], v[244:247], v[16:19]
	v_mfma_f32_16x16x32_bf16 v[16:19], v[194:197], v[230:233], v[66:69]
	v_mfma_f32_16x16x32_bf16 v[70:73], v[142:145], v[244:247], v[16:19]
	s_setprio 0
	s_barrier
	ds_read_b128 v[178:181], v135 offset:49152
	ds_read_b128 v[182:185], v135 offset:50176
	ds_read_b128 v[210:213], v135 offset:51200
	ds_read_b128 v[214:217], v135 offset:52224
	ds_read_b128 v[218:221], v135 offset:53248
	ds_read_b128 v[222:225], v135 offset:54272
	ds_read_b128 v[226:229], v135 offset:55296
	ds_read_b128 v[230:233], v135 offset:56320
	s_add_u32 s2, s22, 0x80
	s_addc_u32 s3, s23, 0
	s_mov_b64 exec, s[100:101]
	s_mov_b32 m0, s51
	s_nop 0
	global_load_lds_dwordx4 v65, s[2:3]
	s_mov_b64 exec, -1
	s_nop 0
	s_mov_b64 exec, s[100:101]
	s_mov_b32 m0, s52
	s_nop 0
	global_load_lds_dwordx4 v114, s[2:3]
	s_mov_b64 exec, -1
	s_add_u32 s2, s22, 0x40080
	s_addc_u32 s3, s23, 0
	s_mov_b64 exec, s[100:101]
	s_mov_b32 m0, s55
	s_nop 0
	global_load_lds_dwordx4 v65, s[2:3]
	s_mov_b64 exec, -1
	s_nop 0
	s_mov_b64 exec, s[100:101]
	s_mov_b32 m0, s56
	s_nop 0
	global_load_lds_dwordx4 v114, s[2:3]
	s_mov_b64 exec, s[100:101]
	s_mov_b64 exec, -1
	s_mov_b32 m0, s53
	s_nop 0
	global_load_lds_dwordx4 v190, s[14:15]
	s_mov_b64 exec, -1
	s_nop 0
	s_mov_b64 exec, s[100:101]
	s_mov_b32 m0, s54
	s_nop 0
	global_load_lds_dwordx4 v191, s[14:15]
	s_mov_b64 exec, -1
	s_waitcnt vmcnt(8)
	s_waitcnt lgkmcnt(0)
	s_barrier
	s_setprio 1
	s_waitcnt lgkmcnt(0)
	v_mfma_f32_16x16x32_bf16 v[16:19], v[0:3], v[178:181], v[60:63]
	s_waitcnt lgkmcnt(6)
	v_mfma_f32_16x16x32_bf16 v[66:69], v[12:15], v[182:185], v[16:19]
	v_mfma_f32_16x16x32_bf16 v[16:19], v[166:169], v[178:181], v[198:201]
	v_mfma_f32_16x16x32_bf16 v[48:51], v[170:173], v[182:185], v[16:19]
	s_waitcnt lgkmcnt(5)
	v_mfma_f32_16x16x32_bf16 v[16:19], v[0:3], v[210:213], v[52:55]
	s_waitcnt lgkmcnt(4)
	v_mfma_f32_16x16x32_bf16 v[44:47], v[12:15], v[214:217], v[16:19]
	v_mfma_f32_16x16x32_bf16 v[16:19], v[166:169], v[210:213], v[202:205]
	v_mfma_f32_16x16x32_bf16 v[32:35], v[170:173], v[214:217], v[16:19]
	s_waitcnt lgkmcnt(3)
	v_mfma_f32_16x16x32_bf16 v[16:19], v[0:3], v[218:221], v[206:209]
	s_waitcnt lgkmcnt(1)
	v_mfma_f32_16x16x32_bf16 v[0:3], v[0:3], v[226:229], v[36:39]
	v_mfma_f32_16x16x32_bf16 v[28:31], v[12:15], v[222:225], v[16:19]
	v_mfma_f32_16x16x32_bf16 v[16:19], v[166:169], v[218:221], v[40:43]
	s_waitcnt lgkmcnt(0)
	v_mfma_f32_16x16x32_bf16 v[12:15], v[12:15], v[230:233], v[0:3]
	v_mfma_f32_16x16x32_bf16 v[0:3], v[166:169], v[226:229], v[146:149]
	v_mfma_f32_16x16x32_bf16 v[16:19], v[170:173], v[222:225], v[16:19]
	v_mfma_f32_16x16x32_bf16 v[0:3], v[170:173], v[230:233], v[0:3]
	s_setprio 0
	s_setprio 1
	v_mfma_f32_16x16x32_bf16 v[20:23], v[174:177], v[210:213], v[20:23]
	v_mfma_f32_16x16x32_bf16 v[36:39], v[174:177], v[178:181], v[150:153]
	v_mfma_f32_16x16x32_bf16 v[40:43], v[186:189], v[214:217], v[20:23]
	v_mfma_f32_16x16x32_bf16 v[20:23], v[194:197], v[210:213], v[154:157]
	v_mfma_f32_16x16x32_bf16 v[60:63], v[186:189], v[182:185], v[36:39]
	v_mfma_f32_16x16x32_bf16 v[24:27], v[194:197], v[178:181], v[24:27]
	v_mfma_f32_16x16x32_bf16 v[36:39], v[142:145], v[214:217], v[20:23]
	v_mfma_f32_16x16x32_bf16 v[20:23], v[174:177], v[218:221], v[158:161]
	v_mfma_f32_16x16x32_bf16 v[8:11], v[194:197], v[218:221], v[8:11]
	v_mfma_f32_16x16x32_bf16 v[4:7], v[174:177], v[226:229], v[4:7]
	v_mfma_f32_16x16x32_bf16 v[52:55], v[142:145], v[182:185], v[24:27]
	v_mfma_f32_16x16x32_bf16 v[24:27], v[186:189], v[222:225], v[20:23]
	v_mfma_f32_16x16x32_bf16 v[20:23], v[142:145], v[222:225], v[8:11]
	v_mfma_f32_16x16x32_bf16 v[8:11], v[186:189], v[230:233], v[4:7]
	v_mfma_f32_16x16x32_bf16 v[4:7], v[194:197], v[226:229], v[162:165]
	v_mfma_f32_16x16x32_bf16 v[4:7], v[142:145], v[230:233], v[4:7]
	s_setprio 0
	s_barrier
	s_andn2_b64 vcc, exec, s[16:17]
	s_cbranch_vccnz .LBB0_1428
	s_barrier

.LBB0_1501:
	s_add_i32 s59, s59, 1
	v_readlane_b32 s0, v254, 38
	s_mul_i32 s0, s59, s0
	s_mul_hi_u32 s1, s59, s70
	s_add_i32 s1, s1, s0
	s_mul_i32 s0, s59, s70
	v_readlane_b32 s4, v255, 0
	s_add_u32 s0, s0, s4
	s_addc_u32 s1, s1, s49
	v_mov_b64_e32 v[0:1], s[30:31]
	v_cmp_ge_i64_e32 vcc, s[0:1], v[0:1]
	v_cmp_lt_i64_e64 s[4:5], s[0:1], v[0:1]
	s_nop 3
	s_cmp_lg_u64 s[4:5], 0
	s_cselect_b64 s[100:101], -1, 1
	s_cbranch_vccnz .LBB0_1503
	s_ashr_i32 s1, s0, 31
	s_lshr_b32 s1, s1, 29
	s_add_i32 s1, s0, s1
	s_ashr_i32 s12, s1, 3
	s_and_b32 s1, s1, -8
	s_sub_i32 s0, s0, s1
	s_lshr_b32 s1, s0, 31
	s_or_b32 s1, s48, s1
	s_mul_i32 s0, s1, s0
	s_add_i32 s0, s0, s12
	s_ashr_i32 s1, s0, 31
	s_lshr_b32 s1, s1, 27
	s_add_i32 s1, s0, s1
	s_ashr_i32 s12, s1, 5
	s_lshl_b32 s13, s12, 3
	s_sub_i32 s12, s29, s13
	s_min_i32 s14, s12, 8
	s_abs_i32 s12, s14
	v_cvt_f32_u32_e32 v0, s12
	s_sub_i32 s16, 0, s12
	s_andn2_b32 s1, s1, 31
	s_sub_i32 s0, s0, s1
	v_rcp_iflag_f32_e32 v0, v0
	s_abs_i32 s1, s0
	s_xor_b32 s15, s0, s14
	s_ashr_i32 s15, s15, 31
	v_mul_f32_e32 v0, 0x4f7ffffe, v0
	v_cvt_u32_f32_e32 v0, v0
	s_nop 0
	v_readfirstlane_b32 s17, v0
	s_mul_i32 s16, s16, s17
	s_mul_hi_u32 s16, s17, s16
	s_add_i32 s17, s17, s16
	s_mul_hi_u32 s16, s1, s17
	s_mul_i32 s17, s16, s12
	s_sub_i32 s1, s1, s17
	s_add_i32 s18, s16, 1
	s_sub_i32 s17, s1, s12
	s_cmp_ge_u32 s1, s12
	s_cselect_b32 s16, s18, s16
	s_cselect_b32 s1, s17, s1
	s_add_i32 s17, s16, 1
	s_cmp_ge_u32 s1, s12
	s_cselect_b32 s1, s17, s16
	s_xor_b32 s1, s1, s15
	s_sub_i32 s12, s1, s15
	s_mul_i32 s1, s12, s14
	s_sub_i32 s0, s0, s1
	s_add_i32 s14, s0, s13

.LBB0_1506:
	s_add_u32 s61, s22, s18
	s_addc_u32 s66, s23, s19
	v_add_u32_e32 v132, 0x10000, v142
	v_add_u32_e32 v133, 0x14000, v142
	s_add_u32 s34, s61, 0x100
	ds_read_b128 v[134:137], v132
	ds_read_b128 v[144:147], v132 offset:1024
	ds_read_b128 v[148:151], v132 offset:2048
	ds_read_b128 v[152:155], v132 offset:3072
	ds_read_b128 v[156:159], v133
	ds_read_b128 v[160:163], v133 offset:1024
	ds_read_b128 v[164:167], v133 offset:2048
	ds_read_b128 v[168:171], v133 offset:3072
	s_addc_u32 s35, s66, 0
	s_add_u32 s26, s61, 0x180
	s_addc_u32 s27, s66, 0
	s_add_u32 s15, s24, s18
	s_addc_u32 s33, s25, s19
	s_add_u32 s62, s15, 0x100
	s_addc_u32 s63, s33, 0
	ds_read_b128 v[172:175], v143
	ds_read_b128 v[176:179], v143 offset:1024
	ds_read_b128 v[180:183], v143 offset:2048
	ds_read_b128 v[184:187], v143 offset:3072
	ds_read_b128 v[188:191], v143 offset:4096
	ds_read_b128 v[194:197], v143 offset:5120
	ds_read_b128 v[198:201], v143 offset:6144
	ds_read_b128 v[202:205], v143 offset:7168
	s_add_u32 s64, s61, 0x40080
	s_addc_u32 s65, s66, 0
	s_mov_b32 m0, s57
	s_nop 0
	global_load_lds_dwordx4 v65, s[64:65]
	s_nop 0
	s_mov_b32 m0, s58
	s_nop 0
	global_load_lds_dwordx4 v140, s[64:65]
	s_waitcnt vmcnt(8)
	s_waitcnt lgkmcnt(0)
	s_barrier
	s_setprio 1
	s_waitcnt lgkmcnt(0)
	v_mfma_f32_16x16x32_bf16 v[128:131], v[134:137], v[172:175], v[128:131]
	v_mfma_f32_16x16x32_bf16 v[124:127], v[148:151], v[172:175], v[124:127]
	s_waitcnt lgkmcnt(5)
	v_mfma_f32_16x16x32_bf16 v[120:123], v[134:137], v[180:183], v[120:123]
	v_mfma_f32_16x16x32_bf16 v[116:119], v[148:151], v[180:183], v[116:119]
	s_waitcnt lgkmcnt(3)
	v_mfma_f32_16x16x32_bf16 v[110:113], v[134:137], v[188:191], v[110:113]
	v_mfma_f32_16x16x32_bf16 v[106:109], v[148:151], v[188:191], v[106:109]
	s_waitcnt lgkmcnt(1)
	v_mfma_f32_16x16x32_bf16 v[102:105], v[134:137], v[198:201], v[102:105]
	v_mfma_f32_16x16x32_bf16 v[98:101], v[148:151], v[198:201], v[98:101]
	v_mfma_f32_16x16x32_bf16 v[128:131], v[144:147], v[176:179], v[128:131]
	v_mfma_f32_16x16x32_bf16 v[124:127], v[152:155], v[176:179], v[124:127]
	v_mfma_f32_16x16x32_bf16 v[120:123], v[144:147], v[184:187], v[120:123]
	v_mfma_f32_16x16x32_bf16 v[116:119], v[152:155], v[184:187], v[116:119]
	v_mfma_f32_16x16x32_bf16 v[110:113], v[144:147], v[194:197], v[110:113]
	v_mfma_f32_16x16x32_bf16 v[106:109], v[152:155], v[194:197], v[106:109]
	s_waitcnt lgkmcnt(0)
	v_mfma_f32_16x16x32_bf16 v[102:105], v[144:147], v[202:205], v[102:105]
	v_mfma_f32_16x16x32_bf16 v[98:101], v[152:155], v[202:205], v[98:101]
	s_setprio 0
	s_setprio 1
	v_mfma_f32_16x16x32_bf16 v[94:97], v[156:159], v[172:175], v[94:97]
	v_mfma_f32_16x16x32_bf16 v[90:93], v[164:167], v[172:175], v[90:93]
	v_mfma_f32_16x16x32_bf16 v[86:89], v[156:159], v[180:183], v[86:89]
	v_mfma_f32_16x16x32_bf16 v[82:85], v[164:167], v[180:183], v[82:85]
	v_mfma_f32_16x16x32_bf16 v[78:81], v[156:159], v[188:191], v[78:81]
	v_mfma_f32_16x16x32_bf16 v[74:77], v[164:167], v[188:191], v[74:77]
	v_mfma_f32_16x16x32_bf16 v[70:73], v[156:159], v[198:201], v[70:73]
	v_mfma_f32_16x16x32_bf16 v[66:69], v[164:167], v[198:201], v[66:69]
	v_mfma_f32_16x16x32_bf16 v[94:97], v[160:163], v[176:179], v[94:97]
	v_mfma_f32_16x16x32_bf16 v[90:93], v[168:171], v[176:179], v[90:93]
	v_mfma_f32_16x16x32_bf16 v[86:89], v[160:163], v[184:187], v[86:89]
	v_mfma_f32_16x16x32_bf16 v[82:85], v[168:171], v[184:187], v[82:85]
	v_mfma_f32_16x16x32_bf16 v[78:81], v[160:163], v[194:197], v[78:81]
	v_mfma_f32_16x16x32_bf16 v[74:77], v[168:171], v[194:197], v[74:77]
	v_mfma_f32_16x16x32_bf16 v[70:73], v[160:163], v[202:205], v[70:73]
	v_mfma_f32_16x16x32_bf16 v[66:69], v[168:171], v[202:205], v[66:69]
	s_setprio 0
	s_barrier
	ds_read_b128 v[172:175], v143 offset:16384
	ds_read_b128 v[176:179], v143 offset:17408
	ds_read_b128 v[180:183], v143 offset:18432
	ds_read_b128 v[184:187], v143 offset:19456
	ds_read_b128 v[188:191], v143 offset:20480
	ds_read_b128 v[194:197], v143 offset:21504
	ds_read_b128 v[198:201], v143 offset:22528
	ds_read_b128 v[202:205], v143 offset:23552
	s_mov_b32 m0, s41
	s_nop 0
	global_load_lds_dwordx4 v114, s[62:63]
	s_nop 0
	s_mov_b32 m0, s42
	s_nop 0
	global_load_lds_dwordx4 v141, s[62:63]
	s_add_u32 s62, s15, 0x40100
	s_addc_u32 s63, s33, 0
	s_mov_b32 m0, s43
	s_nop 0
	global_load_lds_dwordx4 v114, s[62:63]
	s_nop 0
	s_mov_b32 m0, s44
	s_nop 0
	global_load_lds_dwordx4 v141, s[62:63]
	s_mov_b32 m0, s40
	s_nop 0
	global_load_lds_dwordx4 v65, s[34:35]
	s_nop 0
	s_mov_b32 m0, s45
	s_nop 0
	global_load_lds_dwordx4 v140, s[34:35]
	s_waitcnt vmcnt(8)
	s_waitcnt lgkmcnt(0)
	s_barrier
	s_setprio 1
	s_waitcnt lgkmcnt(0)
	v_mfma_f32_16x16x32_bf16 v[60:63], v[134:137], v[172:175], v[60:63]
	v_mfma_f32_16x16x32_bf16 v[56:59], v[148:151], v[172:175], v[56:59]
	s_waitcnt lgkmcnt(5)
	v_mfma_f32_16x16x32_bf16 v[52:55], v[134:137], v[180:183], v[52:55]
	v_mfma_f32_16x16x32_bf16 v[48:51], v[148:151], v[180:183], v[48:51]
	s_waitcnt lgkmcnt(3)
	v_mfma_f32_16x16x32_bf16 v[44:47], v[134:137], v[188:191], v[44:47]
	v_mfma_f32_16x16x32_bf16 v[40:43], v[148:151], v[188:191], v[40:43]
	s_waitcnt lgkmcnt(1)
	v_mfma_f32_16x16x32_bf16 v[36:39], v[134:137], v[198:201], v[36:39]
	v_mfma_f32_16x16x32_bf16 v[32:35], v[148:151], v[198:201], v[32:35]
	v_mfma_f32_16x16x32_bf16 v[60:63], v[144:147], v[176:179], v[60:63]
	v_mfma_f32_16x16x32_bf16 v[56:59], v[152:155], v[176:179], v[56:59]
	v_mfma_f32_16x16x32_bf16 v[52:55], v[144:147], v[184:187], v[52:55]
	v_mfma_f32_16x16x32_bf16 v[48:51], v[152:155], v[184:187], v[48:51]
	v_mfma_f32_16x16x32_bf16 v[44:47], v[144:147], v[194:197], v[44:47]
	v_mfma_f32_16x16x32_bf16 v[40:43], v[152:155], v[194:197], v[40:43]
	s_waitcnt lgkmcnt(0)
	v_mfma_f32_16x16x32_bf16 v[36:39], v[144:147], v[202:205], v[36:39]
	v_mfma_f32_16x16x32_bf16 v[32:35], v[152:155], v[202:205], v[32:35]
	s_setprio 0
	s_setprio 1
	v_mfma_f32_16x16x32_bf16 v[28:31], v[156:159], v[172:175], v[28:31]
	v_mfma_f32_16x16x32_bf16 v[24:27], v[164:167], v[172:175], v[24:27]
	v_mfma_f32_16x16x32_bf16 v[20:23], v[156:159], v[180:183], v[20:23]
	v_mfma_f32_16x16x32_bf16 v[16:19], v[164:167], v[180:183], v[16:19]
	v_mfma_f32_16x16x32_bf16 v[12:15], v[156:159], v[188:191], v[12:15]
	v_mfma_f32_16x16x32_bf16 v[8:11], v[164:167], v[188:191], v[8:11]
	v_mfma_f32_16x16x32_bf16 v[4:7], v[156:159], v[198:201], v[4:7]
	v_mfma_f32_16x16x32_bf16 v[0:3], v[164:167], v[198:201], v[0:3]
	v_mfma_f32_16x16x32_bf16 v[28:31], v[160:163], v[176:179], v[28:31]
	v_mfma_f32_16x16x32_bf16 v[24:27], v[168:171], v[176:179], v[24:27]
	v_mfma_f32_16x16x32_bf16 v[20:23], v[160:163], v[184:187], v[20:23]
	v_mfma_f32_16x16x32_bf16 v[16:19], v[168:171], v[184:187], v[16:19]
	v_mfma_f32_16x16x32_bf16 v[12:15], v[160:163], v[194:197], v[12:15]
	v_mfma_f32_16x16x32_bf16 v[8:11], v[168:171], v[194:197], v[8:11]
	v_mfma_f32_16x16x32_bf16 v[4:7], v[160:163], v[202:205], v[4:7]
	v_mfma_f32_16x16x32_bf16 v[0:3], v[168:171], v[202:205], v[0:3]
	s_setprio 0
	s_barrier
	v_add_u32_e32 v134, 0x18000, v142
	v_add_u32_e32 v135, 0x1c000, v142
	ds_read_b128 v[136:139], v134
	ds_read_b128 v[144:147], v134 offset:1024
	ds_read_b128 v[148:151], v134 offset:2048
	ds_read_b128 v[152:155], v134 offset:3072
	ds_read_b128 v[156:159], v135
	ds_read_b128 v[160:163], v135 offset:1024
	ds_read_b128 v[164:167], v135 offset:2048
	ds_read_b128 v[168:171], v135 offset:3072
	ds_read_b128 v[172:175], v143 offset:32768
	ds_read_b128 v[176:179], v143 offset:33792
	ds_read_b128 v[180:183], v143 offset:34816
	ds_read_b128 v[184:187], v143 offset:35840
	ds_read_b128 v[188:191], v143 offset:36864
	ds_read_b128 v[194:197], v143 offset:37888
	ds_read_b128 v[198:201], v143 offset:38912
	ds_read_b128 v[202:205], v143 offset:39936
	s_add_u32 s34, s61, 0x40100
	s_addc_u32 s35, s66, 0
	s_mov_b32 m0, s46
	s_nop 0
	global_load_lds_dwordx4 v65, s[34:35]
	s_nop 0
	s_mov_b32 m0, s47
	s_nop 0
	global_load_lds_dwordx4 v140, s[34:35]
	s_waitcnt vmcnt(8)
	s_waitcnt lgkmcnt(0)
	s_barrier
	s_setprio 1
	s_waitcnt lgkmcnt(0)
	v_mfma_f32_16x16x32_bf16 v[128:131], v[136:139], v[172:175], v[128:131]
	v_mfma_f32_16x16x32_bf16 v[124:127], v[148:151], v[172:175], v[124:127]
	s_waitcnt lgkmcnt(5)
	v_mfma_f32_16x16x32_bf16 v[120:123], v[136:139], v[180:183], v[120:123]
	v_mfma_f32_16x16x32_bf16 v[116:119], v[148:151], v[180:183], v[116:119]
	s_waitcnt lgkmcnt(3)
	v_mfma_f32_16x16x32_bf16 v[110:113], v[136:139], v[188:191], v[110:113]
	v_mfma_f32_16x16x32_bf16 v[106:109], v[148:151], v[188:191], v[106:109]
	s_waitcnt lgkmcnt(1)
	v_mfma_f32_16x16x32_bf16 v[102:105], v[136:139], v[198:201], v[102:105]
	v_mfma_f32_16x16x32_bf16 v[98:101], v[148:151], v[198:201], v[98:101]
	v_mfma_f32_16x16x32_bf16 v[128:131], v[144:147], v[176:179], v[128:131]
	v_mfma_f32_16x16x32_bf16 v[124:127], v[152:155], v[176:179], v[124:127]
	v_mfma_f32_16x16x32_bf16 v[120:123], v[144:147], v[184:187], v[120:123]
	v_mfma_f32_16x16x32_bf16 v[116:119], v[152:155], v[184:187], v[116:119]
	v_mfma_f32_16x16x32_bf16 v[110:113], v[144:147], v[194:197], v[110:113]
	v_mfma_f32_16x16x32_bf16 v[106:109], v[152:155], v[194:197], v[106:109]
	s_waitcnt lgkmcnt(0)
	v_mfma_f32_16x16x32_bf16 v[102:105], v[144:147], v[202:205], v[102:105]
	v_mfma_f32_16x16x32_bf16 v[98:101], v[152:155], v[202:205], v[98:101]
	s_setprio 0
	s_setprio 1
	v_mfma_f32_16x16x32_bf16 v[94:97], v[156:159], v[172:175], v[94:97]
	v_mfma_f32_16x16x32_bf16 v[90:93], v[164:167], v[172:175], v[90:93]
	v_mfma_f32_16x16x32_bf16 v[86:89], v[156:159], v[180:183], v[86:89]
	v_mfma_f32_16x16x32_bf16 v[82:85], v[164:167], v[180:183], v[82:85]
	v_mfma_f32_16x16x32_bf16 v[78:81], v[156:159], v[188:191], v[78:81]
	v_mfma_f32_16x16x32_bf16 v[74:77], v[164:167], v[188:191], v[74:77]
	v_mfma_f32_16x16x32_bf16 v[70:73], v[156:159], v[198:201], v[70:73]
	v_mfma_f32_16x16x32_bf16 v[66:69], v[164:167], v[198:201], v[66:69]
	v_mfma_f32_16x16x32_bf16 v[94:97], v[160:163], v[176:179], v[94:97]
	v_mfma_f32_16x16x32_bf16 v[90:93], v[168:171], v[176:179], v[90:93]
	v_mfma_f32_16x16x32_bf16 v[86:89], v[160:163], v[184:187], v[86:89]
	v_mfma_f32_16x16x32_bf16 v[82:85], v[168:171], v[184:187], v[82:85]
	v_mfma_f32_16x16x32_bf16 v[78:81], v[160:163], v[194:197], v[78:81]
	v_mfma_f32_16x16x32_bf16 v[74:77], v[168:171], v[194:197], v[74:77]
	v_mfma_f32_16x16x32_bf16 v[70:73], v[160:163], v[202:205], v[70:73]
	v_mfma_f32_16x16x32_bf16 v[66:69], v[168:171], v[202:205], v[66:69]
	s_setprio 0
	s_barrier
	ds_read_b128 v[172:175], v143 offset:49152
	ds_read_b128 v[176:179], v143 offset:50176
	ds_read_b128 v[180:183], v143 offset:51200
	ds_read_b128 v[184:187], v143 offset:52224
	ds_read_b128 v[188:191], v143 offset:53248
	ds_read_b128 v[194:197], v143 offset:54272
	ds_read_b128 v[198:201], v143 offset:55296
	ds_read_b128 v[202:205], v143 offset:56320
	s_add_u32 s34, s15, 0x180
	s_addc_u32 s35, s33, 0
	s_mov_b32 m0, s51
	s_nop 0
	global_load_lds_dwordx4 v114, s[34:35]
	s_nop 0
	s_mov_b32 m0, s52
	s_nop 0
	global_load_lds_dwordx4 v141, s[34:35]
	s_add_u32 s34, s15, 0x40180
	s_addc_u32 s35, s33, 0
	s_mov_b32 m0, s55
	s_nop 0
	global_load_lds_dwordx4 v114, s[34:35]
	s_nop 0
	s_mov_b32 m0, s56
	s_nop 0
	global_load_lds_dwordx4 v141, s[34:35]
	s_nop 0
	s_mov_b32 m0, s53
	s_nop 0
	global_load_lds_dwordx4 v65, s[26:27]
	s_nop 0
	s_mov_b32 m0, s54
	s_nop 0
	global_load_lds_dwordx4 v140, s[26:27]
	s_waitcnt vmcnt(8)
	s_waitcnt lgkmcnt(0)
	s_barrier
	s_setprio 1
	s_waitcnt lgkmcnt(0)
	v_mfma_f32_16x16x32_bf16 v[60:63], v[136:139], v[172:175], v[60:63]
	v_mfma_f32_16x16x32_bf16 v[56:59], v[148:151], v[172:175], v[56:59]
	s_waitcnt lgkmcnt(5)
	v_mfma_f32_16x16x32_bf16 v[52:55], v[136:139], v[180:183], v[52:55]
	v_mfma_f32_16x16x32_bf16 v[48:51], v[148:151], v[180:183], v[48:51]
	s_waitcnt lgkmcnt(3)
	v_mfma_f32_16x16x32_bf16 v[44:47], v[136:139], v[188:191], v[44:47]
	v_mfma_f32_16x16x32_bf16 v[40:43], v[148:151], v[188:191], v[40:43]
	s_waitcnt lgkmcnt(1)
	v_mfma_f32_16x16x32_bf16 v[36:39], v[136:139], v[198:201], v[36:39]
	v_mfma_f32_16x16x32_bf16 v[32:35], v[148:151], v[198:201], v[32:35]
	v_mfma_f32_16x16x32_bf16 v[60:63], v[144:147], v[176:179], v[60:63]
	v_mfma_f32_16x16x32_bf16 v[56:59], v[152:155], v[176:179], v[56:59]
	v_mfma_f32_16x16x32_bf16 v[52:55], v[144:147], v[184:187], v[52:55]
	v_mfma_f32_16x16x32_bf16 v[48:51], v[152:155], v[184:187], v[48:51]
	v_mfma_f32_16x16x32_bf16 v[44:47], v[144:147], v[194:197], v[44:47]
	v_mfma_f32_16x16x32_bf16 v[40:43], v[152:155], v[194:197], v[40:43]
	s_waitcnt lgkmcnt(0)
	v_mfma_f32_16x16x32_bf16 v[36:39], v[144:147], v[202:205], v[36:39]
	v_mfma_f32_16x16x32_bf16 v[32:35], v[152:155], v[202:205], v[32:35]
	s_setprio 0
	s_setprio 1
	v_mfma_f32_16x16x32_bf16 v[28:31], v[156:159], v[172:175], v[28:31]
	v_mfma_f32_16x16x32_bf16 v[24:27], v[164:167], v[172:175], v[24:27]
	v_mfma_f32_16x16x32_bf16 v[20:23], v[156:159], v[180:183], v[20:23]
	v_mfma_f32_16x16x32_bf16 v[16:19], v[164:167], v[180:183], v[16:19]
	v_mfma_f32_16x16x32_bf16 v[12:15], v[156:159], v[188:191], v[12:15]
	v_mfma_f32_16x16x32_bf16 v[8:11], v[164:167], v[188:191], v[8:11]
	v_mfma_f32_16x16x32_bf16 v[4:7], v[156:159], v[198:201], v[4:7]
	v_mfma_f32_16x16x32_bf16 v[0:3], v[164:167], v[198:201], v[0:3]
	v_mfma_f32_16x16x32_bf16 v[28:31], v[160:163], v[176:179], v[28:31]
	v_mfma_f32_16x16x32_bf16 v[24:27], v[168:171], v[176:179], v[24:27]
	v_mfma_f32_16x16x32_bf16 v[20:23], v[160:163], v[184:187], v[20:23]
	v_mfma_f32_16x16x32_bf16 v[16:19], v[168:171], v[184:187], v[16:19]
	v_mfma_f32_16x16x32_bf16 v[12:15], v[160:163], v[194:197], v[12:15]
	v_mfma_f32_16x16x32_bf16 v[8:11], v[168:171], v[194:197], v[8:11]
	v_mfma_f32_16x16x32_bf16 v[4:7], v[160:163], v[202:205], v[4:7]
	v_mfma_f32_16x16x32_bf16 v[0:3], v[168:171], v[202:205], v[0:3]
	s_setprio 0
	s_barrier
	s_add_i32 s13, s13, 2
	s_add_u32 s18, s18, 0x100
	s_addc_u32 s19, s19, 0
	s_cmp_lt_u32 s13, 12
	s_cbranch_scc1 .LBB0_1506
	ds_read_b128 v[136:139], v132
	ds_read_b128 v[144:147], v132 offset:1024
	ds_read_b128 v[148:151], v132 offset:2048
	ds_read_b128 v[152:155], v132 offset:3072
	ds_read_b128 v[156:159], v133
	ds_read_b128 v[160:163], v133 offset:1024
	ds_read_b128 v[164:167], v133 offset:2048
	ds_read_b128 v[168:171], v133 offset:3072
	s_ashr_i32 s15, s14, 31
	s_lshl_b64 s[18:19], s[14:15], 19
	s_add_u32 s18, s36, s18
	s_addc_u32 s19, s37, s19
	s_and_b64 s[4:5], s[4:5], exec
	s_cselect_b32 s24, s18, s22
	s_cselect_b32 s25, s19, s23
	s_add_u32 s4, s24, 0x80
	s_addc_u32 s5, s25, 0
	ds_read_b128 v[172:175], v143
	ds_read_b128 v[176:179], v143 offset:1024
	ds_read_b128 v[180:183], v143 offset:2048
	ds_read_b128 v[184:187], v143 offset:3072
	ds_read_b128 v[188:191], v143 offset:4096
	ds_read_b128 v[194:197], v143 offset:5120
	ds_read_b128 v[198:201], v143 offset:6144
	ds_read_b128 v[202:205], v143 offset:7168
	s_add_u32 s22, s22, 0x40780
	s_addc_u32 s23, s23, 0
	s_mov_b32 m0, s57
	s_nop 0
	global_load_lds_dwordx4 v65, s[22:23]
	s_nop 0
	s_mov_b32 m0, s58
	s_nop 0
	global_load_lds_dwordx4 v140, s[22:23]
	s_waitcnt vmcnt(8)
	s_waitcnt lgkmcnt(0)
	s_barrier
	s_setprio 1
	s_waitcnt lgkmcnt(0)
	v_mfma_f32_16x16x32_bf16 v[128:131], v[136:139], v[172:175], v[128:131]
	v_mfma_f32_16x16x32_bf16 v[124:127], v[148:151], v[172:175], v[124:127]
	s_waitcnt lgkmcnt(3)
	v_mfma_f32_16x16x32_bf16 v[110:113], v[136:139], v[188:191], v[110:113]
	v_mfma_f32_16x16x32_bf16 v[106:109], v[148:151], v[188:191], v[106:109]
	v_mfma_f32_16x16x32_bf16 v[128:131], v[144:147], v[176:179], v[128:131]
	v_mfma_f32_16x16x32_bf16 v[124:127], v[152:155], v[176:179], v[124:127]
	v_mfma_f32_16x16x32_bf16 v[120:123], v[136:139], v[180:183], v[120:123]
	v_mfma_f32_16x16x32_bf16 v[116:119], v[148:151], v[180:183], v[116:119]
	s_waitcnt lgkmcnt(2)
	v_mfma_f32_16x16x32_bf16 v[110:113], v[144:147], v[194:197], v[110:113]
	v_mfma_f32_16x16x32_bf16 v[106:109], v[152:155], v[194:197], v[106:109]
	s_waitcnt lgkmcnt(1)
	v_mfma_f32_16x16x32_bf16 v[102:105], v[136:139], v[198:201], v[102:105]
	v_mfma_f32_16x16x32_bf16 v[98:101], v[148:151], v[198:201], v[98:101]
	v_mfma_f32_16x16x32_bf16 v[206:209], v[144:147], v[184:187], v[120:123]
	v_mfma_f32_16x16x32_bf16 v[210:213], v[152:155], v[184:187], v[116:119]
	s_waitcnt lgkmcnt(0)
	v_mfma_f32_16x16x32_bf16 v[214:217], v[144:147], v[202:205], v[102:105]
	v_mfma_f32_16x16x32_bf16 v[218:221], v[152:155], v[202:205], v[98:101]
	s_setprio 0
	s_setprio 1
	v_mfma_f32_16x16x32_bf16 v[94:97], v[156:159], v[172:175], v[94:97]
	v_mfma_f32_16x16x32_bf16 v[90:93], v[164:167], v[172:175], v[90:93]
	v_mfma_f32_16x16x32_bf16 v[70:73], v[156:159], v[198:201], v[70:73]
	v_mfma_f32_16x16x32_bf16 v[66:69], v[164:167], v[198:201], v[66:69]
	v_mfma_f32_16x16x32_bf16 v[94:97], v[160:163], v[176:179], v[94:97]
	v_mfma_f32_16x16x32_bf16 v[90:93], v[168:171], v[176:179], v[90:93]
	v_mfma_f32_16x16x32_bf16 v[86:89], v[156:159], v[180:183], v[86:89]
	v_mfma_f32_16x16x32_bf16 v[82:85], v[164:167], v[180:183], v[82:85]
	v_mfma_f32_16x16x32_bf16 v[78:81], v[156:159], v[188:191], v[78:81]
	v_mfma_f32_16x16x32_bf16 v[74:77], v[164:167], v[188:191], v[74:77]
	v_mfma_f32_16x16x32_bf16 v[70:73], v[160:163], v[202:205], v[70:73]
	v_mfma_f32_16x16x32_bf16 v[66:69], v[168:171], v[202:205], v[66:69]
	v_mfma_f32_16x16x32_bf16 v[172:175], v[160:163], v[184:187], v[86:89]
	v_mfma_f32_16x16x32_bf16 v[176:179], v[168:171], v[184:187], v[82:85]
	v_mfma_f32_16x16x32_bf16 v[180:183], v[160:163], v[194:197], v[78:81]
	v_mfma_f32_16x16x32_bf16 v[184:187], v[168:171], v[194:197], v[74:77]
	s_setprio 0
	s_barrier
	s_nop 0
	ds_read_b128 v[74:77], v143 offset:16384
	ds_read_b128 v[78:81], v143 offset:17408
	ds_read_b128 v[82:85], v143 offset:18432
	ds_read_b128 v[86:89], v143 offset:19456
	ds_read_b128 v[98:101], v143 offset:20480
	ds_read_b128 v[102:105], v143 offset:21504
	ds_read_b128 v[116:119], v143 offset:22528
	ds_read_b128 v[120:123], v143 offset:23552
	s_mov_b64 exec, s[100:101]
	s_mov_b32 m0, s41
	s_nop 0
	global_load_lds_dwordx4 v114, s[16:17]
	s_mov_b64 exec, -1
	s_add_u32 s22, s16, 0x40000
	s_mov_b64 exec, s[100:101]
	s_mov_b32 m0, s42
	s_nop 0
	global_load_lds_dwordx4 v141, s[16:17]
	s_mov_b64 exec, -1
	s_addc_u32 s23, s17, 0
	s_mov_b64 exec, s[100:101]
	s_mov_b32 m0, s43
	s_nop 0
	global_load_lds_dwordx4 v114, s[22:23]
	s_mov_b64 exec, -1
	s_nop 0
	s_mov_b64 exec, s[100:101]
	s_mov_b32 m0, s44
	s_nop 0
	global_load_lds_dwordx4 v141, s[22:23]
	s_mov_b64 exec, -1
	s_nop 0
	s_mov_b64 exec, s[100:101]
	s_mov_b32 m0, s40
	s_nop 0
	global_load_lds_dwordx4 v65, s[24:25]
	s_mov_b64 exec, -1
	s_nop 0
	s_mov_b64 exec, s[100:101]
	s_mov_b32 m0, s45
	s_nop 0
	global_load_lds_dwordx4 v140, s[24:25]
	s_mov_b64 exec, -1
	s_waitcnt vmcnt(8)
	s_waitcnt lgkmcnt(0)
	s_barrier
	s_setprio 1
	s_waitcnt lgkmcnt(0)
	v_mfma_f32_16x16x32_bf16 v[52:55], v[136:139], v[82:85], v[52:55]
	v_mfma_f32_16x16x32_bf16 v[48:51], v[148:151], v[82:85], v[48:51]
	s_waitcnt lgkmcnt(1)
	v_mfma_f32_16x16x32_bf16 v[36:39], v[136:139], v[116:119], v[36:39]
	v_mfma_f32_16x16x32_bf16 v[32:35], v[148:151], v[116:119], v[32:35]
	v_mfma_f32_16x16x32_bf16 v[60:63], v[136:139], v[74:77], v[60:63]
	v_mfma_f32_16x16x32_bf16 v[56:59], v[148:151], v[74:77], v[56:59]
	v_mfma_f32_16x16x32_bf16 v[52:55], v[144:147], v[86:89], v[52:55]
	v_mfma_f32_16x16x32_bf16 v[48:51], v[152:155], v[86:89], v[48:51]
	v_mfma_f32_16x16x32_bf16 v[44:47], v[136:139], v[98:101], v[44:47]
	v_mfma_f32_16x16x32_bf16 v[40:43], v[148:151], v[98:101], v[40:43]
	s_waitcnt lgkmcnt(0)
	v_mfma_f32_16x16x32_bf16 v[36:39], v[144:147], v[120:123], v[36:39]
	v_mfma_f32_16x16x32_bf16 v[32:35], v[152:155], v[120:123], v[32:35]
	v_mfma_f32_16x16x32_bf16 v[188:191], v[144:147], v[78:81], v[60:63]
	v_mfma_f32_16x16x32_bf16 v[194:197], v[152:155], v[78:81], v[56:59]
	v_mfma_f32_16x16x32_bf16 v[198:201], v[144:147], v[102:105], v[44:47]
	v_mfma_f32_16x16x32_bf16 v[202:205], v[152:155], v[102:105], v[40:43]
	s_setprio 0
	s_setprio 1
	v_mfma_f32_16x16x32_bf16 v[20:23], v[156:159], v[82:85], v[20:23]
	v_mfma_f32_16x16x32_bf16 v[16:19], v[164:167], v[82:85], v[16:19]
	v_mfma_f32_16x16x32_bf16 v[12:15], v[156:159], v[98:101], v[12:15]
	v_mfma_f32_16x16x32_bf16 v[8:11], v[164:167], v[98:101], v[8:11]
	v_mfma_f32_16x16x32_bf16 v[28:31], v[156:159], v[74:77], v[28:31]
	v_mfma_f32_16x16x32_bf16 v[24:27], v[164:167], v[74:77], v[24:27]
	v_mfma_f32_16x16x32_bf16 v[20:23], v[160:163], v[86:89], v[20:23]
	v_mfma_f32_16x16x32_bf16 v[16:19], v[168:171], v[86:89], v[16:19]
	v_mfma_f32_16x16x32_bf16 v[12:15], v[160:163], v[102:105], v[12:15]
	v_mfma_f32_16x16x32_bf16 v[8:11], v[168:171], v[102:105], v[8:11]
	v_mfma_f32_16x16x32_bf16 v[4:7], v[156:159], v[116:119], v[4:7]
	v_mfma_f32_16x16x32_bf16 v[0:3], v[164:167], v[116:119], v[0:3]
	v_mfma_f32_16x16x32_bf16 v[136:139], v[160:163], v[78:81], v[28:31]
	v_mfma_f32_16x16x32_bf16 v[144:147], v[168:171], v[78:81], v[24:27]
	v_mfma_f32_16x16x32_bf16 v[148:151], v[160:163], v[120:123], v[4:7]
	v_mfma_f32_16x16x32_bf16 v[152:155], v[168:171], v[120:123], v[0:3]
	s_setprio 0
	s_barrier
	s_nop 1
	ds_read_b128 v[0:3], v134
	ds_read_b128 v[4:7], v134 offset:1024
	ds_read_b128 v[156:159], v134 offset:2048
	ds_read_b128 v[160:163], v134 offset:3072
	ds_read_b128 v[164:167], v135
	ds_read_b128 v[168:171], v135 offset:1024
	ds_read_b128 v[222:225], v135 offset:2048
	ds_read_b128 v[132:135], v135 offset:3072
	ds_read_b128 v[24:27], v143 offset:32768
	ds_read_b128 v[28:31], v143 offset:33792
	ds_read_b128 v[40:43], v143 offset:34816
	ds_read_b128 v[44:47], v143 offset:35840
	ds_read_b128 v[56:59], v143 offset:36864
	ds_read_b128 v[60:63], v143 offset:37888
	ds_read_b128 v[226:229], v143 offset:38912
	ds_read_b128 v[230:233], v143 offset:39936
	s_add_u32 s22, s24, 0x40000
	s_addc_u32 s23, s25, 0
	s_mov_b64 exec, s[100:101]
	s_mov_b32 m0, s46
	s_nop 0
	global_load_lds_dwordx4 v65, s[22:23]
	s_mov_b64 exec, -1
	s_nop 0
	s_mov_b64 exec, s[100:101]
	s_mov_b32 m0, s47
	s_nop 0
	global_load_lds_dwordx4 v140, s[22:23]
	s_mov_b64 exec, -1
	s_waitcnt vmcnt(8)
	s_waitcnt lgkmcnt(0)
	s_barrier
	s_setprio 1
	s_waitcnt lgkmcnt(0)
	v_mfma_f32_16x16x32_bf16 v[74:77], v[0:3], v[24:27], v[128:131]
	s_waitcnt lgkmcnt(6)
	v_mfma_f32_16x16x32_bf16 v[116:119], v[4:7], v[28:31], v[74:77]
	v_mfma_f32_16x16x32_bf16 v[74:77], v[156:159], v[24:27], v[124:127]
	v_mfma_f32_16x16x32_bf16 v[120:123], v[160:163], v[28:31], v[74:77]
	s_waitcnt lgkmcnt(5)
	v_mfma_f32_16x16x32_bf16 v[74:77], v[0:3], v[40:43], v[206:209]
	s_waitcnt lgkmcnt(4)
	v_mfma_f32_16x16x32_bf16 v[98:101], v[4:7], v[44:47], v[74:77]
	v_mfma_f32_16x16x32_bf16 v[74:77], v[156:159], v[40:43], v[210:213]
	v_mfma_f32_16x16x32_bf16 v[102:105], v[160:163], v[44:47], v[74:77]
	s_waitcnt lgkmcnt(3)
	v_mfma_f32_16x16x32_bf16 v[74:77], v[0:3], v[56:59], v[110:113]
	s_waitcnt lgkmcnt(2)
	v_mfma_f32_16x16x32_bf16 v[82:85], v[4:7], v[60:63], v[74:77]
	v_mfma_f32_16x16x32_bf16 v[74:77], v[156:159], v[56:59], v[106:109]
	v_mfma_f32_16x16x32_bf16 v[86:89], v[160:163], v[60:63], v[74:77]
	s_waitcnt lgkmcnt(1)
	v_mfma_f32_16x16x32_bf16 v[74:77], v[0:3], v[226:229], v[214:217]
	s_waitcnt lgkmcnt(0)
	v_mfma_f32_16x16x32_bf16 v[78:81], v[4:7], v[230:233], v[74:77]
	v_mfma_f32_16x16x32_bf16 v[74:77], v[156:159], v[226:229], v[218:221]
	v_mfma_f32_16x16x32_bf16 v[74:77], v[160:163], v[230:233], v[74:77]
	s_setprio 0
	s_setprio 1
	v_mfma_f32_16x16x32_bf16 v[94:97], v[164:167], v[24:27], v[94:97]
	v_mfma_f32_16x16x32_bf16 v[24:27], v[222:225], v[24:27], v[90:93]
	v_mfma_f32_16x16x32_bf16 v[128:131], v[132:135], v[28:31], v[24:27]
	v_mfma_f32_16x16x32_bf16 v[24:27], v[164:167], v[40:43], v[172:175]
	v_mfma_f32_16x16x32_bf16 v[106:109], v[168:171], v[44:47], v[24:27]
	v_mfma_f32_16x16x32_bf16 v[24:27], v[222:225], v[40:43], v[176:179]
	v_mfma_f32_16x16x32_bf16 v[110:113], v[132:135], v[44:47], v[24:27]
	v_mfma_f32_16x16x32_bf16 v[24:27], v[164:167], v[56:59], v[180:183]
	v_mfma_f32_16x16x32_bf16 v[90:93], v[168:171], v[60:63], v[24:27]
	v_mfma_f32_16x16x32_bf16 v[24:27], v[222:225], v[56:59], v[184:187]
	v_mfma_f32_16x16x32_bf16 v[124:127], v[168:171], v[28:31], v[94:97]
	v_mfma_f32_16x16x32_bf16 v[94:97], v[132:135], v[60:63], v[24:27]
	v_mfma_f32_16x16x32_bf16 v[24:27], v[164:167], v[226:229], v[70:73]
	v_mfma_f32_16x16x32_bf16 v[60:63], v[168:171], v[230:233], v[24:27]
	v_mfma_f32_16x16x32_bf16 v[24:27], v[222:225], v[226:229], v[66:69]
	v_mfma_f32_16x16x32_bf16 v[56:59], v[132:135], v[230:233], v[24:27]
	s_setprio 0
	s_barrier
	ds_read_b128 v[172:175], v143 offset:49152
	ds_read_b128 v[176:179], v143 offset:50176
	ds_read_b128 v[180:183], v143 offset:51200
	ds_read_b128 v[184:187], v143 offset:52224
	ds_read_b128 v[206:209], v143 offset:53248
	ds_read_b128 v[210:213], v143 offset:54272
	ds_read_b128 v[214:217], v143 offset:55296
	ds_read_b128 v[218:221], v143 offset:56320
	s_add_u32 s22, s16, 0x80
	s_addc_u32 s23, s17, 0
	s_mov_b64 exec, s[100:101]
	s_mov_b32 m0, s51
	s_nop 0
	global_load_lds_dwordx4 v114, s[22:23]
	s_mov_b64 exec, -1
	s_nop 0
	s_mov_b64 exec, s[100:101]
	s_mov_b32 m0, s52
	s_nop 0
	global_load_lds_dwordx4 v141, s[22:23]
	s_mov_b64 exec, -1
	s_add_u32 s22, s16, 0x40080
	s_addc_u32 s23, s17, 0
	s_mov_b64 exec, s[100:101]
	s_mov_b32 m0, s55
	s_nop 0
	global_load_lds_dwordx4 v114, s[22:23]
	s_mov_b64 exec, -1
	s_nop 0
	s_mov_b64 exec, s[100:101]
	s_mov_b32 m0, s56
	s_nop 0
	global_load_lds_dwordx4 v141, s[22:23]
	s_mov_b64 exec, -1
	s_nop 0
	s_mov_b64 exec, s[100:101]
	s_mov_b32 m0, s53
	s_nop 0
	global_load_lds_dwordx4 v65, s[4:5]
	s_mov_b64 exec, -1
	s_nop 0
	s_mov_b64 exec, s[100:101]
	s_mov_b32 m0, s54
	s_nop 0
	global_load_lds_dwordx4 v140, s[4:5]
	s_mov_b64 exec, -1
	s_waitcnt vmcnt(8)
	s_waitcnt lgkmcnt(0)
	s_barrier
	s_setprio 1
	s_waitcnt lgkmcnt(0)
	v_mfma_f32_16x16x32_bf16 v[24:27], v[0:3], v[172:175], v[188:191]
	s_waitcnt lgkmcnt(6)
	v_mfma_f32_16x16x32_bf16 v[66:69], v[4:7], v[176:179], v[24:27]
	v_mfma_f32_16x16x32_bf16 v[24:27], v[156:159], v[172:175], v[194:197]
	v_mfma_f32_16x16x32_bf16 v[70:73], v[160:163], v[176:179], v[24:27]
	s_waitcnt lgkmcnt(5)
	v_mfma_f32_16x16x32_bf16 v[24:27], v[0:3], v[180:183], v[52:55]
	s_waitcnt lgkmcnt(4)
	v_mfma_f32_16x16x32_bf16 v[40:43], v[4:7], v[184:187], v[24:27]
	v_mfma_f32_16x16x32_bf16 v[24:27], v[156:159], v[180:183], v[48:51]
	v_mfma_f32_16x16x32_bf16 v[44:47], v[160:163], v[184:187], v[24:27]
	s_waitcnt lgkmcnt(3)
	v_mfma_f32_16x16x32_bf16 v[24:27], v[0:3], v[206:209], v[198:201]
	s_waitcnt lgkmcnt(1)
	v_mfma_f32_16x16x32_bf16 v[0:3], v[0:3], v[214:217], v[36:39]
	v_mfma_f32_16x16x32_bf16 v[24:27], v[4:7], v[210:213], v[24:27]
	v_mfma_f32_16x16x32_bf16 v[28:31], v[156:159], v[206:209], v[202:205]
	s_waitcnt lgkmcnt(0)
	v_mfma_f32_16x16x32_bf16 v[0:3], v[4:7], v[218:221], v[0:3]
	v_mfma_f32_16x16x32_bf16 v[4:7], v[156:159], v[214:217], v[32:35]
	v_mfma_f32_16x16x32_bf16 v[28:31], v[160:163], v[210:213], v[28:31]
	v_mfma_f32_16x16x32_bf16 v[4:7], v[160:163], v[218:221], v[4:7]
	s_setprio 0
	s_setprio 1
	v_mfma_f32_16x16x32_bf16 v[32:35], v[164:167], v[172:175], v[136:139]
	v_mfma_f32_16x16x32_bf16 v[52:55], v[168:171], v[176:179], v[32:35]
	v_mfma_f32_16x16x32_bf16 v[32:35], v[222:225], v[172:175], v[144:147]
	v_mfma_f32_16x16x32_bf16 v[20:23], v[164:167], v[180:183], v[20:23]
	v_mfma_f32_16x16x32_bf16 v[16:19], v[222:225], v[180:183], v[16:19]
	v_mfma_f32_16x16x32_bf16 v[12:15], v[164:167], v[206:209], v[12:15]
	v_mfma_f32_16x16x32_bf16 v[8:11], v[222:225], v[206:209], v[8:11]
	v_mfma_f32_16x16x32_bf16 v[48:51], v[132:135], v[176:179], v[32:35]
	v_mfma_f32_16x16x32_bf16 v[36:39], v[168:171], v[184:187], v[20:23]
	v_mfma_f32_16x16x32_bf16 v[32:35], v[132:135], v[184:187], v[16:19]
	v_mfma_f32_16x16x32_bf16 v[20:23], v[168:171], v[210:213], v[12:15]
	v_mfma_f32_16x16x32_bf16 v[16:19], v[132:135], v[210:213], v[8:11]
	v_mfma_f32_16x16x32_bf16 v[8:11], v[164:167], v[214:217], v[148:151]
	v_mfma_f32_16x16x32_bf16 v[12:15], v[222:225], v[214:217], v[152:155]
	v_mfma_f32_16x16x32_bf16 v[8:11], v[168:171], v[218:221], v[8:11]
	v_mfma_f32_16x16x32_bf16 v[12:15], v[132:135], v[218:221], v[12:15]
	s_setprio 0
	s_barrier
	s_andn2_b64 vcc, exec, s[10:11]
	s_cbranch_vccnz .LBB0_1509
	s_barrier
